# parallel icache warm-up chains in all 4 kernels (touch points per 64B line), kernels moved to .text
# speedup vs baseline: 1.0423x; 1.0423x over previous
_Z7k_frontPKiS0_PiS1_PjPKfS4_S4_P15HIP_vector_typeIjLj4EES7_PKS5_IfLj4EES7_S7_:
	s_movk_i32 s34, 0x5aa5
	v_lshrrev_b32_e32 v1, 6, v0
	s_nop 0
	v_readfirstlane_b32 s35, v1
	s_mov_b64 exec, 0
	s_cmpk_lt_u32 s35, 8
	s_cbranch_scc1 .Lw0d0_16
	s_cmpk_lt_u32 s35, 12
	s_cbranch_scc1 .Lw0d8_16
	s_cmpk_lt_u32 s35, 14
	s_cbranch_scc1 .Lw0d12_16
	s_cmpk_lt_u32 s35, 15
	s_cbranch_scc1 .Lw0d14_16
	s_branch .Lw0t15
.Lw0d14_16:
	s_branch .Lw0t14
.Lw0d12_16:
	s_cmpk_lt_u32 s35, 13
	s_cbranch_scc1 .Lw0d12_14
	s_branch .Lw0t13

.Lw0d8_16:
	s_cmpk_lt_u32 s35, 10
	s_cbranch_scc1 .Lw0d8_12
	s_cmpk_lt_u32 s35, 11
	s_cbranch_scc1 .Lw0d10_12
	s_branch .Lw0t11

.Lw0d8_12:
	s_cmpk_lt_u32 s35, 9
	s_cbranch_scc1 .Lw0d8_10
	s_branch .Lw0t9

.Lw0d0_16:
	s_cmpk_lt_u32 s35, 4
	s_cbranch_scc1 .Lw0d0_8
	s_cmpk_lt_u32 s35, 6
	s_cbranch_scc1 .Lw0d4_8
	s_cmpk_lt_u32 s35, 7
	s_cbranch_scc1 .Lw0d6_8
	s_branch .Lw0t7

.Lw0d4_8:
	s_cmpk_lt_u32 s35, 5
	s_cbranch_scc1 .Lw0d4_6
	s_branch .Lw0t5

.Lw0d0_8:
	s_cmpk_lt_u32 s35, 2
	s_cbranch_scc1 .Lw0d0_4
	s_cmpk_lt_u32 s35, 3
	s_cbranch_scc1 .Lw0d2_4
	s_branch .Lw0t3

.Lw0d0_4:
	s_cmpk_lt_u32 s35, 1
	s_cbranch_scc1 .Lw0d0_2
	s_branch .Lw0t1

.Lw0end:
	s_mov_b32 s34, 0
	s_mov_b64 exec, -1
	s_cmpk_gt_i32 s2, 0xc3
	s_mov_b64 s[4:5], -1
	s_cbranch_scc0 .LBB0_39
.Lw0t0:
	s_cbranch_execz .Lw0c0
.Lw0b0:
	s_load_dwordx2 s[4:5], s[0:1], 0x58
	s_cmpk_gt_u32 s2, 0xce
	s_mov_b64 s[6:7], -1
	s_cbranch_scc0 .LBB0_5
	s_lshl_b32 s3, s2, 10
	s_add_i32 s3, s3, 0xfffcc400

.Lw0b1:
	v_and_b32_e32 v1, 0x3c0, v0
	v_or_b32_e32 v1, s3, v1
	s_mov_b32 s3, 0x186a00
	v_cmp_gt_u32_e32 vcc, s3, v1
	s_and_saveexec_b64 s[6:7], vcc
	s_cbranch_execz .LBB0_4
	s_load_dwordx2 s[8:9], s[0:1], 0x50
	v_and_b32_e32 v2, 63, v0
	v_mov_b32_e32 v11, 0
	v_lshl_or_b32 v10, v1, 1, v2

.Lw0b2:
	s_waitcnt lgkmcnt(0)
	v_lshl_add_u64 v[12:13], v[10:11], 4, s[8:9]
	global_load_dwordx4 v[2:5], v[12:13], off nt
	global_load_dwordx4 v[6:9], v[12:13], off offset:1024 nt
	v_and_b32_e32 v12, 1, v0
	v_bfe_u32 v10, v0, 1, 5
	v_lshlrev_b32_e32 v13, 5, v12
	v_or3_b32 v10, v13, v10, v1
	v_cmp_eq_u32_e32 vcc, 0, v12
	s_waitcnt vmcnt(1)

.Lw0b3:
	v_cvt_pk_f16_f32 v1, v4, v5
	v_cvt_pk_f16_f32 v2, v2, v3
	s_waitcnt vmcnt(0)
	v_cvt_pk_f16_f32 v5, v8, v9
	v_cvt_pk_f16_f32 v4, v6, v7
	v_cndmask_b32_e32 v3, v2, v4, vcc
	v_cndmask_b32_e32 v6, v1, v5, vcc
	s_nop 0
	v_mov_b32_dpp v7, v3 quad_perm:[1,0,3,2] row_mask:0xf bank_mask:0xf bound_ctrl:1
	v_mov_b32_dpp v6, v6 quad_perm:[1,0,3,2] row_mask:0xf bank_mask:0xf bound_ctrl:1

.Lw0b4:
	v_cndmask_b32_e32 v2, v7, v2, vcc
	v_cndmask_b32_e32 v3, v6, v1, vcc
	v_cndmask_b32_e32 v4, v4, v7, vcc
	v_cndmask_b32_e32 v5, v5, v6, vcc
	v_lshl_add_u64 v[6:7], v[10:11], 4, s[4:5]
	global_store_dwordx4 v[6:7], v[2:5], off sc1

.Lw0b5:
	v_lshl_or_b32 v2, s3, 10, v0
	s_cmp_gt_u32 s3, 7
	s_mov_b64 s[6:7], -1
	s_cbranch_scc0 .LBB0_30
	s_load_dwordx2 s[6:7], s[0:1], 0x48
	s_cmp_gt_u32 s3, 9
	s_mov_b64 s[8:9], -1
	s_cbranch_scc0 .LBB0_27
	s_movk_i32 s8, 0x2900
	v_cmp_gt_u32_e32 vcc, s8, v2
	s_and_saveexec_b64 s[8:9], vcc
	s_cbranch_execz .LBB0_26
	s_load_dwordx2 s[10:11], s[0:1], 0x38

.Lw0b6:
	v_add_u32_e32 v1, 0xffffd800, v2
	v_lshlrev_b32_e32 v4, 1, v0
	v_lshrrev_b32_e32 v1, 3, v1
	v_and_b32_e32 v4, 0x60, v4
	v_and_b32_e32 v1, 0x1ffffff8, v1
	v_and_b32_e32 v3, 15, v0
	v_add_u32_e32 v4, v1, v4
	v_cmp_gt_u32_e32 vcc, 2, v3
	v_mov_b32_e32 v1, 0
	v_lshl_or_b32 v4, v4, 1, v3

.Lw0b7:
	v_mov_b32_e32 v3, 0
	s_and_saveexec_b64 s[12:13], vcc
	s_cbranch_execz .LBB0_11
	v_mov_b32_e32 v5, 0
	s_waitcnt lgkmcnt(0)
	v_lshl_add_u64 v[6:7], v[4:5], 2, s[10:11]
	global_load_dword v3, v[6:7], off
	s_waitcnt vmcnt(0)
	v_cvt_f16_f32_e32 v3, v3

.Lw0b8:
	s_waitcnt lgkmcnt(0)
	v_lshl_add_u64 v[6:7], v[4:5], 2, s[10:11]
	global_load_dword v1, v[6:7], off offset:8
	s_waitcnt vmcnt(0)
	v_cvt_f16_f32_e32 v1, v1

.Lw0b9:
	global_load_dword v5, v[8:9], off offset:16
	s_waitcnt vmcnt(0)
	v_cvt_f16_f32_e32 v7, v5

.Lw0b10:
	v_cvt_f16_f32_e32 v6, v5

.Lw0b11:
	s_and_saveexec_b64 s[12:13], vcc
	s_cbranch_execz .LBB0_21
	v_mov_b32_e32 v5, 0
	s_waitcnt lgkmcnt(0)
	v_lshl_add_u64 v[10:11], v[4:5], 2, s[10:11]
	global_load_dword v5, v[10:11], off offset:40
	s_waitcnt vmcnt(0)
	v_cvt_f16_f32_e32 v8, v5

.Lw0b12:
	v_mov_b32_e32 v5, 0
	s_waitcnt lgkmcnt(0)
	v_lshl_add_u64 v[12:13], v[4:5], 2, s[10:11]
	global_load_dword v5, v[12:13], off offset:48
	s_waitcnt vmcnt(0)
	v_cvt_f16_f32_e32 v11, v5

.Lw0b13:
	global_load_dword v4, v[4:5], off offset:56
	s_waitcnt vmcnt(0)
	v_cvt_f16_f32_e32 v10, v4

.Lw0b14:
	v_lshl_add_u64 v[4:5], v[2:3], 4, s[6:7]
	v_add_co_u32_e32 v4, vcc, 0xfffe0000, v4
	v_perm_b32 v9, v6, v7, s10
	s_nop 0
	v_addc_co_u32_e32 v5, vcc, -1, v5, vcc
	global_store_dwordx4 v[4:5], v[8:11], off

.Lw0b15:
	v_lshlrev_b32_e32 v1, 3, v0
	v_lshrrev_b32_e32 v3, 4, v0
	v_add_u32_e32 v8, 0xffffe000, v2
	v_and_b32_e32 v1, 0x60, v1
	v_and_b32_e32 v3, 28, v3
	v_and_b32_e32 v4, 3, v0
	v_or3_b32 v1, v3, v4, v1
	v_lshlrev_b32_e32 v3, 1, v0
	v_lshrrev_b32_e32 v4, 6, v8
	v_and_b32_e32 v3, 0x60, v3

.Lw0b16:
	v_and_b32_e32 v4, 0x3fffff8, v4
	v_add_u32_e32 v4, v4, v3
	v_lshlrev_b32_e32 v6, 2, v1
	v_mov_b32_e32 v7, 0
	s_waitcnt lgkmcnt(0)
	v_lshl_add_u64 v[10:11], s[8:9], 0, v[6:7]
	v_or_b32_e32 v6, 1, v4
	v_lshlrev_b64 v[14:15], 9, v[6:7]
	v_or_b32_e32 v6, 2, v4
	v_lshlrev_b64 v[16:17], 9, v[6:7]
	v_or_b32_e32 v6, 3, v4

.Lw0b17:
	v_lshlrev_b64 v[18:19], 9, v[6:7]
	v_or_b32_e32 v6, 4, v4
	v_lshlrev_b64 v[20:21], 9, v[6:7]
	v_or_b32_e32 v6, 5, v4
	v_mov_b32_e32 v5, v7
	v_lshlrev_b64 v[22:23], 9, v[6:7]
	v_or_b32_e32 v6, 6, v4
	v_lshlrev_b64 v[12:13], 9, v[4:5]
	v_lshlrev_b64 v[24:25], 9, v[6:7]
	v_or_b32_e32 v6, 7, v4

.Lw0b18:
	v_lshl_add_u64 v[12:13], v[10:11], 0, v[12:13]
	v_lshlrev_b64 v[4:5], 9, v[6:7]
	v_lshl_add_u64 v[14:15], v[10:11], 0, v[14:15]
	v_lshl_add_u64 v[16:17], v[10:11], 0, v[16:17]
	v_lshl_add_u64 v[18:19], v[10:11], 0, v[18:19]
	v_lshl_add_u64 v[20:21], v[10:11], 0, v[20:21]
	v_lshl_add_u64 v[22:23], v[10:11], 0, v[22:23]
	v_lshl_add_u64 v[24:25], v[10:11], 0, v[24:25]

.Lw0b19:
	v_lshl_add_u64 v[4:5], v[10:11], 0, v[4:5]
	global_load_dword v1, v[12:13], off
	global_load_dword v3, v[14:15], off
	global_load_dword v6, v[16:17], off
	global_load_dword v10, v[18:19], off
	global_load_dword v11, v[20:21], off
	global_load_dword v26, v[22:23], off

.Lw0b20:
	global_load_dword v27, v[24:25], off
	global_load_dword v28, v[4:5], off
	v_mov_b32_e32 v9, v7
	v_lshl_add_u64 v[8:9], v[8:9], 4, s[6:7]
	s_waitcnt vmcnt(6)
	v_cvt_pk_f16_f32 v4, v1, v3
	s_waitcnt vmcnt(4)
	v_cvt_pk_f16_f32 v5, v6, v10
	s_waitcnt vmcnt(2)
	v_cvt_pk_f16_f32 v6, v11, v26

.Lw0b21:
	s_waitcnt vmcnt(0)
	v_cvt_pk_f16_f32 v7, v27, v28
	global_store_dwordx4 v[8:9], v[4:7], off

.Lw0b22:
	v_and_b32_e32 v4, 28, v3
	v_and_b32_e32 v5, 3, v0
	v_lshrrev_b32_e32 v6, 1, v0
	v_and_b32_e32 v6, 24, v6
	s_movk_i32 s8, 0x1e0
	v_or3_b32 v1, v1, v5, v4
	v_and_or_b32 v3, v3, s8, v6
	v_lshlrev_b32_e32 v1, 2, v1
	v_lshl_or_b32 v1, v3, 9, v1
	s_waitcnt lgkmcnt(0)
	global_load_dword v4, v1, s[6:7] offset:1024

.Lw0b23:
	global_load_dword v5, v1, s[6:7] offset:1536
	global_load_dword v6, v1, s[6:7] offset:2048
	global_load_dword v7, v1, s[6:7] offset:3072
	global_load_dword v8, v1, s[6:7] offset:3584
	global_load_dword v9, v1, s[6:7] offset:2560
	global_load_dword v10, v1, s[6:7]
	global_load_dword v11, v1, s[6:7] offset:512

.Lw0b24:
	s_load_dwordx2 s[6:7], s[0:1], 0x40
	v_mov_b32_e32 v3, 0
	s_waitcnt lgkmcnt(0)
	v_lshl_add_u64 v[2:3], v[2:3], 4, s[6:7]
	s_waitcnt vmcnt(6)
	v_cvt_pk_f16_f32 v5, v4, v5
	s_waitcnt vmcnt(3)
	v_cvt_pk_f16_f32 v7, v7, v8
	s_waitcnt vmcnt(2)
	v_cvt_pk_f16_f32 v6, v6, v9

.Lw0b25:
	s_waitcnt vmcnt(0)
	v_cvt_pk_f16_f32 v4, v10, v11
	global_store_dwordx4 v[2:3], v[4:7], off

.Lw0b26:
	s_xor_b64 s[8:9], exec, s[8:9]
	s_cbranch_execz .LBB0_35
	s_load_dwordx2 s[10:11], s[0:1], 0x60
	s_waitcnt lgkmcnt(0)
	v_lshl_add_u64 v[4:5], s[10:11], 0, v[2:3]
	v_add_co_u32_e32 v6, vcc, 0x1869000, v4
	v_mov_b32_e32 v2, v3
	s_nop 0
	v_addc_co_u32_e32 v7, vcc, 0, v5, vcc
	v_mov_b32_e32 v4, v3
	v_mov_b32_e32 v5, v3
	global_store_dwordx4 v[6:7], v[2:5], off offset:3840
.LBB0_35:
.Lw0t27:
	s_cbranch_execz .Lw0c27

.Lw0b29:
	s_sub_i32 s25, s2, s3
	s_addk_i32 s2, 0x61
	s_cmpk_lt_u32 s2, 0xc3
	s_waitcnt lgkmcnt(0)
	s_cselect_b32 s16, s4, s6
	s_cselect_b32 s17, s5, s7
	s_add_u32 s18, s16, 0x30d400
	s_addc_u32 s19, s17, 0
	s_lshl_b32 s20, s25, 13
	s_min_i32 s24, s20, 0xc1500
	s_addk_i32 s24, 0x2000
	v_or_b32_e32 v2, s20, v0
	v_cmp_gt_i32_e32 vcc, s24, v2

.Lw0b30:
	v_mov_b32_e32 v1, -1
	v_ashrrev_i32_e32 v3, 31, v2
	v_mov_b32_e32 v21, -1
	s_and_saveexec_b64 s[2:3], vcc
	s_cbranch_execz .LBB0_42
	v_lshl_add_u64 v[4:5], v[2:3], 2, s[18:19]
	global_load_dword v21, v[4:5], off nt

.Lw0b31:
	s_and_saveexec_b64 s[4:5], s[2:3]
	s_cbranch_execz .LBB0_44
	v_lshl_add_u64 v[6:7], v[4:5], 2, s[18:19]
	global_load_dword v1, v[6:7], off nt

.Lw0b32:
	s_cbranch_execz .LBB0_46
	v_lshl_add_u64 v[8:9], v[6:7], 2, s[18:19]
	global_load_dword v22, v[8:9], off nt

.Lw0b33:
	global_load_dword v18, v[10:11], off nt

.Lw0b35:
	v_cmp_gt_i32_e64 s[12:13], s24, v14
	v_mov_b32_e32 v20, -1
	v_ashrrev_i32_e32 v15, 31, v14
	v_mov_b32_e32 v24, -1
	s_and_saveexec_b64 s[14:15], s[12:13]
	s_cbranch_execz .LBB0_54
	v_lshl_add_u64 v[16:17], v[14:15], 2, s[18:19]
	global_load_dword v24, v[16:17], off nt

.Lw0b36:
	v_cmp_gt_i32_e64 s[14:15], s24, v16
	v_ashrrev_i32_e32 v17, 31, v16
	s_and_saveexec_b64 s[22:23], s[14:15]
	s_cbranch_execz .LBB0_56
	v_lshl_add_u64 v[26:27], v[16:17], 2, s[18:19]
	global_load_dword v20, v[26:27], off nt

.Lw0b37:
	global_load_dword v27, v[2:3], off nt

.Lw0b38:
	v_lshl_add_u64 v[2:3], v[6:7], 2, s[16:17]
	global_load_dword v26, v[2:3], off nt

.Lw0b39:
	s_cbranch_execz .LBB0_66
	v_lshl_add_u64 v[2:3], v[10:11], 2, s[16:17]
	global_load_dword v7, v[2:3], off nt

.Lw0b40:
	s_and_saveexec_b64 s[2:3], s[12:13]
	s_cbranch_execz .LBB0_70
	v_lshl_add_u64 v[8:9], v[14:15], 2, s[16:17]
	global_load_dword v6, v[8:9], off nt

.Lw0b41:
	v_cmp_gt_u32_e64 s[16:17], s2, v0
	v_lshlrev_b32_e32 v2, 2, v0
	s_and_saveexec_b64 s[2:3], s[16:17]
	v_mov_b32_e32 v8, 0
	ds_write_b32 v2, v8 offset:33552
	s_or_b64 exec, exec, s[2:3]
	s_waitcnt lgkmcnt(0)
	s_waitcnt vmcnt(0)
	v_cmp_lt_i32_e32 vcc, -1, v21
	v_mov_b32_e32 v8, 0
	v_lshrrev_b32_e32 v14, 7, v21
	v_mov_b32_e32 v12, 0
	s_barrier

.Lw0b42:
	s_and_saveexec_b64 s[2:3], vcc
	v_and_b32_e32 v9, 0x1fffffc, v14
	v_mov_b32_e32 v10, 1
	ds_add_rtn_u32 v12, v9, v10 offset:33552
	s_or_b64 exec, exec, s[2:3]
	v_cmp_lt_i32_e64 s[2:3], -1, v1
	v_lshrrev_b32_e32 v13, 7, v1
	s_and_saveexec_b64 s[4:5], s[2:3]
	v_and_b32_e32 v8, 0x1fffffc, v13
	v_mov_b32_e32 v9, 1
	ds_add_rtn_u32 v8, v8, v9 offset:33552

.Lw0b43:
	s_or_b64 exec, exec, s[4:5]
	v_cmp_lt_i32_e64 s[4:5], -1, v22
	v_mov_b32_e32 v9, 0
	v_lshrrev_b32_e32 v17, 7, v22
	v_mov_b32_e32 v15, 0
	s_and_saveexec_b64 s[6:7], s[4:5]
	v_and_b32_e32 v10, 0x1fffffc, v17
	v_mov_b32_e32 v11, 1
	ds_add_rtn_u32 v15, v10, v11 offset:33552
	s_or_b64 exec, exec, s[6:7]
	v_cmp_lt_i32_e64 s[6:7], -1, v18

.Lw0b44:
	v_lshrrev_b32_e32 v16, 7, v18
	s_and_saveexec_b64 s[8:9], s[6:7]
	v_and_b32_e32 v9, 0x1fffffc, v16
	v_mov_b32_e32 v10, 1
	ds_add_rtn_u32 v9, v9, v10 offset:33552
	s_or_b64 exec, exec, s[8:9]
	v_cmp_lt_i32_e64 s[8:9], -1, v23
	v_mov_b32_e32 v10, 0
	v_lshrrev_b32_e32 v33, 7, v23
	v_mov_b32_e32 v28, 0
	s_and_saveexec_b64 s[10:11], s[8:9]

.Lw0b45:
	v_and_b32_e32 v11, 0x1fffffc, v33
	v_mov_b32_e32 v28, 1
	ds_add_rtn_u32 v28, v11, v28 offset:33552
	s_or_b64 exec, exec, s[10:11]
	v_cmp_lt_i32_e64 s[12:13], -1, v19
	v_lshrrev_b32_e32 v32, 7, v19
	s_and_saveexec_b64 s[10:11], s[12:13]
	v_and_b32_e32 v10, 0x1fffffc, v32
	v_mov_b32_e32 v11, 1
	ds_add_rtn_u32 v10, v10, v11 offset:33552

.Lw0b46:
	s_or_b64 exec, exec, s[10:11]
	v_cmp_lt_i32_e64 s[10:11], -1, v24
	v_mov_b32_e32 v11, 0
	v_lshrrev_b32_e32 v31, 7, v24
	v_mov_b32_e32 v29, 0
	s_and_saveexec_b64 s[14:15], s[10:11]
	v_and_b32_e32 v29, 0x1fffffc, v31
	v_mov_b32_e32 v30, 1
	ds_add_rtn_u32 v29, v29, v30 offset:33552
	s_or_b64 exec, exec, s[14:15]
	v_cmp_lt_i32_e64 s[14:15], -1, v20

.Lw0b47:
	v_lshrrev_b32_e32 v30, 7, v20
	s_and_saveexec_b64 s[18:19], s[14:15]
	v_and_b32_e32 v11, 0x1fffffc, v30
	v_mov_b32_e32 v34, 1
	ds_add_rtn_u32 v11, v11, v34 offset:33552
	s_or_b64 exec, exec, s[18:19]
	v_mov_b32_e32 v34, 0
	s_waitcnt lgkmcnt(0)
	s_barrier
	s_and_saveexec_b64 s[18:19], s[16:17]
	ds_read_b32 v34, v2 offset:33552
	s_or_b64 exec, exec, s[18:19]

.Lw0b48:
	s_waitcnt lgkmcnt(0)
	v_add_u32_dpp v35, v34, v34 row_shr:1 row_mask:0xf bank_mask:0xf bound_ctrl:1
	v_and_b32_e32 v36, 63, v0
	v_cmp_eq_u32_e64 s[18:19], 63, v36
	v_add_u32_dpp v35, v35, v35 row_shr:2 row_mask:0xf bank_mask:0xf bound_ctrl:1
	s_nop 1
	v_add_u32_dpp v35, v35, v35 row_shr:4 row_mask:0xf bank_mask:0xf bound_ctrl:1
	s_nop 1
	v_add_u32_dpp v35, v35, v35 row_shr:8 row_mask:0xf bank_mask:0xf bound_ctrl:1
	s_nop 1

.Lw0b49:
	v_add_u32_dpp v35, v35, v35 row_bcast:15 row_mask:0xa bank_mask:0xf
	s_nop 1
	v_add_u32_dpp v35, v35, v35 row_bcast:31 row_mask:0xc bank_mask:0xf
	s_and_saveexec_b64 s[22:23], s[18:19]
	v_lshrrev_b32_e32 v36, 4, v0
	v_and_b32_e32 v36, 60, v36
	ds_write_b32 v36, v35 offset:34336
	s_or_b64 exec, exec, s[22:23]
	s_waitcnt lgkmcnt(0)
	s_barrier
	s_and_saveexec_b64 s[18:19], s[16:17]
	s_cbranch_execz .LBB0_96

.Lw0b50:
	v_mov_b32_e32 v36, 0
	ds_read_b96 v[36:38], v36 offset:34336
	s_movk_i32 s16, 0xbf
	s_movk_i32 s22, 0x7f
	v_cmp_lt_u32_e64 s[16:17], s16, v0
	v_sub_u32_e32 v35, v35, v34
	s_load_dwordx4 s[28:31], s[0:1], 0x10
	s_waitcnt lgkmcnt(0)
	v_cndmask_b32_e64 v38, 0, v38, s[16:17]
	v_cmp_lt_u32_e64 s[16:17], s22, v0

.Lw0b51:
	s_nop 1
	v_cndmask_b32_e64 v37, 0, v37, s[16:17]
	v_cmp_lt_u32_e64 s[16:17], 63, v0
	s_nop 1
	v_cndmask_b32_e64 v36, 0, v36, s[16:17]
	v_add_u32_e32 v36, v37, v36
	s_mul_i32 s16, s21, 0xc4
	v_add3_u32 v40, v38, v36, v35
	v_add_u32_e32 v35, s16, v0
	s_movk_i32 s16, 0x62

.Lw0b52:
	v_mul_lo_u32 v35, v35, s16
	v_add_u32_e32 v36, s25, v35
	v_ashrrev_i32_e32 v37, 31, v36
	v_lshlrev_b64 v[36:37], 2, v[36:37]
	v_lshl_add_u64 v[38:39], s[28:29], 0, v[36:37]
	global_store_dword v[38:39], v34, off
	v_lshl_add_u64 v[34:35], s[30:31], 0, v[36:37]
	ds_write_b32 v2, v40 offset:32768
	global_store_dword v[34:35], v40, off

.Lw0b55:
	ds_read_b32 v1, v1 offset:32768
	v_lshlrev_b32_e32 v4, 17, v20
	s_mov_b32 s4, 0x3fe0000
	v_and_or_b32 v3, v4, s4, v3
	v_lshlrev_b32_e32 v4, 2, v11
	s_waitcnt lgkmcnt(0)
	v_lshl_add_u32 v1, v1, 2, v4
	ds_write_b32 v1, v3

.Lw0b56:
	s_mul_hi_i32 s2, s21, 0x30d400
	s_mul_i32 s21, s21, 0x30d400
	s_waitcnt lgkmcnt(0)
	s_add_u32 s3, s0, s21
	s_addc_u32 s2, s1, s2
	s_ashr_i32 s21, s20, 31
	s_lshl_b64 s[0:1], s[20:21], 2
	s_add_u32 s0, s3, s0
	s_addc_u32 s1, s2, s1
	s_sub_i32 s4, s24, s20
	v_cmp_gt_i32_e32 vcc, s4, v0
	s_barrier
	s_and_saveexec_b64 s[2:3], vcc

.Lw0b57:
	s_cbranch_execz .LBB0_107
	ds_read_b32 v1, v2
	s_waitcnt lgkmcnt(0)
	global_store_dword v2, v1, s[0:1]

.Lw0b58:
	s_waitcnt lgkmcnt(0)
	global_store_dword v1, v3, s[0:1]

.Lw0b60:
	v_cmp_gt_i32_e32 vcc, s4, v1
	s_and_saveexec_b64 s[2:3], vcc
	s_cbranch_execz .LBB0_115
	ds_read_b32 v3, v2 offset:16384
	v_lshlrev_b32_e32 v1, 2, v1
	s_waitcnt lgkmcnt(0)
	global_store_dword v1, v3, s[0:1]

.Lw0b61:
	ds_read_b32 v3, v2 offset:20480
	v_lshlrev_b32_e32 v1, 2, v1
	s_waitcnt lgkmcnt(0)
	global_store_dword v1, v3, s[0:1]

.Lw0b64:
	s_or_b64 exec, exec, s[16:17]
	s_and_saveexec_b64 s[16:17], s[2:3]
	s_cbranch_execz .LBB0_98

.Lw0b65:
	v_lshl_add_u32 v8, v12, 2, v8
	ds_write_b32 v8, v1
	s_or_b64 exec, exec, s[16:17]
	s_and_saveexec_b64 s[2:3], s[4:5]
	s_cbranch_execz .LBB0_99

.Lw0b66:
	v_and_or_b32 v8, v8, s4, v26
	s_waitcnt lgkmcnt(0)
	v_lshl_add_u32 v1, v1, 2, v12
	ds_write_b32 v1, v8
	s_or_b64 exec, exec, s[2:3]
	s_and_saveexec_b64 s[2:3], s[6:7]
	s_cbranch_execz .LBB0_100

.Lw0b67:
	s_mov_b32 s4, 0x3fe0000
	v_and_or_b32 v5, v8, s4, v5
	v_lshlrev_b32_e32 v8, 2, v9
	s_waitcnt lgkmcnt(0)
	v_lshl_add_u32 v1, v1, 2, v8
	ds_write_b32 v1, v5
	s_or_b64 exec, exec, s[2:3]
	s_and_saveexec_b64 s[2:3], s[8:9]
	s_cbranch_execz .LBB0_101

.Lw0b68:
	ds_read_b32 v1, v1 offset:32768
	v_lshlrev_b32_e32 v5, 17, v23
	s_mov_b32 s4, 0x3fe0000
	v_and_or_b32 v5, v5, s4, v7
	v_lshlrev_b32_e32 v7, 2, v28
	s_waitcnt lgkmcnt(0)
	v_lshl_add_u32 v1, v1, 2, v7
	ds_write_b32 v1, v5
	s_or_b64 exec, exec, s[2:3]
	s_and_saveexec_b64 s[2:3], s[12:13]

.Lw0b70:
	s_or_b64 exec, exec, s[2:3]
	s_load_dwordx2 s[0:1], s[0:1], 0x20
	s_and_saveexec_b64 s[2:3], s[10:11]
	s_cbranch_execz .LBB0_103

.Lw0b71:
	s_waitcnt lgkmcnt(0)
	v_lshl_add_u32 v1, v1, 2, v5
	ds_write_b32 v1, v4
	s_or_b64 exec, exec, s[2:3]
	s_and_saveexec_b64 s[2:3], s[14:15]
	s_cbranch_execnz .LBB0_104
	s_branch .LBB0_105
.Lw0c0:
	s_cmpk_eq_u32 s34, 0x5aa5
	s_cbranch_scc1 .Lw0t16
	s_branch .Lw0b0

	.amdhsa_kernel _Z7k_frontPKiS0_PiS1_PjPKfS4_S4_P15HIP_vector_typeIjLj4EES7_PKS5_IfLj4EES7_S7_
		.amdhsa_group_segment_fixed_size 34400
		.amdhsa_private_segment_fixed_size 0
		.amdhsa_kernarg_size 104
		.amdhsa_user_sgpr_count 2
		.amdhsa_user_sgpr_dispatch_ptr 0
		.amdhsa_user_sgpr_queue_ptr 0
		.amdhsa_user_sgpr_kernarg_segment_ptr 1
		.amdhsa_user_sgpr_dispatch_id 0
		.amdhsa_user_sgpr_kernarg_preload_length 0
		.amdhsa_user_sgpr_kernarg_preload_offset 0
		.amdhsa_user_sgpr_private_segment_size 0
		.amdhsa_uses_dynamic_stack 0
		.amdhsa_enable_private_segment 0
		.amdhsa_system_sgpr_workgroup_id_x 1
		.amdhsa_system_sgpr_workgroup_id_y 0
		.amdhsa_system_sgpr_workgroup_id_z 0
		.amdhsa_system_sgpr_workgroup_info 0
		.amdhsa_system_vgpr_workitem_id 0
		.amdhsa_next_free_vgpr 41
		.amdhsa_next_free_sgpr 36
		.amdhsa_accum_offset 44
		.amdhsa_reserve_vcc 1
		.amdhsa_float_round_mode_32 0
		.amdhsa_float_round_mode_16_64 0
		.amdhsa_float_denorm_mode_32 3
		.amdhsa_float_denorm_mode_16_64 3
		.amdhsa_dx10_clamp 1
		.amdhsa_ieee_mode 1
		.amdhsa_fp16_overflow 0
		.amdhsa_tg_split 0
		.amdhsa_exception_fp_ieee_invalid_op 0
		.amdhsa_exception_fp_denorm_src 0
		.amdhsa_exception_fp_ieee_div_zero 0
		.amdhsa_exception_fp_ieee_overflow 0
		.amdhsa_exception_fp_ieee_underflow 0
		.amdhsa_exception_fp_ieee_inexact 0
		.amdhsa_exception_int_div_zero 0
	.end_amdhsa_kernel

_Z8k_bucketPKiS0_PKjPiS3_PK15HIP_vector_typeIfLj4EEPS4_IjLj4EE:
	s_movk_i32 s64, 0x5aa5
	v_lshrrev_b32_e32 v1, 6, v0
	s_nop 0
	v_readfirstlane_b32 s65, v1
	s_mov_b64 exec, 0
	s_cmpk_lt_u32 s65, 8
	s_cbranch_scc1 .Lw1d0_16
	s_cmpk_lt_u32 s65, 12
	s_cbranch_scc1 .Lw1d8_16
	s_cmpk_lt_u32 s65, 14
	s_cbranch_scc1 .Lw1d12_16
	s_cmpk_lt_u32 s65, 15
	s_cbranch_scc1 .Lw1d14_16
	s_branch .Lw1t15

.Lw1d12_16:
	s_cmpk_lt_u32 s65, 13
	s_cbranch_scc1 .Lw1d12_14
	s_branch .Lw1t13

.Lw1d8_16:
	s_cmpk_lt_u32 s65, 10
	s_cbranch_scc1 .Lw1d8_12
	s_cmpk_lt_u32 s65, 11
	s_cbranch_scc1 .Lw1d10_12
	s_branch .Lw1t11

.Lw1d8_12:
	s_cmpk_lt_u32 s65, 9
	s_cbranch_scc1 .Lw1d8_10
	s_branch .Lw1t9

.Lw1d0_16:
	s_cmpk_lt_u32 s65, 4
	s_cbranch_scc1 .Lw1d0_8
	s_cmpk_lt_u32 s65, 6
	s_cbranch_scc1 .Lw1d4_8
	s_cmpk_lt_u32 s65, 7
	s_cbranch_scc1 .Lw1d6_8
	s_branch .Lw1t7

.Lw1d4_8:
	s_cmpk_lt_u32 s65, 5
	s_cbranch_scc1 .Lw1d4_6
	s_branch .Lw1t5

.Lw1d0_8:
	s_cmpk_lt_u32 s65, 2
	s_cbranch_scc1 .Lw1d0_4
	s_cmpk_lt_u32 s65, 3
	s_cbranch_scc1 .Lw1d2_4
	s_branch .Lw1t3

.Lw1d0_4:
	s_cmpk_lt_u32 s65, 1
	s_cbranch_scc1 .Lw1d0_2
	s_branch .Lw1t1

.Lw1end:
	s_mov_b32 s64, 0
	s_mov_b64 exec, -1
	s_cmpk_lt_u32 s2, 0x188
	s_mov_b64 s[4:5], -1
	s_cbranch_scc0 .LBB1_391

.Lw1b0:
	v_mov_b32_e32 v1, 0xc4
	v_sub_co_u32_e32 v1, vcc, s2, v1
	s_and_b64 s[4:5], vcc, exec
	v_readfirstlane_b32 s3, v1
	s_cselect_b32 s33, s2, s3
	s_cmpk_gt_u32 s2, 0xc3
	s_cselect_b64 s[30:31], -1, 0

.Lw1b1:
	s_and_b64 s[4:5], s[30:31], exec
	s_cselect_b32 s3, 0xc4, 0
	s_add_i32 s3, s3, s33
	s_movk_i32 s6, 0x62
	s_mul_hi_u32 s5, s3, 0x62
	s_mul_i32 s4, s3, 0x62
	v_cmp_gt_u32_e32 vcc, s6, v0
	v_mov_b32_e32 v1, 0
	v_mov_b32_e32 v2, 0
	s_and_saveexec_b64 s[6:7], vcc
	s_cbranch_execz .LBB1_3

.Lw1b2:
	s_load_dwordx2 s[8:9], s[0:1], 0x0
	s_lshl_b64 s[10:11], s[4:5], 2
	v_lshlrev_b32_e32 v2, 2, v0
	s_waitcnt lgkmcnt(0)
	s_add_u32 s8, s8, s10
	s_addc_u32 s9, s9, s11
	global_load_dword v2, v2, s[8:9]

.Lw1b3:
	s_lshl_b64 s[4:5], s[4:5], 2
	v_lshlrev_b32_e32 v4, 2, v0
	s_waitcnt lgkmcnt(0)
	s_add_u32 s4, s8, s4
	s_addc_u32 s5, s9, s5
	global_load_dword v3, v4, s[4:5]
	v_add_u32_e32 v4, 0x11990, v4
	s_waitcnt vmcnt(0)
	ds_write_b32 v4, v3

.Lw1b4:
	v_and_b32_e32 v5, 63, v0
	v_cmp_eq_u32_e64 s[4:5], 63, v5
	v_add_u32_dpp v3, v3, v3 row_shr:2 row_mask:0xf bank_mask:0xf bound_ctrl:1
	s_nop 1
	v_add_u32_dpp v3, v3, v3 row_shr:4 row_mask:0xf bank_mask:0xf bound_ctrl:1
	s_nop 1
	v_add_u32_dpp v4, v3, v3 row_shr:8 row_mask:0xf bank_mask:0xf bound_ctrl:1
	s_waitcnt vmcnt(0)
	v_add_u32_dpp v3, v2, v2 row_shr:1 row_mask:0xf bank_mask:0xf bound_ctrl:1
	v_add_u32_dpp v4, v4, v4 row_bcast:15 row_mask:0xa bank_mask:0xf

.Lw1b5:
	s_nop 0
	v_add_u32_dpp v3, v3, v3 row_shr:2 row_mask:0xf bank_mask:0xf bound_ctrl:1
	v_mov_b32_dpp v1, v4 row_bcast:31 row_mask:0xc bank_mask:0xf
	s_nop 0
	v_add_u32_dpp v3, v3, v3 row_shr:4 row_mask:0xf bank_mask:0xf bound_ctrl:1
	s_nop 1
	v_add_u32_dpp v3, v3, v3 row_shr:8 row_mask:0xf bank_mask:0xf bound_ctrl:1
	s_nop 1
	v_add_u32_dpp v3, v3, v3 row_bcast:15 row_mask:0xa bank_mask:0xf

.Lw1b6:
	s_nop 1
	v_add_u32_dpp v3, v3, v3 row_bcast:31 row_mask:0xc bank_mask:0xf
	s_and_saveexec_b64 s[6:7], s[4:5]
	s_cbranch_execz .LBB1_7
	v_lshrrev_b32_e32 v5, 4, v0
	v_and_b32_e32 v5, 60, v5
	v_add_u32_e32 v6, 0x11b20, v5
	v_add_u32_e32 v5, 0x11b60, v5
	v_add_u32_e32 v1, v4, v1
	ds_write_b32 v5, v3
	ds_write_b32 v6, v1

.Lw1b8:
	ds_write_b32 v4, v5

.Lw1b9:
	s_movk_i32 s3, 0x7f
	s_waitcnt lgkmcnt(1)
	v_readfirstlane_b32 s40, v4
	v_readfirstlane_b32 s41, v5
	v_readfirstlane_b32 s42, v6
	v_readfirstlane_b32 s43, v7
	ds_read_b128 v[4:7], v1
	v_mov_b32_e32 v1, 0x11b50
	s_waitcnt lgkmcnt(1)
	v_readfirstlane_b32 s44, v8
	v_readfirstlane_b32 s45, v9
	v_readfirstlane_b32 s46, v10
	v_readfirstlane_b32 s47, v11

.Lw1b10:
	ds_read_b128 v[8:11], v1
	v_mov_b32_e32 v1, 0x11b60
	s_waitcnt lgkmcnt(1)
	v_readfirstlane_b32 s48, v4
	v_readfirstlane_b32 s49, v5
	v_readfirstlane_b32 s50, v6
	v_readfirstlane_b32 s51, v7
	s_waitcnt lgkmcnt(0)
	v_readfirstlane_b32 s52, v8
	ds_read_b128 v[4:7], v1
	v_mov_b32_e32 v8, 0x11b70

.Lw1b11:
	v_readfirstlane_b32 s53, v9
	v_readfirstlane_b32 s54, v10
	v_readfirstlane_b32 s55, v11
	ds_read_b128 v[8:11], v8
	v_cmp_lt_u32_e64 s[8:9], s3, v0
	s_movk_i32 s3, 0xbf
	v_cmp_lt_u32_e64 s[10:11], s3, v0
	s_movk_i32 s3, 0xff
	v_cmp_lt_u32_e64 s[12:13], s3, v0
	s_movk_i32 s3, 0x13f
	v_cmp_gt_u32_e64 s[6:7], 64, v0

.Lw1b12:
	v_cmp_lt_u32_e64 s[14:15], s3, v0
	s_movk_i32 s3, 0x17f
	s_waitcnt lgkmcnt(1)
	v_cndmask_b32_e64 v4, v4, 0, s[6:7]
	v_cndmask_b32_e64 v5, 0, v5, s[8:9]
	v_cndmask_b32_e64 v6, 0, v6, s[10:11]
	v_cmp_lt_u32_e64 s[16:17], s3, v0
	s_movk_i32 s3, 0x1bf
	v_add3_u32 v4, v5, v4, v6

.Lw1b13:
	v_cndmask_b32_e64 v5, 0, v7, s[12:13]
	s_waitcnt lgkmcnt(0)
	v_cndmask_b32_e64 v6, 0, v8, s[14:15]
	v_cmp_lt_u32_e64 s[18:19], s3, v0
	v_add3_u32 v4, v5, v4, v6
	v_cndmask_b32_e64 v5, 0, v9, s[16:17]
	v_cndmask_b32_e64 v6, 0, v10, s[18:19]
	v_add3_u32 v12, v5, v4, v6

.Lw1b14:
	v_mov_b32_e32 v4, 0x11b80
	ds_read_b128 v[4:7], v4
	s_movk_i32 s3, 0x1ff
	v_cmp_lt_u32_e64 s[20:21], s3, v0
	s_movk_i32 s3, 0x23f
	v_mov_b32_e32 v8, 0x11b90
	v_cndmask_b32_e64 v11, 0, v11, s[20:21]
	ds_read_b96 v[8:10], v8

.Lw1b15:
	v_cmp_lt_u32_e64 s[20:21], s3, v0
	s_movk_i32 s3, 0x27f
	s_load_dwordx2 s[24:25], s[0:1], 0x10
	s_waitcnt lgkmcnt(0)
	v_cndmask_b32_e64 v4, 0, v4, s[20:21]
	v_cmp_lt_u32_e64 s[20:21], s3, v0
	s_movk_i32 s3, 0x2bf
	v_add3_u32 v4, v11, v12, v4
	v_cndmask_b32_e64 v5, 0, v5, s[20:21]

.Lw1b16:
	v_cmp_lt_u32_e64 s[20:21], s3, v0
	s_movk_i32 s3, 0x2ff
	v_lshrrev_b32_e32 v1, 6, v0
	v_cndmask_b32_e64 v6, 0, v6, s[20:21]
	v_cmp_lt_u32_e64 s[20:21], s3, v0
	s_movk_i32 s3, 0x33f
	v_add3_u32 v4, v5, v4, v6
	v_cndmask_b32_e64 v5, 0, v7, s[20:21]
	v_cmp_lt_u32_e64 s[20:21], s3, v0

.Lw1b17:
	s_movk_i32 s3, 0x37f
	s_nop 0
	v_cndmask_b32_e64 v6, 0, v8, s[20:21]
	v_cmp_lt_u32_e64 s[20:21], s3, v0
	v_add3_u32 v4, v5, v4, v6
	s_nop 0
	v_cndmask_b32_e64 v5, 0, v9, s[20:21]
	v_cmp_eq_u32_e64 s[20:21], 15, v1
	s_nop 1
	v_cndmask_b32_e64 v6, 0, v10, s[20:21]

.Lw1b18:
	v_add3_u32 v4, v5, v4, v6
	s_and_saveexec_b64 s[26:27], vcc
	v_mov_b32_e32 v5, 0x11800
	v_sub_u32_e32 v2, v3, v2
	v_lshl_add_u32 v5, v0, 2, v5
	v_add_u32_e32 v2, v2, v4
	ds_write_b32 v5, v2
	s_or_b64 exec, exec, s[26:27]
	s_movk_i32 s3, 0x61
	v_cmp_eq_u32_e32 vcc, s3, v0

.Lw1b19:
	s_and_saveexec_b64 s[26:27], vcc
	v_add_u32_e32 v2, v4, v3
	v_mov_b32_e32 v3, 0x11988
	ds_write_b32 v3, v2
	s_or_b64 exec, exec, s[26:27]
	v_mov_b32_e32 v2, 0x11988
	s_waitcnt lgkmcnt(0)
	s_barrier
	ds_read_b32 v2, v2
	v_mov_b32_e32 v3, 0x11900

.Lw1b20:
	s_and_b64 s[26:27], s[30:31], exec
	ds_read_b32 v5, v3
	s_cselect_b32 s26, 0xc3500, 0
	s_lshl_b32 s56, s26, 2
	s_add_u32 s28, s24, s56
	s_movk_i32 s24, 0x2001
	s_waitcnt lgkmcnt(1)
	v_cmp_gt_i32_e32 vcc, s24, v2
	v_readfirstlane_b32 s3, v2
	s_addc_u32 s29, s25, 0
	s_mov_b64 s[34:35], -1
	s_cbranch_vccnz .LBB1_37
	s_mov_b64 s[24:25], 0

.Lw1b21:
	v_mov_b32_e32 v3, 0x11880
	s_movk_i32 s36, 0x51
	s_movk_i32 s37, 0x52
	s_movk_i32 s38, 0x59
	s_movk_i32 s39, 0x5a
	s_movk_i32 s57, 0x5d
	s_movk_i32 s58, 0x5e
	s_movk_i32 s59, 0x5f
	s_movk_i32 s60, 0x60
	s_movk_i32 s61, 0x61
	v_mov_b32_e32 v4, 0x11990
	v_mov_b32_e32 v6, 1
	v_mov_b32_e32 v7, 0x11840

.Lw1b22:
	v_mov_b32_e32 v8, 0x11820
	v_mov_b32_e32 v9, 0x11810
	v_mov_b32_e32 v10, 0x11808
	v_mov_b32_e32 v11, 0x11804
	v_mov_b32_e32 v12, 0x11800
	v_mov_b32_e32 v13, v0
	s_branch .LBB1_16

.Lw1b23:
	ds_read_b32 v14, v14
	s_waitcnt lgkmcnt(0)
	v_lshl_add_u32 v14, v16, 13, v14
	v_sub_u32_e32 v14, v14, v15
	v_add_u32_e32 v14, v13, v14
	v_ashrrev_i32_e32 v15, 31, v14
	v_lshl_add_u64 v[14:15], v[14:15], 2, s[28:29]
	global_load_dword v14, v[14:15], off
	v_add_u32_e32 v13, 0x400, v13

.Lw1b24:
	v_cmp_le_i32_e32 vcc, s3, v13
	s_or_b64 s[24:25], vcc, s[24:25]
	s_waitcnt vmcnt(0)
	v_lshrrev_b32_e32 v14, 15, v14
	v_and_b32_e32 v14, 0x1fffc, v14
	v_add_u32_e32 v14, 0x10000, v14
	ds_add_u32 v14, v6
	s_andn2_b64 exec, exec, s[24:25]
	s_cbranch_execz .LBB1_36

.Lw1b25:
	v_cndmask_b32_e64 v14, 64, 0, vcc
	v_lshl_or_b32 v15, v14, 2, v3
	ds_read_b32 v15, v15
	v_or_b32_e32 v16, 32, v14
	s_waitcnt lgkmcnt(0)
	v_cmp_gt_i32_e32 vcc, v15, v13
	s_nop 1
	v_cndmask_b32_e32 v15, v16, v14, vcc
	v_cmp_lt_u32_e64 s[26:27], s36, v15
	v_cmp_gt_u32_e32 vcc, s37, v15
	s_and_saveexec_b64 s[34:35], vcc

.Lw1b26:
	s_cbranch_execz .LBB1_18
	v_lshl_add_u32 v14, v15, 2, v7
	ds_read_b32 v16, v14
	s_andn2_b64 s[26:27], s[26:27], exec
	v_or_b32_e32 v14, 16, v15
	s_waitcnt lgkmcnt(0)
	v_cmp_gt_i32_e32 vcc, v16, v13
	s_and_b64 s[62:63], vcc, exec
	s_or_b64 s[26:27], s[26:27], s[62:63]

.Lw1b27:
	v_cmp_lt_u32_e64 s[26:27], s38, v14
	v_cmp_gt_u32_e32 vcc, s39, v14
	s_and_saveexec_b64 s[34:35], vcc
	s_cbranch_execz .LBB1_22
	v_lshl_add_u32 v15, v14, 2, v8
	ds_read_b32 v16, v15
	s_andn2_b64 s[26:27], s[26:27], exec
	v_add_u32_e32 v15, 8, v14
	s_waitcnt lgkmcnt(0)
	v_cmp_gt_i32_e32 vcc, v16, v13
	s_and_b64 s[62:63], vcc, exec
	s_or_b64 s[26:27], s[26:27], s[62:63]

.Lw1b29:
	s_waitcnt lgkmcnt(0)
	v_cmp_gt_i32_e32 vcc, v14, v13
	s_and_b64 s[62:63], vcc, exec
	s_or_b64 s[26:27], s[26:27], s[62:63]

.Lw1b30:
	ds_read_b32 v15, v14
	s_andn2_b64 s[26:27], s[26:27], exec
	v_add_u32_e32 v14, 2, v16
	s_waitcnt lgkmcnt(0)
	v_cmp_gt_i32_e32 vcc, v15, v13
	s_and_b64 s[62:63], vcc, exec
	s_or_b64 s[26:27], s[26:27], s[62:63]

.Lw1b31:
	s_and_saveexec_b64 s[34:35], vcc
	s_cbranch_execz .LBB1_34
	v_lshl_add_u32 v15, v14, 2, v11
	ds_read_b32 v15, v15
	s_andn2_b64 s[26:27], s[26:27], exec
	v_add_u32_e32 v16, 1, v14
	s_waitcnt lgkmcnt(0)
	v_cmp_gt_i32_e32 vcc, v15, v13
	s_and_b64 s[62:63], vcc, exec
	s_or_b64 s[26:27], s[26:27], s[62:63]

.Lw1b32:
	v_lshl_add_u32 v15, v14, 2, v12
	ds_read_b32 v15, v15
	v_mov_b32_e32 v16, v14
	s_branch .LBB1_15

.Lw1b33:
	s_and_saveexec_b64 s[34:35], vcc
	s_cbranch_execz .LBB1_60
	s_waitcnt lgkmcnt(0)
	v_cmp_gt_i32_e32 vcc, v5, v0
	v_mov_b32_e32 v4, 0x11880
	s_movk_i32 s36, 0x51
	v_cndmask_b32_e64 v3, 64, 0, vcc
	v_lshl_or_b32 v4, v3, 2, v4
	ds_read_b32 v4, v4
	v_or_b32_e32 v6, 32, v3
	s_movk_i32 s38, 0x52

.Lw1b34:
	s_waitcnt lgkmcnt(0)
	v_cmp_gt_i32_e32 vcc, v4, v0
	s_nop 1
	v_cndmask_b32_e32 v4, v6, v3, vcc
	v_cmp_lt_u32_e64 s[36:37], s36, v4
	v_cmp_gt_u32_e32 vcc, s38, v4
	s_and_saveexec_b64 s[38:39], vcc
	s_cbranch_execz .LBB1_41
	v_mov_b32_e32 v3, 0x11840
	v_lshl_add_u32 v3, v4, 2, v3
	ds_read_b32 v6, v3

.Lw1b35:
	s_andn2_b64 s[36:37], s[36:37], exec
	v_or_b32_e32 v3, 16, v4
	s_waitcnt lgkmcnt(0)
	v_cmp_gt_i32_e32 vcc, v6, v0
	s_and_b64 s[58:59], vcc, exec
	s_or_b64 s[36:37], s[36:37], s[58:59]

.Lw1b36:
	s_and_saveexec_b64 s[38:39], vcc
	s_cbranch_execz .LBB1_45
	v_mov_b32_e32 v4, 0x11820
	v_lshl_add_u32 v4, v3, 2, v4
	ds_read_b32 v6, v4
	s_andn2_b64 s[36:37], s[36:37], exec
	v_add_u32_e32 v4, 8, v3
	s_waitcnt lgkmcnt(0)
	v_cmp_gt_i32_e32 vcc, v6, v0
	s_and_b64 s[58:59], vcc, exec
	s_or_b64 s[36:37], s[36:37], s[58:59]

.Lw1b37:
	s_and_saveexec_b64 s[38:39], s[36:37]
	v_mov_b32_e32 v4, v3
	s_or_b64 exec, exec, s[38:39]
	s_movk_i32 s36, 0x5d
	s_movk_i32 s38, 0x5e
	v_cmp_lt_u32_e64 s[36:37], s36, v4
	v_cmp_gt_u32_e32 vcc, s38, v4
	s_and_saveexec_b64 s[38:39], vcc
	s_cbranch_execz .LBB1_49
	v_mov_b32_e32 v3, 0x11810
	v_lshl_add_u32 v3, v4, 2, v3
	ds_read_b32 v3, v3

.Lw1b38:
	s_andn2_b64 s[36:37], s[36:37], exec
	v_add_u32_e32 v6, 4, v4
	s_waitcnt lgkmcnt(0)
	v_cmp_gt_i32_e32 vcc, v3, v0
	s_and_b64 s[58:59], vcc, exec
	s_or_b64 s[36:37], s[36:37], s[58:59]

.Lw1b39:
	v_cmp_gt_u32_e32 vcc, s38, v6
	s_and_saveexec_b64 s[38:39], vcc
	s_cbranch_execz .LBB1_53
	v_mov_b32_e32 v3, 0x11808
	v_lshl_add_u32 v3, v6, 2, v3
	ds_read_b32 v4, v3
	s_andn2_b64 s[36:37], s[36:37], exec
	v_add_u32_e32 v3, 2, v6
	s_waitcnt lgkmcnt(0)
	v_cmp_gt_i32_e32 vcc, v4, v0
	s_and_b64 s[58:59], vcc, exec
	s_or_b64 s[36:37], s[36:37], s[58:59]

.Lw1b41:
	ds_read_b32 v4, v4
	s_andn2_b64 s[36:37], s[36:37], exec
	v_add_u32_e32 v6, 1, v3
	s_waitcnt lgkmcnt(0)
	v_cmp_gt_i32_e32 vcc, v4, v0
	s_and_b64 s[58:59], vcc, exec
	s_or_b64 s[36:37], s[36:37], s[58:59]

.Lw1b42:
	v_mov_b32_e32 v6, v3
	s_or_b64 exec, exec, s[38:39]
	v_mov_b32_e32 v3, 0x11990
	v_lshl_add_u32 v3, v6, 2, v3
	ds_read_b32 v3, v3
	v_lshlrev_b32_e32 v6, 13, v6
	s_waitcnt lgkmcnt(1)
	v_sub_u32_e32 v4, v0, v4
	s_waitcnt lgkmcnt(0)
	v_add3_u32 v6, v4, v6, v3

.Lw1b43:
	v_ashrrev_i32_e32 v7, 31, v6
	v_lshl_add_u64 v[6:7], v[6:7], 2, s[28:29]
	global_load_dword v3, v[6:7], off

.Lw1b44:
	s_movk_i32 s36, 0x51
	v_cndmask_b32_e64 v4, 64, 0, vcc
	v_lshl_or_b32 v7, v4, 2, v7
	ds_read_b32 v7, v7
	v_or_b32_e32 v8, 32, v4
	s_movk_i32 s38, 0x52
	s_waitcnt lgkmcnt(0)
	v_cmp_gt_i32_e32 vcc, v7, v6
	s_nop 1
	v_cndmask_b32_e32 v7, v8, v4, vcc
	v_cmp_lt_u32_e64 s[36:37], s36, v7

.Lw1b45:
	v_cmp_gt_u32_e32 vcc, s38, v7
	s_and_saveexec_b64 s[38:39], vcc
	s_cbranch_execz .LBB1_63
	v_mov_b32_e32 v4, 0x11840
	v_lshl_add_u32 v4, v7, 2, v4
	ds_read_b32 v8, v4
	s_andn2_b64 s[36:37], s[36:37], exec
	v_or_b32_e32 v4, 16, v7
	s_waitcnt lgkmcnt(0)
	v_cmp_gt_i32_e32 vcc, v8, v6
	s_and_b64 s[58:59], vcc, exec

.Lw1b46:
	s_or_b64 s[36:37], s[36:37], s[58:59]

.Lw1b47:
	ds_read_b32 v8, v7
	s_andn2_b64 s[36:37], s[36:37], exec
	v_add_u32_e32 v7, 8, v4
	s_waitcnt lgkmcnt(0)
	v_cmp_gt_i32_e32 vcc, v8, v6
	s_and_b64 s[58:59], vcc, exec
	s_or_b64 s[36:37], s[36:37], s[58:59]

.Lw1b48:
	v_cmp_lt_u32_e64 s[36:37], s36, v7
	v_cmp_gt_u32_e32 vcc, s38, v7
	s_and_saveexec_b64 s[38:39], vcc
	s_cbranch_execz .LBB1_71
	v_mov_b32_e32 v4, 0x11810
	v_lshl_add_u32 v4, v7, 2, v4
	ds_read_b32 v4, v4
	s_andn2_b64 s[36:37], s[36:37], exec
	v_add_u32_e32 v8, 4, v7
	s_waitcnt lgkmcnt(0)
	v_cmp_gt_i32_e32 vcc, v4, v6

.Lw1b49:
	s_and_b64 s[58:59], vcc, exec
	s_or_b64 s[36:37], s[36:37], s[58:59]

.Lw1b50:
	v_lshl_add_u32 v4, v8, 2, v4
	ds_read_b32 v7, v4
	s_andn2_b64 s[36:37], s[36:37], exec
	v_add_u32_e32 v4, 2, v8
	s_waitcnt lgkmcnt(0)
	v_cmp_gt_i32_e32 vcc, v7, v6
	s_and_b64 s[58:59], vcc, exec
	s_or_b64 s[36:37], s[36:37], s[58:59]

.Lw1b51:
	s_movk_i32 s38, 0x61
	v_cmp_lt_u32_e64 s[36:37], s36, v4
	v_cmp_gt_u32_e32 vcc, s38, v4
	s_and_saveexec_b64 s[38:39], vcc
	s_cbranch_execz .LBB1_79
	v_mov_b32_e32 v7, 0x11804
	v_lshl_add_u32 v7, v4, 2, v7
	ds_read_b32 v7, v7
	s_andn2_b64 s[36:37], s[36:37], exec
	v_add_u32_e32 v8, 1, v4
	s_waitcnt lgkmcnt(0)

.Lw1b52:
	v_cmp_gt_i32_e32 vcc, v7, v6
	s_and_b64 s[58:59], vcc, exec
	s_or_b64 s[36:37], s[36:37], s[58:59]

.Lw1b53:
	v_lshl_add_u32 v4, v8, 2, v4
	ds_read_b32 v4, v4
	v_lshlrev_b32_e32 v8, 13, v8
	s_waitcnt lgkmcnt(1)
	v_sub_u32_e32 v6, v6, v7
	s_waitcnt lgkmcnt(0)
	v_add3_u32 v6, v6, v8, v4
	v_ashrrev_i32_e32 v7, 31, v6
	v_lshl_add_u64 v[6:7], v[6:7], 2, s[28:29]
	global_load_dword v4, v[6:7], off

.Lw1b55:
	ds_read_b32 v8, v8
	v_or_b32_e32 v9, 32, v6
	s_movk_i32 s38, 0x52
	s_waitcnt lgkmcnt(0)
	v_cmp_gt_i32_e32 vcc, v8, v7
	s_nop 1
	v_cndmask_b32_e32 v8, v9, v6, vcc
	v_cmp_lt_u32_e64 s[36:37], s36, v8
	v_cmp_gt_u32_e32 vcc, s38, v8
	s_and_saveexec_b64 s[38:39], vcc
	s_cbranch_execz .LBB1_85
	v_mov_b32_e32 v6, 0x11840

.Lw1b56:
	v_lshl_add_u32 v6, v8, 2, v6
	ds_read_b32 v9, v6
	s_andn2_b64 s[36:37], s[36:37], exec
	v_or_b32_e32 v6, 16, v8
	s_waitcnt lgkmcnt(0)
	v_cmp_gt_i32_e32 vcc, v9, v7
	s_and_b64 s[58:59], vcc, exec
	s_or_b64 s[36:37], s[36:37], s[58:59]

.Lw1b57:
	s_movk_i32 s36, 0x59
	s_movk_i32 s38, 0x5a
	v_cmp_lt_u32_e64 s[36:37], s36, v6
	v_cmp_gt_u32_e32 vcc, s38, v6
	s_and_saveexec_b64 s[38:39], vcc
	s_cbranch_execz .LBB1_89
	v_mov_b32_e32 v8, 0x11820
	v_lshl_add_u32 v8, v6, 2, v8
	ds_read_b32 v9, v8
	s_andn2_b64 s[36:37], s[36:37], exec
	v_add_u32_e32 v8, 8, v6

.Lw1b58:
	s_waitcnt lgkmcnt(0)
	v_cmp_gt_i32_e32 vcc, v9, v7
	s_and_b64 s[58:59], vcc, exec
	s_or_b64 s[36:37], s[36:37], s[58:59]

.Lw1b59:
	v_mov_b32_e32 v6, 0x11810
	v_lshl_add_u32 v6, v8, 2, v6
	ds_read_b32 v6, v6
	s_andn2_b64 s[36:37], s[36:37], exec
	v_add_u32_e32 v9, 4, v8
	s_waitcnt lgkmcnt(0)
	v_cmp_gt_i32_e32 vcc, v6, v7
	s_and_b64 s[58:59], vcc, exec
	s_or_b64 s[36:37], s[36:37], s[58:59]

.Lw1b60:
	s_or_b64 exec, exec, s[38:39]
	s_movk_i32 s36, 0x5f
	s_movk_i32 s38, 0x60
	v_cmp_lt_u32_e64 s[36:37], s36, v9
	v_cmp_gt_u32_e32 vcc, s38, v9
	s_and_saveexec_b64 s[38:39], vcc
	s_cbranch_execz .LBB1_97
	v_mov_b32_e32 v6, 0x11808
	v_lshl_add_u32 v6, v9, 2, v6
	ds_read_b32 v8, v6
	s_andn2_b64 s[36:37], s[36:37], exec

.Lw1b61:
	v_add_u32_e32 v6, 2, v9
	s_waitcnt lgkmcnt(0)
	v_cmp_gt_i32_e32 vcc, v8, v7
	s_and_b64 s[58:59], vcc, exec
	s_or_b64 s[36:37], s[36:37], s[58:59]

.Lw1b62:
	s_cbranch_execz .LBB1_101
	v_mov_b32_e32 v8, 0x11804
	v_lshl_add_u32 v8, v6, 2, v8
	ds_read_b32 v8, v8
	s_andn2_b64 s[36:37], s[36:37], exec
	v_add_u32_e32 v9, 1, v6
	s_waitcnt lgkmcnt(0)
	v_cmp_gt_i32_e32 vcc, v8, v7
	s_and_b64 s[58:59], vcc, exec
	s_or_b64 s[36:37], s[36:37], s[58:59]

.Lw1b63:
	v_mov_b32_e32 v8, 0x11800
	v_lshl_add_u32 v8, v6, 2, v8
	ds_read_b32 v8, v8
	v_mov_b32_e32 v9, v6
	s_or_b64 exec, exec, s[38:39]
	v_mov_b32_e32 v6, 0x11990
	v_lshl_add_u32 v6, v9, 2, v6
	ds_read_b32 v6, v6
	v_lshlrev_b32_e32 v9, 13, v9

.Lw1b64:
	s_waitcnt lgkmcnt(1)
	v_sub_u32_e32 v7, v7, v8
	s_waitcnt lgkmcnt(0)
	v_add3_u32 v6, v7, v9, v6
	v_ashrrev_i32_e32 v7, 31, v6
	v_lshl_add_u64 v[6:7], v[6:7], 2, s[28:29]
	global_load_dword v6, v[6:7], off

.Lw1b65:
	s_and_saveexec_b64 s[34:35], vcc
	s_cbranch_execz .LBB1_126
	s_waitcnt lgkmcnt(0)
	v_cmp_gt_i32_e32 vcc, v5, v8
	v_mov_b32_e32 v9, 0x11880
	s_movk_i32 s36, 0x51
	v_cndmask_b32_e64 v7, 64, 0, vcc
	v_lshl_or_b32 v9, v7, 2, v9
	ds_read_b32 v9, v9
	v_or_b32_e32 v10, 32, v7
	s_movk_i32 s38, 0x52

.Lw1b66:
	s_waitcnt lgkmcnt(0)
	v_cmp_gt_i32_e32 vcc, v9, v8
	s_nop 1
	v_cndmask_b32_e32 v9, v10, v7, vcc
	v_cmp_lt_u32_e64 s[36:37], s36, v9
	v_cmp_gt_u32_e32 vcc, s38, v9
	s_and_saveexec_b64 s[38:39], vcc
	s_cbranch_execz .LBB1_107
	v_mov_b32_e32 v7, 0x11840
	v_lshl_add_u32 v7, v9, 2, v7
	ds_read_b32 v10, v7

.Lw1b67:
	s_andn2_b64 s[36:37], s[36:37], exec
	v_or_b32_e32 v7, 16, v9
	s_waitcnt lgkmcnt(0)
	v_cmp_gt_i32_e32 vcc, v10, v8
	s_and_b64 s[58:59], vcc, exec
	s_or_b64 s[36:37], s[36:37], s[58:59]

.Lw1b68:
	s_and_saveexec_b64 s[38:39], vcc
	s_cbranch_execz .LBB1_111
	v_mov_b32_e32 v9, 0x11820
	v_lshl_add_u32 v9, v7, 2, v9
	ds_read_b32 v10, v9
	s_andn2_b64 s[36:37], s[36:37], exec
	v_add_u32_e32 v9, 8, v7
	s_waitcnt lgkmcnt(0)
	v_cmp_gt_i32_e32 vcc, v10, v8
	s_and_b64 s[58:59], vcc, exec
	s_or_b64 s[36:37], s[36:37], s[58:59]

.Lw1b69:
	s_and_saveexec_b64 s[38:39], s[36:37]
	v_mov_b32_e32 v9, v7
	s_or_b64 exec, exec, s[38:39]
	s_movk_i32 s36, 0x5d
	s_movk_i32 s38, 0x5e
	v_cmp_lt_u32_e64 s[36:37], s36, v9
	v_cmp_gt_u32_e32 vcc, s38, v9
	s_and_saveexec_b64 s[38:39], vcc
	s_cbranch_execz .LBB1_115
	v_mov_b32_e32 v7, 0x11810
	v_lshl_add_u32 v7, v9, 2, v7
	ds_read_b32 v7, v7

.Lw1b70:
	s_andn2_b64 s[36:37], s[36:37], exec
	v_add_u32_e32 v10, 4, v9
	s_waitcnt lgkmcnt(0)
	v_cmp_gt_i32_e32 vcc, v7, v8
	s_and_b64 s[58:59], vcc, exec
	s_or_b64 s[36:37], s[36:37], s[58:59]

.Lw1b71:
	v_cmp_gt_u32_e32 vcc, s38, v10
	s_and_saveexec_b64 s[38:39], vcc
	s_cbranch_execz .LBB1_119
	v_mov_b32_e32 v7, 0x11808
	v_lshl_add_u32 v7, v10, 2, v7
	ds_read_b32 v9, v7
	s_andn2_b64 s[36:37], s[36:37], exec
	v_add_u32_e32 v7, 2, v10
	s_waitcnt lgkmcnt(0)
	v_cmp_gt_i32_e32 vcc, v9, v8
	s_and_b64 s[58:59], vcc, exec
	s_or_b64 s[36:37], s[36:37], s[58:59]

.Lw1b73:
	ds_read_b32 v9, v9
	s_andn2_b64 s[36:37], s[36:37], exec
	v_add_u32_e32 v10, 1, v7
	s_waitcnt lgkmcnt(0)
	v_cmp_gt_i32_e32 vcc, v9, v8
	s_and_b64 s[58:59], vcc, exec
	s_or_b64 s[36:37], s[36:37], s[58:59]

.Lw1b74:
	v_mov_b32_e32 v10, v7
	s_or_b64 exec, exec, s[38:39]
	v_mov_b32_e32 v7, 0x11990
	v_lshl_add_u32 v7, v10, 2, v7
	ds_read_b32 v7, v7
	v_lshlrev_b32_e32 v10, 13, v10
	s_waitcnt lgkmcnt(1)
	v_sub_u32_e32 v8, v8, v9
	s_waitcnt lgkmcnt(0)
	v_add3_u32 v8, v8, v10, v7

.Lw1b75:
	v_ashrrev_i32_e32 v9, 31, v8
	v_lshl_add_u64 v[8:9], v[8:9], 2, s[28:29]
	global_load_dword v7, v[8:9], off

.Lw1b76:
	s_movk_i32 s36, 0x51
	v_cndmask_b32_e64 v8, 64, 0, vcc
	v_lshl_or_b32 v10, v8, 2, v10
	ds_read_b32 v10, v10
	v_or_b32_e32 v11, 32, v8
	s_movk_i32 s38, 0x52
	s_waitcnt lgkmcnt(0)
	v_cmp_gt_i32_e32 vcc, v10, v9
	s_nop 1
	v_cndmask_b32_e32 v10, v11, v8, vcc
	v_cmp_lt_u32_e64 s[36:37], s36, v10

.Lw1b77:
	v_cmp_gt_u32_e32 vcc, s38, v10
	s_and_saveexec_b64 s[38:39], vcc
	s_cbranch_execz .LBB1_129
	v_mov_b32_e32 v8, 0x11840
	v_lshl_add_u32 v8, v10, 2, v8
	ds_read_b32 v11, v8
	s_andn2_b64 s[36:37], s[36:37], exec
	v_or_b32_e32 v8, 16, v10
	s_waitcnt lgkmcnt(0)
	v_cmp_gt_i32_e32 vcc, v11, v9
	s_and_b64 s[58:59], vcc, exec

.Lw1b79:
	ds_read_b32 v11, v10
	s_andn2_b64 s[36:37], s[36:37], exec
	v_add_u32_e32 v10, 8, v8
	s_waitcnt lgkmcnt(0)
	v_cmp_gt_i32_e32 vcc, v11, v9
	s_and_b64 s[58:59], vcc, exec
	s_or_b64 s[36:37], s[36:37], s[58:59]

.Lw1b80:
	v_cmp_lt_u32_e64 s[36:37], s36, v10
	v_cmp_gt_u32_e32 vcc, s38, v10
	s_and_saveexec_b64 s[38:39], vcc
	s_cbranch_execz .LBB1_137
	v_mov_b32_e32 v8, 0x11810
	v_lshl_add_u32 v8, v10, 2, v8
	ds_read_b32 v8, v8
	s_andn2_b64 s[36:37], s[36:37], exec
	v_add_u32_e32 v11, 4, v10
	s_waitcnt lgkmcnt(0)
	v_cmp_gt_i32_e32 vcc, v8, v9

.Lw1b82:
	v_lshl_add_u32 v8, v11, 2, v8
	ds_read_b32 v10, v8
	s_andn2_b64 s[36:37], s[36:37], exec
	v_add_u32_e32 v8, 2, v11
	s_waitcnt lgkmcnt(0)
	v_cmp_gt_i32_e32 vcc, v10, v9
	s_and_b64 s[58:59], vcc, exec
	s_or_b64 s[36:37], s[36:37], s[58:59]

.Lw1b83:
	s_movk_i32 s38, 0x61
	v_cmp_lt_u32_e64 s[36:37], s36, v8
	v_cmp_gt_u32_e32 vcc, s38, v8
	s_and_saveexec_b64 s[38:39], vcc
	s_cbranch_execz .LBB1_145
	v_mov_b32_e32 v10, 0x11804
	v_lshl_add_u32 v10, v8, 2, v10
	ds_read_b32 v10, v10
	s_andn2_b64 s[36:37], s[36:37], exec
	v_add_u32_e32 v11, 1, v8
	s_waitcnt lgkmcnt(0)

.Lw1b84:
	v_cmp_gt_i32_e32 vcc, v10, v9
	s_and_b64 s[58:59], vcc, exec
	s_or_b64 s[36:37], s[36:37], s[58:59]

.Lw1b85:
	v_lshl_add_u32 v8, v11, 2, v8
	ds_read_b32 v8, v8
	v_lshlrev_b32_e32 v11, 13, v11
	s_waitcnt lgkmcnt(1)
	v_sub_u32_e32 v9, v9, v10
	s_waitcnt lgkmcnt(0)
	v_add3_u32 v8, v9, v11, v8
	v_ashrrev_i32_e32 v9, 31, v8
	v_lshl_add_u64 v[8:9], v[8:9], 2, s[28:29]
	global_load_dword v8, v[8:9], off

.Lw1b87:
	ds_read_b32 v11, v11
	v_or_b32_e32 v12, 32, v9
	s_movk_i32 s38, 0x52
	s_waitcnt lgkmcnt(0)
	v_cmp_gt_i32_e32 vcc, v11, v10
	s_nop 1
	v_cndmask_b32_e32 v11, v12, v9, vcc
	v_cmp_lt_u32_e64 s[36:37], s36, v11
	v_cmp_gt_u32_e32 vcc, s38, v11
	s_and_saveexec_b64 s[38:39], vcc
	s_cbranch_execz .LBB1_151
	v_mov_b32_e32 v9, 0x11840

.Lw1b88:
	v_lshl_add_u32 v9, v11, 2, v9
	ds_read_b32 v12, v9
	s_andn2_b64 s[36:37], s[36:37], exec
	v_or_b32_e32 v9, 16, v11
	s_waitcnt lgkmcnt(0)
	v_cmp_gt_i32_e32 vcc, v12, v10
	s_and_b64 s[58:59], vcc, exec
	s_or_b64 s[36:37], s[36:37], s[58:59]

.Lw1b89:
	s_movk_i32 s36, 0x59
	s_movk_i32 s38, 0x5a
	v_cmp_lt_u32_e64 s[36:37], s36, v9
	v_cmp_gt_u32_e32 vcc, s38, v9
	s_and_saveexec_b64 s[38:39], vcc
	s_cbranch_execz .LBB1_155
	v_mov_b32_e32 v11, 0x11820
	v_lshl_add_u32 v11, v9, 2, v11
	ds_read_b32 v12, v11
	s_andn2_b64 s[36:37], s[36:37], exec
	v_add_u32_e32 v11, 8, v9

.Lw1b90:
	s_waitcnt lgkmcnt(0)
	v_cmp_gt_i32_e32 vcc, v12, v10
	s_and_b64 s[58:59], vcc, exec
	s_or_b64 s[36:37], s[36:37], s[58:59]

.Lw1b91:
	v_mov_b32_e32 v9, 0x11810
	v_lshl_add_u32 v9, v11, 2, v9
	ds_read_b32 v9, v9
	s_andn2_b64 s[36:37], s[36:37], exec
	v_add_u32_e32 v12, 4, v11
	s_waitcnt lgkmcnt(0)
	v_cmp_gt_i32_e32 vcc, v9, v10
	s_and_b64 s[58:59], vcc, exec
	s_or_b64 s[36:37], s[36:37], s[58:59]

.Lw1b92:
	s_or_b64 exec, exec, s[38:39]
	s_movk_i32 s36, 0x5f
	s_movk_i32 s38, 0x60
	v_cmp_lt_u32_e64 s[36:37], s36, v12
	v_cmp_gt_u32_e32 vcc, s38, v12
	s_and_saveexec_b64 s[38:39], vcc
	s_cbranch_execz .LBB1_163
	v_mov_b32_e32 v9, 0x11808
	v_lshl_add_u32 v9, v12, 2, v9
	ds_read_b32 v11, v9
	s_andn2_b64 s[36:37], s[36:37], exec

.Lw1b93:
	v_add_u32_e32 v9, 2, v12
	s_waitcnt lgkmcnt(0)
	v_cmp_gt_i32_e32 vcc, v11, v10
	s_and_b64 s[58:59], vcc, exec
	s_or_b64 s[36:37], s[36:37], s[58:59]

.Lw1b94:
	s_cbranch_execz .LBB1_167
	v_mov_b32_e32 v11, 0x11804
	v_lshl_add_u32 v11, v9, 2, v11
	ds_read_b32 v11, v11
	s_andn2_b64 s[36:37], s[36:37], exec
	v_add_u32_e32 v12, 1, v9
	s_waitcnt lgkmcnt(0)
	v_cmp_gt_i32_e32 vcc, v11, v10
	s_and_b64 s[58:59], vcc, exec
	s_or_b64 s[36:37], s[36:37], s[58:59]

.Lw1b95:
	v_mov_b32_e32 v11, 0x11800
	v_lshl_add_u32 v11, v9, 2, v11
	ds_read_b32 v11, v11
	v_mov_b32_e32 v12, v9
	s_or_b64 exec, exec, s[38:39]
	v_mov_b32_e32 v9, 0x11990
	v_lshl_add_u32 v9, v12, 2, v9
	ds_read_b32 v9, v9
	v_lshlrev_b32_e32 v12, 13, v12

.Lw1b96:
	s_waitcnt lgkmcnt(1)
	v_sub_u32_e32 v10, v10, v11
	s_waitcnt lgkmcnt(0)
	v_add3_u32 v10, v10, v12, v9
	v_ashrrev_i32_e32 v11, 31, v10
	v_lshl_add_u64 v[10:11], v[10:11], 2, s[28:29]
	global_load_dword v9, v[10:11], off

.Lw1b97:
	s_and_saveexec_b64 s[34:35], vcc
	s_cbranch_execz .LBB1_192
	s_waitcnt lgkmcnt(0)
	v_cmp_gt_i32_e32 vcc, v5, v11
	v_mov_b32_e32 v12, 0x11880
	s_movk_i32 s36, 0x51
	v_cndmask_b32_e64 v10, 64, 0, vcc
	v_lshl_or_b32 v12, v10, 2, v12
	ds_read_b32 v12, v12
	v_or_b32_e32 v13, 32, v10
	s_movk_i32 s38, 0x52

.Lw1b98:
	s_waitcnt lgkmcnt(0)
	v_cmp_gt_i32_e32 vcc, v12, v11
	s_nop 1
	v_cndmask_b32_e32 v12, v13, v10, vcc
	v_cmp_lt_u32_e64 s[36:37], s36, v12
	v_cmp_gt_u32_e32 vcc, s38, v12
	s_and_saveexec_b64 s[38:39], vcc
	s_cbranch_execz .LBB1_173
	v_mov_b32_e32 v10, 0x11840
	v_lshl_add_u32 v10, v12, 2, v10
	ds_read_b32 v13, v10

.Lw1b99:
	s_andn2_b64 s[36:37], s[36:37], exec
	v_or_b32_e32 v10, 16, v12
	s_waitcnt lgkmcnt(0)
	v_cmp_gt_i32_e32 vcc, v13, v11
	s_and_b64 s[58:59], vcc, exec
	s_or_b64 s[36:37], s[36:37], s[58:59]

.Lw1b100:
	s_and_saveexec_b64 s[38:39], vcc
	s_cbranch_execz .LBB1_177
	v_mov_b32_e32 v12, 0x11820
	v_lshl_add_u32 v12, v10, 2, v12
	ds_read_b32 v13, v12
	s_andn2_b64 s[36:37], s[36:37], exec
	v_add_u32_e32 v12, 8, v10
	s_waitcnt lgkmcnt(0)
	v_cmp_gt_i32_e32 vcc, v13, v11
	s_and_b64 s[58:59], vcc, exec
	s_or_b64 s[36:37], s[36:37], s[58:59]

.Lw1b101:
	s_and_saveexec_b64 s[38:39], s[36:37]
	v_mov_b32_e32 v12, v10
	s_or_b64 exec, exec, s[38:39]
	s_movk_i32 s36, 0x5d
	s_movk_i32 s38, 0x5e
	v_cmp_lt_u32_e64 s[36:37], s36, v12
	v_cmp_gt_u32_e32 vcc, s38, v12
	s_and_saveexec_b64 s[38:39], vcc
	s_cbranch_execz .LBB1_181
	v_mov_b32_e32 v10, 0x11810
	v_lshl_add_u32 v10, v12, 2, v10
	ds_read_b32 v10, v10

.Lw1b102:
	s_andn2_b64 s[36:37], s[36:37], exec
	v_add_u32_e32 v13, 4, v12
	s_waitcnt lgkmcnt(0)
	v_cmp_gt_i32_e32 vcc, v10, v11
	s_and_b64 s[58:59], vcc, exec
	s_or_b64 s[36:37], s[36:37], s[58:59]

.Lw1b103:
	v_cmp_gt_u32_e32 vcc, s38, v13
	s_and_saveexec_b64 s[38:39], vcc
	s_cbranch_execz .LBB1_185
	v_mov_b32_e32 v10, 0x11808
	v_lshl_add_u32 v10, v13, 2, v10
	ds_read_b32 v12, v10
	s_andn2_b64 s[36:37], s[36:37], exec
	v_add_u32_e32 v10, 2, v13
	s_waitcnt lgkmcnt(0)
	v_cmp_gt_i32_e32 vcc, v12, v11
	s_and_b64 s[58:59], vcc, exec
	s_or_b64 s[36:37], s[36:37], s[58:59]

.Lw1b105:
	ds_read_b32 v12, v12
	s_andn2_b64 s[36:37], s[36:37], exec
	v_add_u32_e32 v13, 1, v10
	s_waitcnt lgkmcnt(0)
	v_cmp_gt_i32_e32 vcc, v12, v11
	s_and_b64 s[58:59], vcc, exec
	s_or_b64 s[36:37], s[36:37], s[58:59]

.Lw1b106:
	v_mov_b32_e32 v13, v10
	s_or_b64 exec, exec, s[38:39]
	v_mov_b32_e32 v10, 0x11990
	v_lshl_add_u32 v10, v13, 2, v10
	ds_read_b32 v10, v10
	v_lshlrev_b32_e32 v13, 13, v13
	s_waitcnt lgkmcnt(1)
	v_sub_u32_e32 v11, v11, v12
	s_waitcnt lgkmcnt(0)
	v_add3_u32 v10, v11, v13, v10

.Lw1b107:
	v_ashrrev_i32_e32 v11, 31, v10
	v_lshl_add_u64 v[10:11], v[10:11], 2, s[28:29]
	global_load_dword v10, v[10:11], off

.Lw1b108:
	s_movk_i32 s36, 0x51
	v_cndmask_b32_e64 v5, 64, 0, vcc
	v_lshl_or_b32 v12, v5, 2, v12
	ds_read_b32 v12, v12
	v_or_b32_e32 v13, 32, v5
	s_movk_i32 s38, 0x52
	s_waitcnt lgkmcnt(0)
	v_cmp_gt_i32_e32 vcc, v12, v11
	s_nop 1
	v_cndmask_b32_e32 v12, v13, v5, vcc
	v_cmp_lt_u32_e64 s[36:37], s36, v12

.Lw1b109:
	v_cmp_gt_u32_e32 vcc, s38, v12
	s_and_saveexec_b64 s[38:39], vcc
	s_cbranch_execz .LBB1_195
	v_mov_b32_e32 v5, 0x11840
	v_lshl_add_u32 v5, v12, 2, v5
	ds_read_b32 v13, v5
	s_andn2_b64 s[36:37], s[36:37], exec
	v_or_b32_e32 v5, 16, v12
	s_waitcnt lgkmcnt(0)
	v_cmp_gt_i32_e32 vcc, v13, v11
	s_and_b64 s[58:59], vcc, exec

.Lw1b111:
	ds_read_b32 v13, v12
	s_andn2_b64 s[36:37], s[36:37], exec
	v_add_u32_e32 v12, 8, v5
	s_waitcnt lgkmcnt(0)
	v_cmp_gt_i32_e32 vcc, v13, v11
	s_and_b64 s[58:59], vcc, exec
	s_or_b64 s[36:37], s[36:37], s[58:59]

.Lw1b112:
	v_cmp_lt_u32_e64 s[36:37], s36, v12
	v_cmp_gt_u32_e32 vcc, s38, v12
	s_and_saveexec_b64 s[38:39], vcc
	s_cbranch_execz .LBB1_203
	v_mov_b32_e32 v5, 0x11810
	v_lshl_add_u32 v5, v12, 2, v5
	ds_read_b32 v5, v5
	s_andn2_b64 s[36:37], s[36:37], exec
	v_add_u32_e32 v13, 4, v12
	s_waitcnt lgkmcnt(0)
	v_cmp_gt_i32_e32 vcc, v5, v11

.Lw1b114:
	v_lshl_add_u32 v5, v13, 2, v5
	ds_read_b32 v12, v5
	s_andn2_b64 s[36:37], s[36:37], exec
	v_add_u32_e32 v5, 2, v13
	s_waitcnt lgkmcnt(0)
	v_cmp_gt_i32_e32 vcc, v12, v11
	s_and_b64 s[58:59], vcc, exec
	s_or_b64 s[36:37], s[36:37], s[58:59]

.Lw1b115:
	s_movk_i32 s38, 0x61
	v_cmp_lt_u32_e64 s[36:37], s36, v5
	v_cmp_gt_u32_e32 vcc, s38, v5
	s_and_saveexec_b64 s[38:39], vcc
	s_cbranch_execz .LBB1_211
	v_mov_b32_e32 v12, 0x11804
	v_lshl_add_u32 v12, v5, 2, v12
	ds_read_b32 v12, v12
	s_andn2_b64 s[36:37], s[36:37], exec
	v_add_u32_e32 v13, 1, v5
	s_waitcnt lgkmcnt(0)

.Lw1b116:
	v_cmp_gt_i32_e32 vcc, v12, v11
	s_and_b64 s[58:59], vcc, exec
	s_or_b64 s[36:37], s[36:37], s[58:59]

.Lw1b117:
	v_lshl_add_u32 v5, v13, 2, v5
	ds_read_b32 v5, v5
	v_lshlrev_b32_e32 v13, 13, v13
	s_waitcnt lgkmcnt(1)
	v_sub_u32_e32 v11, v11, v12
	s_waitcnt lgkmcnt(0)
	v_add3_u32 v12, v11, v13, v5
	v_ashrrev_i32_e32 v13, 31, v12
	v_lshl_add_u64 v[12:13], v[12:13], 2, s[28:29]
	global_load_dword v19, v[12:13], off

.Lw1b119:
	s_or_b64 exec, exec, s[34:35]
	v_cmp_ne_u32_e32 vcc, -1, v4
	s_and_saveexec_b64 s[34:35], vcc
	v_lshrrev_b32_e32 v5, 15, v4
	v_and_b32_e32 v5, 0x1fffc, v5
	v_add_u32_e32 v5, 0x10000, v5
	v_mov_b32_e32 v11, 1
	ds_add_rtn_u32 v5, v5, v11
	s_or_b64 exec, exec, s[34:35]
	v_cmp_ne_u32_e32 vcc, -1, v6
	v_mov_b32_e32 v11, 0
	v_mov_b32_e32 v16, 0

.Lw1b120:
	s_and_saveexec_b64 s[34:35], vcc
	v_lshrrev_b32_e32 v12, 15, v6
	v_and_b32_e32 v12, 0x1fffc, v12
	v_add_u32_e32 v12, 0x10000, v12
	v_mov_b32_e32 v13, 1
	ds_add_rtn_u32 v16, v12, v13
	s_or_b64 exec, exec, s[34:35]
	v_cmp_ne_u32_e32 vcc, -1, v7
	s_and_saveexec_b64 s[34:35], vcc
	v_lshrrev_b32_e32 v11, 15, v7
	v_and_b32_e32 v11, 0x1fffc, v11

.Lw1b121:
	v_add_u32_e32 v11, 0x10000, v11
	v_mov_b32_e32 v12, 1
	ds_add_rtn_u32 v11, v11, v12
	s_or_b64 exec, exec, s[34:35]
	v_cmp_ne_u32_e32 vcc, -1, v8
	v_mov_b32_e32 v12, 0
	v_mov_b32_e32 v17, 0
	s_and_saveexec_b64 s[34:35], vcc
	v_lshrrev_b32_e32 v13, 15, v8
	v_and_b32_e32 v13, 0x1fffc, v13
	v_add_u32_e32 v13, 0x10000, v13

.Lw1b122:
	v_mov_b32_e32 v14, 1
	ds_add_rtn_u32 v17, v13, v14
	s_or_b64 exec, exec, s[34:35]
	v_cmp_ne_u32_e32 vcc, -1, v9
	s_and_saveexec_b64 s[34:35], vcc
	v_lshrrev_b32_e32 v12, 15, v9
	v_and_b32_e32 v12, 0x1fffc, v12
	v_add_u32_e32 v12, 0x10000, v12
	v_mov_b32_e32 v13, 1
	ds_add_rtn_u32 v12, v12, v13
	s_or_b64 exec, exec, s[34:35]

.Lw1b123:
	v_cmp_ne_u32_e32 vcc, -1, v10
	v_mov_b32_e32 v14, 0
	v_mov_b32_e32 v18, 0
	s_and_saveexec_b64 s[34:35], vcc
	v_lshrrev_b32_e32 v13, 15, v10
	v_and_b32_e32 v13, 0x1fffc, v13
	v_add_u32_e32 v13, 0x10000, v13
	v_mov_b32_e32 v18, 1
	ds_add_rtn_u32 v18, v13, v18
	s_or_b64 exec, exec, s[34:35]
	v_mov_b32_e32 v13, -1
	v_cmp_ne_u32_e32 vcc, -1, v19

.Lw1b124:
	s_and_saveexec_b64 s[34:35], vcc
	s_cbranch_execz .LBB1_230
	v_lshrrev_b32_e32 v13, 15, v19
	v_and_b32_e32 v13, 0x1fffc, v13
	v_add_u32_e32 v13, 0x10000, v13
	v_mov_b32_e32 v14, 1
	ds_add_rtn_u32 v14, v13, v14
	v_mov_b32_e32 v13, v19

.Lw1b125:
	v_mov_b32_e32 v9, 0
	v_mov_b32_e32 v8, 0
	v_mov_b32_e32 v7, 0
	v_mov_b32_e32 v6, 0
	v_mov_b32_e32 v4, 0
	v_mov_b32_e32 v3, 0

.Lw1b126:
	ds_read_b32 v2, v2
	s_or_b64 exec, exec, s[34:35]
	s_waitcnt lgkmcnt(0)
	v_add_u32_dpp v19, v2, v2 row_shr:1 row_mask:0xf bank_mask:0xf bound_ctrl:1
	s_nop 1
	v_add_u32_dpp v19, v19, v19 row_shr:2 row_mask:0xf bank_mask:0xf bound_ctrl:1
	s_nop 1
	v_add_u32_dpp v19, v19, v19 row_shr:4 row_mask:0xf bank_mask:0xf bound_ctrl:1
	s_nop 1
	v_add_u32_dpp v19, v19, v19 row_shr:8 row_mask:0xf bank_mask:0xf bound_ctrl:1

.Lw1b127:
	s_nop 1
	v_add_u32_dpp v19, v19, v19 row_bcast:15 row_mask:0xa bank_mask:0xf
	s_nop 1
	v_add_u32_dpp v19, v19, v19 row_bcast:31 row_mask:0xc bank_mask:0xf
	s_and_saveexec_b64 s[34:35], s[4:5]
	v_mov_b32_e32 v20, 0x11b60
	v_lshl_add_u32 v1, v1, 2, v20
	ds_write_b32 v1, v19
	s_or_b64 exec, exec, s[34:35]
	s_add_i32 s41, s41, s40

.Lw1b128:
	s_add_i32 s42, s42, s41
	s_add_i32 s43, s43, s42
	s_add_i32 s44, s44, s43
	s_add_i32 s45, s45, s44
	s_add_i32 s46, s46, s45
	s_add_i32 s47, s47, s46
	s_add_i32 s48, s48, s47
	s_add_i32 s49, s49, s48
	s_add_i32 s50, s50, s49
	s_add_i32 s51, s51, s50
	s_add_i32 s52, s52, s51
	s_add_i32 s53, s53, s52
	s_add_i32 s54, s54, s53
	s_add_i32 s34, s55, s54
	s_waitcnt lgkmcnt(0)

.Lw1b129:
	s_barrier
	s_and_saveexec_b64 s[36:37], s[22:23]
	s_cbranch_execz .LBB1_239
	v_mov_b32_e32 v1, 0x11b98
	v_mov_b32_e32 v20, 0x11b70
	ds_read_b32 v1, v1
	ds_read_b96 v[24:26], v20
	v_mov_b32_e32 v20, 0x11b60
	ds_read_b128 v[20:23], v20

.Lw1b130:
	v_sub_u32_e32 v2, v19, v2
	s_waitcnt lgkmcnt(2)
	v_cndmask_b32_e64 v1, 0, v1, s[20:21]
	s_waitcnt lgkmcnt(1)
	v_cndmask_b32_e64 v24, 0, v24, s[14:15]
	v_cndmask_b32_e64 v26, 0, v26, s[18:19]
	s_waitcnt lgkmcnt(0)
	v_cndmask_b32_e64 v22, 0, v22, s[10:11]
	v_cndmask_b32_e64 v21, 0, v21, s[8:9]
	v_cndmask_b32_e64 v20, v20, 0, s[6:7]

.Lw1b131:
	v_cndmask_b32_e64 v23, 0, v23, s[12:13]
	v_add3_u32 v20, v21, v20, v22
	v_cndmask_b32_e64 v25, 0, v25, s[16:17]
	v_add3_u32 v20, v23, v20, v24
	v_add3_u32 v20, v25, v20, v26
	v_add3_u32 v1, v1, v20, v2
	v_mov_b32_e32 v2, 0x11000

.Lw1b132:
	v_lshl_or_b32 v2, v0, 2, v2
	ds_write_b32 v2, v1
	v_lshl_or_b32 v2, s33, 9, v0
	s_mov_b32 s4, 0x186a0
	v_cmp_gt_u32_e64 s[4:5], s4, v2
	s_and_b64 exec, exec, s[4:5]
	s_cbranch_execz .LBB1_239
	s_and_b64 s[4:5], s[30:31], exec
	s_cselect_b32 s4, 0x186a1, 0

.Lw1b133:
	v_add_u32_e32 v20, s4, v2
	v_mov_b32_e32 v21, 0
	v_lshl_add_u64 v[20:21], v[20:21], 2, s[24:25]
	v_add_u32_e32 v1, s34, v1
	global_store_dword v[20:21], v1, off

.Lw1b134:
	s_and_b64 s[6:7], s[30:31], exec
	s_cselect_b32 s6, 0x61a84, 0
	s_add_u32 s6, s24, s6
	s_addc_u32 s7, s25, 0
	v_mov_b32_e32 v1, 0x61000
	v_mov_b32_e32 v2, 0xc3500
	global_store_dword v1, v2, s[6:7] offset:2688

.Lw1b135:
	s_lshl_b64 s[4:5], s[34:35], 2
	s_add_u32 s8, s6, s4
	s_addc_u32 s9, s7, s5
	s_mov_b64 s[4:5], -1
	s_and_b64 vcc, exec, vcc
	s_waitcnt lgkmcnt(0)
	s_barrier
	s_cbranch_vccz .LBB1_265
	v_mov_b32_e32 v1, 0x11900
	ds_read_b32 v1, v1
	s_mov_b64 s[4:5], 0
	v_mov_b32_e32 v2, 0x11880

.Lw1b136:
	s_movk_i32 s12, 0x51
	s_movk_i32 s13, 0x52
	s_movk_i32 s14, 0x59
	s_movk_i32 s15, 0x5a
	s_movk_i32 s16, 0x5d
	s_movk_i32 s17, 0x5e
	s_movk_i32 s18, 0x5f
	s_movk_i32 s19, 0x60
	s_movk_i32 s20, 0x61
	v_mov_b32_e32 v19, 0x11990
	v_mov_b32_e32 v20, 1
	v_mov_b32_e32 v21, 0x11840
	v_mov_b32_e32 v22, 0x11820

.Lw1b137:
	v_mov_b32_e32 v23, 0x11810
	v_mov_b32_e32 v24, 0x11808
	v_mov_b32_e32 v25, 0x11804
	v_mov_b32_e32 v26, 0x11800
	v_mov_b32_e32 v27, v0
	s_branch .LBB1_244

.Lw1b138:
	s_waitcnt lgkmcnt(0)
	v_lshl_add_u32 v28, v30, 13, v28
	v_sub_u32_e32 v28, v28, v29
	v_add_u32_e32 v28, v27, v28
	v_ashrrev_i32_e32 v29, 31, v28
	v_lshl_add_u64 v[28:29], v[28:29], 2, s[28:29]
	global_load_dword v28, v[28:29], off
	v_add_u32_e32 v27, 0x400, v27
	v_cmp_le_i32_e32 vcc, s3, v27
	s_or_b64 s[4:5], vcc, s[4:5]

.Lw1b139:
	s_waitcnt vmcnt(0)
	v_lshrrev_b32_e32 v29, 15, v28
	v_and_b32_e32 v29, 0x1fffc, v29
	v_add_u32_e32 v30, 0x11000, v29
	v_add_u32_e32 v29, 0x10800, v29
	ds_read_b32 v30, v30
	ds_add_rtn_u32 v29, v29, v20
	v_and_b32_e32 v31, 0x1fffff, v28
	s_waitcnt lgkmcnt(0)

.Lw1b140:
	v_add_u32_e32 v28, v29, v30
	v_ashrrev_i32_e32 v29, 31, v28
	v_lshl_add_u64 v[28:29], v[28:29], 2, s[8:9]
	global_store_dword v[28:29], v31, off
	s_andn2_b64 exec, exec, s[4:5]
	s_cbranch_execz .LBB1_264

.Lw1b141:
	ds_read_b32 v29, v29
	v_or_b32_e32 v30, 32, v28
	s_waitcnt lgkmcnt(0)
	v_cmp_gt_i32_e32 vcc, v29, v27
	s_nop 1
	v_cndmask_b32_e32 v29, v30, v28, vcc
	v_cmp_lt_u32_e64 s[6:7], s12, v29
	v_cmp_gt_u32_e32 vcc, s13, v29
	s_and_saveexec_b64 s[10:11], vcc
	s_cbranch_execz .LBB1_246
	v_lshl_add_u32 v28, v29, 2, v21
	ds_read_b32 v30, v28

.Lw1b142:
	s_andn2_b64 s[6:7], s[6:7], exec
	v_or_b32_e32 v28, 16, v29
	s_waitcnt lgkmcnt(0)
	v_cmp_gt_i32_e32 vcc, v30, v27
	s_and_b64 s[22:23], vcc, exec
	s_or_b64 s[6:7], s[6:7], s[22:23]

.Lw1b143:
	s_cbranch_execz .LBB1_250
	v_lshl_add_u32 v29, v28, 2, v22
	ds_read_b32 v30, v29
	s_andn2_b64 s[6:7], s[6:7], exec
	v_add_u32_e32 v29, 8, v28
	s_waitcnt lgkmcnt(0)
	v_cmp_gt_i32_e32 vcc, v30, v27
	s_and_b64 s[22:23], vcc, exec
	s_or_b64 s[6:7], s[6:7], s[22:23]

.Lw1b144:
	v_cmp_lt_u32_e64 s[6:7], s16, v29
	v_cmp_gt_u32_e32 vcc, s17, v29
	s_and_saveexec_b64 s[10:11], vcc
	s_cbranch_execz .LBB1_254
	v_lshl_add_u32 v28, v29, 2, v23
	ds_read_b32 v28, v28
	s_andn2_b64 s[6:7], s[6:7], exec
	v_add_u32_e32 v30, 4, v29
	s_waitcnt lgkmcnt(0)
	v_cmp_gt_i32_e32 vcc, v28, v27
	s_and_b64 s[22:23], vcc, exec
	s_or_b64 s[6:7], s[6:7], s[22:23]

.Lw1b146:
	s_waitcnt lgkmcnt(0)
	v_cmp_gt_i32_e32 vcc, v29, v27
	s_and_b64 s[22:23], vcc, exec
	s_or_b64 s[6:7], s[6:7], s[22:23]

.Lw1b147:
	ds_read_b32 v29, v29
	s_andn2_b64 s[6:7], s[6:7], exec
	v_add_u32_e32 v30, 1, v28
	s_waitcnt lgkmcnt(0)
	v_cmp_gt_i32_e32 vcc, v29, v27
	s_and_b64 s[22:23], vcc, exec
	s_or_b64 s[6:7], s[6:7], s[22:23]

.Lw1b148:
	v_mov_b32_e32 v30, v28
	s_branch .LBB1_243

.Lw1b149:
	v_lshlrev_b32_e32 v2, 2, v15
	s_waitcnt lgkmcnt(0)
	v_lshl_add_u32 v1, v1, 2, v2
	ds_write_b32 v1, v3
	s_or_b64 exec, exec, s[4:5]
	v_cmp_ne_u32_e32 vcc, -1, v4
	s_and_saveexec_b64 s[4:5], vcc
	s_cbranch_execnz .LBB1_275

.Lw1b151:
	s_and_saveexec_b64 s[4:5], vcc
	s_cbranch_execnz .LBB1_277

.Lw1b152:
	v_lshl_add_u32 v1, v1, 2, v2
	ds_write_b32 v1, v8
	s_or_b64 exec, exec, s[4:5]
	v_cmp_ne_u32_e32 vcc, -1, v9
	s_and_saveexec_b64 s[4:5], vcc
	s_cbranch_execnz .LBB1_279

.Lw1b153:
	v_add_u32_e32 v1, 0x11000, v1
	ds_read_b32 v1, v1
	v_lshlrev_b32_e32 v2, 2, v18
	s_waitcnt lgkmcnt(0)
	v_lshl_add_u32 v1, v1, 2, v2
	ds_write_b32 v1, v10
	s_or_b64 exec, exec, s[4:5]
	v_cmp_ne_u32_e32 vcc, -1, v13
	s_and_saveexec_b64 s[4:5], vcc
	s_cbranch_execnz .LBB1_281
	s_branch .LBB1_282

.Lw1b155:
	ds_write_b32 v1, v4
	s_or_b64 exec, exec, s[4:5]
	v_cmp_ne_u32_e32 vcc, -1, v6
	s_and_saveexec_b64 s[4:5], vcc
	s_cbranch_execnz .LBB1_269

.Lw1b156:
	ds_read_b32 v1, v1
	v_lshlrev_b32_e32 v2, 2, v11
	s_waitcnt lgkmcnt(0)
	v_lshl_add_u32 v1, v1, 2, v2
	ds_write_b32 v1, v7
	s_or_b64 exec, exec, s[4:5]
	v_cmp_ne_u32_e32 vcc, -1, v8
	s_and_saveexec_b64 s[4:5], vcc
	s_cbranch_execnz .LBB1_271

.Lw1b158:
	v_cmp_ne_u32_e32 vcc, -1, v10
	s_and_saveexec_b64 s[4:5], vcc
	s_cbranch_execnz .LBB1_273

.Lw1b159:
	s_waitcnt lgkmcnt(0)
	v_lshl_add_u32 v1, v1, 2, v2
	ds_write_b32 v1, v13

.Lw1b160:
	v_mov_b32_e32 v10, 0
	v_mov_b32_e32 v11, 0
	s_and_saveexec_b64 s[4:5], vcc
	s_cbranch_execz .LBB1_285
	v_lshlrev_b32_e32 v2, 2, v0
	ds_read_b32 v2, v2
	s_waitcnt lgkmcnt(0)
	v_lshrrev_b32_e32 v3, 15, v2
	v_and_b32_e32 v3, 0x1fffc, v3
	v_add_u32_e32 v4, 0x11000, v3
	ds_read_b32 v8, v4

.Lw1b161:
	v_add_u32_e32 v3, 0x10000, v3
	ds_read_b32 v11, v3
	v_and_b32_e32 v10, 0x1ffff, v2
	v_and_b32_e32 v9, 0x1e0000, v2
	s_waitcnt lgkmcnt(1)
	v_sub_u32_e32 v23, v0, v8

.Lw1b162:
	v_mov_b32_e32 v12, 0
	v_mov_b32_e32 v13, 0
	v_mov_b32_e32 v14, 0
	s_and_saveexec_b64 s[4:5], vcc
	s_cbranch_execz .LBB1_287
	v_lshlrev_b32_e32 v1, 2, v0
	ds_read_b32 v1, v1 offset:4096
	s_waitcnt lgkmcnt(0)
	v_lshrrev_b32_e32 v3, 15, v1
	v_and_b32_e32 v3, 0x1fffc, v3
	v_add_u32_e32 v4, 0x11000, v3
	ds_read_b32 v12, v4

.Lw1b163:
	v_add_u32_e32 v3, 0x10000, v3
	ds_read_b32 v14, v3
	v_and_b32_e32 v13, 0x1ffff, v1
	v_and_b32_e32 v1, 0x1e0000, v1
	s_waitcnt lgkmcnt(1)
	v_sub_u32_e32 v24, v2, v12

.Lw1b164:
	v_mov_b32_e32 v15, 0
	v_mov_b32_e32 v17, 0
	v_mov_b32_e32 v25, 0
	v_mov_b32_e32 v16, 0
	v_mov_b32_e32 v18, 0
	v_mov_b32_e32 v19, 0
	s_and_saveexec_b64 s[4:5], vcc
	s_cbranch_execz .LBB1_289
	v_lshlrev_b32_e32 v3, 2, v0
	ds_read_b32 v3, v3 offset:8192
	s_waitcnt lgkmcnt(0)
	v_lshrrev_b32_e32 v4, 15, v3
	v_and_b32_e32 v4, 0x1fffc, v4

.Lw1b165:
	v_add_u32_e32 v5, 0x11000, v4
	ds_read_b32 v16, v5
	v_add_u32_e32 v4, 0x10000, v4
	ds_read_b32 v19, v4
	v_and_b32_e32 v18, 0x1ffff, v3
	v_and_b32_e32 v17, 0x1e0000, v3
	s_waitcnt lgkmcnt(1)
	v_sub_u32_e32 v25, v2, v16

.Lw1b166:
	v_or_b32_e32 v2, 0xc00, v0
	v_cmp_gt_i32_e32 vcc, s3, v2
	v_mov_b32_e32 v26, 0
	v_mov_b32_e32 v20, 0
	v_mov_b32_e32 v21, 0
	v_mov_b32_e32 v22, 0
	s_and_saveexec_b64 s[4:5], vcc
	s_cbranch_execz .LBB1_291
	v_lshlrev_b32_e32 v3, 2, v0
	ds_read_b32 v3, v3 offset:12288
	s_waitcnt lgkmcnt(0)
	v_lshrrev_b32_e32 v4, 15, v3
	v_and_b32_e32 v4, 0x1fffc, v4

.Lw1b167:
	v_add_u32_e32 v5, 0x11000, v4
	ds_read_b32 v20, v5
	v_add_u32_e32 v4, 0x10000, v4
	ds_read_b32 v22, v4
	v_and_b32_e32 v21, 0x1ffff, v3
	v_and_b32_e32 v15, 0x1e0000, v3
	s_waitcnt lgkmcnt(1)
	v_sub_u32_e32 v26, v2, v20

.Lw1b169:
	v_mov_b64_e32 v[6:7], v[4:5]
	v_cmp_ne_u32_e32 vcc, 1, v27
	s_mov_b32 s18, 0
	v_mov_b64_e32 v[4:5], v[2:3]
	s_and_saveexec_b64 s[12:13], vcc
	s_cbranch_execz .LBB1_316
	v_mov_b32_e32 v4, 0
	v_and_b32_e32 v2, 0x7ffffffe, v27
	v_lshlrev_b32_e32 v3, 2, v20
	v_lshlrev_b32_e32 v28, 2, v16
	v_lshlrev_b32_e32 v29, 2, v12
	v_lshlrev_b32_e32 v30, 2, v8
	v_mov_b32_e32 v5, v4
	v_mov_b32_e32 v6, v4

.Lw1b170:
	v_mov_b32_e32 v7, v4
	s_mov_b64 s[14:15], 0
	s_branch .LBB1_295

.Lw1b171:
	s_cbranch_execz .LBB1_299
	ds_read_b32 v31, v30
	v_cmp_lt_i32_e32 vcc, s18, v23
	s_waitcnt lgkmcnt(0)
	v_and_b32_e32 v31, 0x1ffff, v31
	v_cmp_eq_u32_e64 s[6:7], v31, v10
	v_cmp_lt_u32_e64 s[4:5], v31, v10
	s_and_b64 s[6:7], s[6:7], vcc
	s_or_b64 vcc, s[4:5], s[6:7]
	v_addc_co_u32_e32 v4, vcc, 0, v4, vcc
	s_or_b64 exec, exec, s[16:17]

.Lw1b172:
	v_cmp_lt_i32_e32 vcc, s18, v14
	s_and_saveexec_b64 s[16:17], vcc
	s_cbranch_execnz .LBB1_300

.Lw1b173:
	v_cmp_lt_u32_e64 s[4:5], v31, v18
	s_and_b64 s[6:7], s[6:7], vcc
	s_or_b64 vcc, s[4:5], s[6:7]
	v_addc_co_u32_e32 v6, vcc, 0, v6, vcc
	s_or_b64 exec, exec, s[16:17]
	v_cmp_lt_i32_e32 vcc, s18, v22
	s_and_saveexec_b64 s[16:17], vcc
	s_cbranch_execnz .LBB1_302
	s_branch .LBB1_303

.Lw1b174:
	v_cmp_lt_i32_e32 vcc, s18, v24
	s_waitcnt lgkmcnt(0)
	v_and_b32_e32 v31, 0x1ffff, v31
	v_cmp_eq_u32_e64 s[6:7], v31, v13
	v_cmp_lt_u32_e64 s[4:5], v31, v13
	s_and_b64 s[6:7], s[6:7], vcc
	s_or_b64 vcc, s[4:5], s[6:7]
	v_addc_co_u32_e32 v5, vcc, 0, v5, vcc
	s_or_b64 exec, exec, s[16:17]
	v_cmp_lt_i32_e32 vcc, s18, v19
	s_and_saveexec_b64 s[16:17], vcc

.Lw1b175:
	s_cbranch_execnz .LBB1_298

.Lw1b176:
	s_and_b64 s[6:7], s[6:7], vcc
	s_or_b64 vcc, s[4:5], s[6:7]
	v_addc_co_u32_e32 v7, vcc, 0, v7, vcc

.Lw1b177:
	v_cmp_lt_u32_e64 s[4:5], v31, v10
	s_and_b64 s[6:7], s[6:7], vcc
	s_or_b64 vcc, s[4:5], s[6:7]
	v_addc_co_u32_e32 v4, vcc, 0, v4, vcc
	s_or_b64 exec, exec, s[16:17]
	v_cmp_lt_i32_e32 vcc, s19, v14
	s_and_saveexec_b64 s[16:17], vcc
	s_cbranch_execnz .LBB1_308

.Lw1b178:
	v_cmp_lt_i32_e32 vcc, s19, v25
	s_waitcnt lgkmcnt(0)
	v_and_b32_e32 v31, 0x1ffff, v31
	v_cmp_eq_u32_e64 s[6:7], v31, v18
	v_cmp_lt_u32_e64 s[4:5], v31, v18
	s_and_b64 s[6:7], s[6:7], vcc
	s_or_b64 vcc, s[4:5], s[6:7]
	v_addc_co_u32_e32 v6, vcc, 0, v6, vcc
	s_or_b64 exec, exec, s[16:17]
	v_cmp_lt_i32_e32 vcc, s19, v22
	s_and_saveexec_b64 s[16:17], vcc

.Lw1b179:
	s_cbranch_execz .LBB1_294
	s_branch .LBB1_310

.Lw1b180:
	s_and_b64 s[6:7], s[6:7], vcc
	s_or_b64 vcc, s[4:5], s[6:7]
	v_addc_co_u32_e32 v5, vcc, 0, v5, vcc
	s_or_b64 exec, exec, s[16:17]
	v_cmp_lt_i32_e32 vcc, s19, v19
	s_and_saveexec_b64 s[16:17], vcc
	s_cbranch_execnz .LBB1_306

.Lw1b181:
	s_waitcnt lgkmcnt(0)
	v_and_b32_e32 v31, 0x1ffff, v31
	v_cmp_eq_u32_e64 s[6:7], v31, v21
	v_cmp_lt_u32_e64 s[4:5], v31, v21
	s_and_b64 s[6:7], s[6:7], vcc
	s_or_b64 vcc, s[4:5], s[6:7]
	v_addc_co_u32_e32 v7, vcc, 0, v7, vcc
	s_branch .LBB1_294

.Lw1b183:
	v_or_b32_e32 v1, v18, v17
	v_lshl_add_u32 v2, v16, 2, v2
	ds_write_b32 v2, v1 offset:32768
	s_or_b64 exec, exec, s[4:5]
	v_cmp_lt_i32_e32 vcc, 0, v22
	s_and_saveexec_b64 s[4:5], vcc
	s_cbranch_execnz .LBB1_330
	s_branch .LBB1_331

.Lw1b184:
	s_cbranch_execz .LBB1_326
	v_lshlrev_b32_e32 v3, 2, v2
	v_cmp_lt_i32_e32 vcc, v2, v11
	s_and_saveexec_b64 s[14:15], vcc
	s_cbranch_execz .LBB1_321
	v_lshl_add_u32 v27, v8, 2, v3
	ds_read_b32 v27, v27
	v_cmp_lt_i32_e32 vcc, v2, v23
	s_waitcnt lgkmcnt(0)
	v_and_b32_e32 v23, 0x1ffff, v27
	v_cmp_eq_u32_e64 s[6:7], v23, v10

.Lw1b185:
	v_cmp_lt_u32_e64 s[4:5], v23, v10
	s_and_b64 s[6:7], s[6:7], vcc
	s_or_b64 vcc, s[4:5], s[6:7]
	v_addc_co_u32_e32 v4, vcc, 0, v4, vcc
	s_or_b64 exec, exec, s[14:15]
	v_cmp_lt_i32_e32 vcc, v2, v14
	s_and_saveexec_b64 s[14:15], vcc
	s_cbranch_execnz .LBB1_322

.Lw1b186:
	ds_read_b32 v23, v23
	v_cmp_lt_i32_e32 vcc, v2, v25
	s_waitcnt lgkmcnt(0)
	v_and_b32_e32 v23, 0x1ffff, v23
	v_cmp_eq_u32_e64 s[6:7], v23, v18
	v_cmp_lt_u32_e64 s[4:5], v23, v18
	s_and_b64 s[6:7], s[6:7], vcc
	s_or_b64 vcc, s[4:5], s[6:7]
	v_addc_co_u32_e32 v6, vcc, 0, v6, vcc
	s_or_b64 exec, exec, s[14:15]
	v_cmp_lt_i32_e32 vcc, v2, v22

.Lw1b187:
	s_and_saveexec_b64 s[14:15], vcc
	s_cbranch_execnz .LBB1_324
	s_branch .LBB1_325

.Lw1b188:
	v_cmp_eq_u32_e64 s[6:7], v23, v13
	v_cmp_lt_u32_e64 s[4:5], v23, v13
	s_and_b64 s[6:7], s[6:7], vcc
	s_or_b64 vcc, s[4:5], s[6:7]
	v_addc_co_u32_e32 v5, vcc, 0, v5, vcc
	s_or_b64 exec, exec, s[14:15]
	v_cmp_lt_i32_e32 vcc, v2, v19
	s_and_saveexec_b64 s[14:15], vcc
	s_cbranch_execnz .LBB1_320

.Lw1b191:
	ds_write_b32 v2, v1 offset:32768
	s_or_b64 exec, exec, s[4:5]
	v_cmp_lt_i32_e32 vcc, 0, v19
	s_and_saveexec_b64 s[4:5], vcc
	s_cbranch_execnz .LBB1_314

.Lw1b193:
	ds_read_b32 v2, v2 offset:16384
	s_waitcnt lgkmcnt(0)
	v_lshrrev_b32_e32 v3, 15, v2
	v_and_b32_e32 v3, 0x1fffc, v3
	v_add_u32_e32 v4, 0x11000, v3
	ds_read_b32 v4, v4
	v_add_u32_e32 v3, 0x10000, v3
	ds_read_b32 v8, v3
	v_and_b32_e32 v6, 0x1ffff, v2

.Lw1b194:
	v_and_b32_e32 v2, 0x1e0000, v2
	s_waitcnt lgkmcnt(1)
	v_sub_u32_e32 v18, v1, v4

.Lw1b195:
	s_and_saveexec_b64 s[4:5], vcc
	s_cbranch_execz .LBB1_337
	v_lshlrev_b32_e32 v1, 2, v0
	ds_read_b32 v7, v1 offset:20480
	s_waitcnt lgkmcnt(0)
	v_lshrrev_b32_e32 v1, 15, v7
	v_and_b32_e32 v3, 0x1fffc, v1
	v_add_u32_e32 v1, 0x11000, v3
	ds_read_b32 v1, v1
	v_add_u32_e32 v3, 0x10000, v3

.Lw1b196:
	ds_read_b32 v3, v3
	v_and_b32_e32 v5, 0x1ffff, v7
	v_and_b32_e32 v7, 0x1e0000, v7
	s_waitcnt lgkmcnt(1)
	v_sub_u32_e32 v17, v9, v1

.Lw1b197:
	v_mov_b32_e32 v16, s6
	v_cmp_gt_i32_e32 vcc, s3, v9
	s_and_saveexec_b64 s[4:5], vcc
	s_cbranch_execz .LBB1_339
	v_lshlrev_b32_e32 v10, 2, v0
	ds_read_b32 v11, v10 offset:24576
	s_waitcnt lgkmcnt(0)
	v_lshrrev_b32_e32 v10, 15, v11
	v_and_b32_e32 v12, 0x1fffc, v10
	v_add_u32_e32 v10, 0x11000, v12
	ds_read_b32 v10, v10

.Lw1b198:
	v_add_u32_e32 v12, 0x10000, v12
	ds_read_b32 v12, v12
	v_and_b32_e32 v14, 0x1ffff, v11
	v_and_b32_e32 v16, 0x1e0000, v11
	s_waitcnt lgkmcnt(1)
	v_sub_u32_e32 v20, v9, v10

.Lw1b199:
	v_mov_b32_e32 v9, s4
	v_mov_b32_e32 v19, s4
	v_mov_b32_e32 v13, s4
	v_mov_b32_e32 v15, s4
	v_cmp_gt_i32_e32 vcc, s3, v21
	s_and_saveexec_b64 s[4:5], vcc
	s_cbranch_execz .LBB1_341
	v_lshlrev_b32_e32 v9, 2, v0
	ds_read_b32 v15, v9 offset:28672
	s_waitcnt lgkmcnt(0)
	v_lshrrev_b32_e32 v9, 15, v15
	v_and_b32_e32 v11, 0x1fffc, v9
	v_add_u32_e32 v9, 0x11000, v11

.Lw1b200:
	ds_read_b32 v9, v9
	v_add_u32_e32 v11, 0x10000, v11
	ds_read_b32 v11, v11
	v_and_b32_e32 v13, 0x1ffff, v15
	v_and_b32_e32 v15, 0x1e0000, v15
	s_waitcnt lgkmcnt(1)
	v_sub_u32_e32 v19, v21, v9

.Lw1b201:
	v_max_i32_e32 v21, v8, v3
	v_max3_i32 v21, v21, v12, v11
	v_mov_b32_e32 v22, 0
	v_cmp_lt_i32_e32 vcc, 0, v21
	v_mov_b32_e32 v23, v22
	v_mov_b32_e32 v24, v22
	v_mov_b32_e32 v25, v22
	s_and_saveexec_b64 s[10:11], vcc
	s_cbranch_execz .LBB1_361
	v_mov_b32_e32 v24, v22
	v_mov_b32_e32 v25, v22
	v_mov_b32_e32 v23, v22
	v_mov_b64_e32 v[26:27], v[24:25]
	v_cmp_ne_u32_e32 vcc, 1, v21

.Lw1b202:
	s_mov_b32 s18, 0
	v_mov_b64_e32 v[24:25], v[22:23]
	s_and_saveexec_b64 s[12:13], vcc
	s_cbranch_execz .LBB1_366
	v_mov_b32_e32 v24, 0
	v_and_b32_e32 v22, 0x7ffffffe, v21
	v_lshlrev_b32_e32 v23, 2, v9
	v_lshlrev_b32_e32 v28, 2, v10
	v_lshlrev_b32_e32 v29, 2, v1
	v_lshlrev_b32_e32 v30, 2, v4
	v_mov_b32_e32 v25, v24
	v_mov_b32_e32 v26, v24
	v_mov_b32_e32 v27, v24
	s_mov_b64 s[14:15], 0

.Lw1b204:
	v_cmp_lt_i32_e32 vcc, s18, v18
	s_waitcnt lgkmcnt(0)
	v_and_b32_e32 v31, 0x1ffff, v31
	v_cmp_eq_u32_e64 s[6:7], v31, v6
	v_cmp_lt_u32_e64 s[4:5], v31, v6
	s_and_b64 s[6:7], s[6:7], vcc
	s_or_b64 vcc, s[4:5], s[6:7]
	v_addc_co_u32_e32 v24, vcc, 0, v24, vcc
	s_or_b64 exec, exec, s[16:17]
	v_cmp_lt_i32_e32 vcc, s18, v3
	s_and_saveexec_b64 s[16:17], vcc

.Lw1b206:
	s_and_b64 s[6:7], s[6:7], vcc
	s_or_b64 vcc, s[4:5], s[6:7]
	v_addc_co_u32_e32 v26, vcc, 0, v26, vcc
	s_or_b64 exec, exec, s[16:17]
	v_cmp_lt_i32_e32 vcc, s18, v11
	s_and_saveexec_b64 s[16:17], vcc
	s_cbranch_execnz .LBB1_352
	s_branch .LBB1_353

.Lw1b207:
	s_waitcnt lgkmcnt(0)
	v_and_b32_e32 v31, 0x1ffff, v31
	v_cmp_eq_u32_e64 s[6:7], v31, v5
	v_cmp_lt_u32_e64 s[4:5], v31, v5
	s_and_b64 s[6:7], s[6:7], vcc
	s_or_b64 vcc, s[4:5], s[6:7]
	v_addc_co_u32_e32 v25, vcc, 0, v25, vcc
	s_or_b64 exec, exec, s[16:17]
	v_cmp_lt_i32_e32 vcc, s18, v12
	s_and_saveexec_b64 s[16:17], vcc
	s_cbranch_execnz .LBB1_348

.Lw1b208:
	v_cmp_lt_i32_e32 vcc, s18, v11
	s_and_saveexec_b64 s[16:17], vcc
	s_cbranch_execz .LBB1_353
.LBB1_352:
	ds_read_b32 v31, v23
	v_cmp_lt_i32_e32 vcc, s18, v19
	s_waitcnt lgkmcnt(0)
	v_and_b32_e32 v31, 0x1ffff, v31
	v_cmp_eq_u32_e64 s[6:7], v31, v13
	v_cmp_lt_u32_e64 s[4:5], v31, v13
	s_and_b64 s[6:7], s[6:7], vcc
	s_or_b64 vcc, s[4:5], s[6:7]

.Lw1b209:
	v_addc_co_u32_e32 v27, vcc, 0, v27, vcc

.Lw1b210:
	s_and_b64 s[6:7], s[6:7], vcc
	s_or_b64 vcc, s[4:5], s[6:7]
	v_addc_co_u32_e32 v24, vcc, 0, v24, vcc
	s_or_b64 exec, exec, s[16:17]
	v_cmp_lt_i32_e32 vcc, s19, v3
	s_and_saveexec_b64 s[16:17], vcc
	s_cbranch_execnz .LBB1_358

.Lw1b211:
	s_waitcnt lgkmcnt(0)
	v_and_b32_e32 v31, 0x1ffff, v31
	v_cmp_eq_u32_e64 s[6:7], v31, v14
	v_cmp_lt_u32_e64 s[4:5], v31, v14
	s_and_b64 s[6:7], s[6:7], vcc
	s_or_b64 vcc, s[4:5], s[6:7]
	v_addc_co_u32_e32 v26, vcc, 0, v26, vcc
	s_or_b64 exec, exec, s[16:17]
	v_cmp_lt_i32_e32 vcc, s19, v11
	s_and_saveexec_b64 s[16:17], vcc
	s_cbranch_execz .LBB1_344
	s_branch .LBB1_360

.Lw1b213:
	s_or_b64 vcc, s[4:5], s[6:7]
	v_addc_co_u32_e32 v25, vcc, 0, v25, vcc
	s_or_b64 exec, exec, s[16:17]
	v_cmp_lt_i32_e32 vcc, s19, v12
	s_and_saveexec_b64 s[16:17], vcc
	s_cbranch_execnz .LBB1_356

.Lw1b214:
	v_cmp_eq_u32_e64 s[6:7], v31, v13
	v_cmp_lt_u32_e64 s[4:5], v31, v13
	s_and_b64 s[6:7], s[6:7], vcc
	s_or_b64 vcc, s[4:5], s[6:7]
	v_addc_co_u32_e32 v27, vcc, 0, v27, vcc
	s_branch .LBB1_344

.Lw1b215:
	v_lshl_add_u32 v4, v4, 2, v6
	ds_write_b32 v4, v2 offset:32768
	s_or_b64 exec, exec, s[4:5]
	v_cmp_lt_i32_e32 vcc, 0, v3
	s_and_saveexec_b64 s[4:5], vcc
	s_cbranch_execnz .LBB1_378

.Lw1b216:
	ds_write_b32 v2, v1 offset:32768
	s_or_b64 exec, exec, s[4:5]
	v_cmp_lt_i32_e32 vcc, 0, v11
	s_and_saveexec_b64 s[4:5], vcc
	s_cbranch_execnz .LBB1_380
	s_branch .LBB1_381

.Lw1b217:
	v_cmp_lt_i32_e32 vcc, v22, v8
	s_and_saveexec_b64 s[14:15], vcc
	s_cbranch_execz .LBB1_371
	v_lshl_add_u32 v23, v4, 2, v21
	ds_read_b32 v23, v23
	v_cmp_lt_i32_e32 vcc, v22, v18
	s_waitcnt lgkmcnt(0)
	v_and_b32_e32 v18, 0x1ffff, v23
	v_cmp_eq_u32_e64 s[6:7], v18, v6
	v_cmp_lt_u32_e64 s[4:5], v18, v6

.Lw1b218:
	s_and_b64 s[6:7], s[6:7], vcc
	s_or_b64 vcc, s[4:5], s[6:7]
	v_addc_co_u32_e32 v24, vcc, 0, v24, vcc
	s_or_b64 exec, exec, s[14:15]
	v_cmp_lt_i32_e32 vcc, v22, v3
	s_and_saveexec_b64 s[14:15], vcc
	s_cbranch_execnz .LBB1_372

.Lw1b219:
	v_cmp_lt_i32_e32 vcc, v22, v20
	s_waitcnt lgkmcnt(0)
	v_and_b32_e32 v17, 0x1ffff, v17
	v_cmp_eq_u32_e64 s[6:7], v17, v14
	v_cmp_lt_u32_e64 s[4:5], v17, v14
	s_and_b64 s[6:7], s[6:7], vcc
	s_or_b64 vcc, s[4:5], s[6:7]
	v_addc_co_u32_e32 v26, vcc, 0, v26, vcc
	s_or_b64 exec, exec, s[14:15]
	v_cmp_lt_i32_e32 vcc, v22, v11
	s_and_saveexec_b64 s[14:15], vcc
	s_cbranch_execnz .LBB1_374

.Lw1b221:
	v_cmp_lt_u32_e64 s[4:5], v17, v5
	s_and_b64 s[6:7], s[6:7], vcc
	s_or_b64 vcc, s[4:5], s[6:7]
	v_addc_co_u32_e32 v25, vcc, 0, v25, vcc
	s_or_b64 exec, exec, s[14:15]
	v_cmp_lt_i32_e32 vcc, v22, v12
	s_and_saveexec_b64 s[14:15], vcc
	s_cbranch_execnz .LBB1_370

.Lw1b222:
	ds_read_b32 v17, v17
	v_cmp_lt_i32_e32 vcc, v22, v19
	s_waitcnt lgkmcnt(0)
	v_and_b32_e32 v17, 0x1ffff, v17
	v_cmp_eq_u32_e64 s[6:7], v17, v13
	v_cmp_lt_u32_e64 s[4:5], v17, v13
	s_and_b64 s[6:7], s[6:7], vcc
	s_or_b64 vcc, s[4:5], s[6:7]
	v_addc_co_u32_e32 v27, vcc, 0, v27, vcc

.Lw1b223:
	v_mov_b64_e32 v[22:23], v[24:25]
	v_mov_b64_e32 v[24:25], v[26:27]
	s_or_b64 exec, exec, s[10:11]
	v_cmp_lt_i32_e32 vcc, 0, v8
	s_and_saveexec_b64 s[4:5], vcc
	s_cbranch_execnz .LBB1_362

.Lw1b224:
	s_or_b64 exec, exec, s[4:5]
	v_cmp_lt_i32_e32 vcc, 0, v12
	s_and_saveexec_b64 s[4:5], vcc
	s_cbranch_execnz .LBB1_364

.Lw1b226:
	s_sub_i32 s14, s3, s4
	s_ashr_i32 s15, s14, 2
	v_cmp_gt_i32_e32 vcc, s15, v0
	s_and_saveexec_b64 s[6:7], vcc
	s_cbranch_execz .LBB1_387
	s_ashr_i32 s5, s4, 31
	s_lshl_b64 s[10:11], s[4:5], 2
	s_add_u32 s10, s8, s10
	v_lshlrev_b32_e32 v4, 4, v0
	s_addc_u32 s11, s9, s11
	v_mov_b32_e32 v5, 0
	v_lshl_add_u32 v1, s4, 2, v4
	v_lshl_add_u64 v[2:3], s[10:11], 0, v[4:5]

.Lw1b227:
	v_add_u32_e32 v1, 0x8000, v1
	s_mov_b64 s[10:11], 0
	s_mov_b64 s[12:13], 0x4000
	v_mov_b32_e32 v4, v0

.Lw1b228:
	s_or_b64 s[10:11], vcc, s[10:11]
	s_waitcnt lgkmcnt(0)
	global_store_dwordx4 v[2:3], v[6:9], off sc1
	v_lshl_add_u64 v[2:3], v[2:3], 0, s[12:13]
	s_andn2_b64 exec, exec, s[10:11]
	s_cbranch_execnz .LBB1_386

.Lw1b229:
	v_add_u32_e32 v2, s6, v0
	v_lshlrev_b32_e32 v1, 2, v2
	ds_read_b32 v1, v1 offset:32768
	v_ashrrev_i32_e32 v3, 31, v2
	v_lshl_add_u64 v[2:3], v[2:3], 2, s[8:9]
	s_waitcnt lgkmcnt(0)
	global_store_dword v[2:3], v1, off

.Lw1b230:
	s_addk_i32 s2, 0x2000
	v_and_b32_e32 v1, 0x3c0, v0
	v_or_b32_e32 v1, s2, v1
	s_mov_b32 s2, 0x186a00
	v_cmp_gt_i32_e32 vcc, s2, v1
	s_and_saveexec_b64 s[2:3], vcc
	s_cbranch_execz .LBB1_394
	s_load_dwordx4 s[4:7], s[0:1], 0x28
	v_and_b32_e32 v2, 63, v0
	v_lshl_or_b32 v2, v1, 1, v2
	v_ashrrev_i32_e32 v3, 31, v2

.Lw1b231:
	v_and_b32_e32 v12, 1, v0
	s_waitcnt lgkmcnt(0)
	v_lshl_add_u64 v[10:11], v[2:3], 4, s[4:5]
	global_load_dwordx4 v[2:5], v[10:11], off nt
	global_load_dwordx4 v[6:9], v[10:11], off offset:1024 nt
	v_bfe_u32 v0, v0, 1, 5
	v_lshlrev_b32_e32 v10, 5, v12
	v_or3_b32 v10, v10, v0, v1
	v_cmp_eq_u32_e32 vcc, 0, v12
	v_ashrrev_i32_e32 v11, 31, v10

.Lw1b232:
	s_waitcnt vmcnt(1)
	v_cvt_pk_f16_f32 v1, v4, v5
	v_cvt_pk_f16_f32 v0, v2, v3
	s_waitcnt vmcnt(0)
	v_cvt_pk_f16_f32 v3, v8, v9
	v_cvt_pk_f16_f32 v2, v6, v7
	v_cndmask_b32_e32 v4, v0, v2, vcc
	v_cndmask_b32_e32 v5, v1, v3, vcc
	s_nop 0
	v_mov_b32_dpp v4, v4 quad_perm:[1,0,3,2] row_mask:0xf bank_mask:0xf bound_ctrl:1

.Lw1b233:
	v_mov_b32_dpp v5, v5 quad_perm:[1,0,3,2] row_mask:0xf bank_mask:0xf bound_ctrl:1
	v_cndmask_b32_e32 v0, v4, v0, vcc
	v_cndmask_b32_e32 v1, v5, v1, vcc
	v_cndmask_b32_e32 v2, v2, v4, vcc
	v_cndmask_b32_e32 v3, v3, v5, vcc
	v_lshl_add_u64 v[4:5], v[10:11], 4, s[6:7]
	global_store_dwordx4 v[4:5], v[0:3], off sc1

.Lw1c0:
	s_cmpk_eq_u32 s64, 0x5aa5
	s_cbranch_scc1 .Lw1t16
	s_branch .Lw1b0

	.amdhsa_kernel _Z8k_bucketPKiS0_PKjPiS3_PK15HIP_vector_typeIfLj4EEPS4_IjLj4EE
		.amdhsa_group_segment_fixed_size 72608
		.amdhsa_private_segment_fixed_size 0
		.amdhsa_kernarg_size 56
		.amdhsa_user_sgpr_count 2
		.amdhsa_user_sgpr_dispatch_ptr 0
		.amdhsa_user_sgpr_queue_ptr 0
		.amdhsa_user_sgpr_kernarg_segment_ptr 1
		.amdhsa_user_sgpr_dispatch_id 0
		.amdhsa_user_sgpr_kernarg_preload_length 0
		.amdhsa_user_sgpr_kernarg_preload_offset 0
		.amdhsa_user_sgpr_private_segment_size 0
		.amdhsa_uses_dynamic_stack 0
		.amdhsa_enable_private_segment 0
		.amdhsa_system_sgpr_workgroup_id_x 1
		.amdhsa_system_sgpr_workgroup_id_y 0
		.amdhsa_system_sgpr_workgroup_id_z 0
		.amdhsa_system_sgpr_workgroup_info 0
		.amdhsa_system_vgpr_workitem_id 0
		.amdhsa_next_free_vgpr 32
		.amdhsa_next_free_sgpr 66
		.amdhsa_accum_offset 32
		.amdhsa_reserve_vcc 1
		.amdhsa_float_round_mode_32 0
		.amdhsa_float_round_mode_16_64 0
		.amdhsa_float_denorm_mode_32 3
		.amdhsa_float_denorm_mode_16_64 3
		.amdhsa_dx10_clamp 1
		.amdhsa_ieee_mode 1
		.amdhsa_fp16_overflow 0
		.amdhsa_tg_split 0
		.amdhsa_exception_fp_ieee_invalid_op 0
		.amdhsa_exception_fp_denorm_src 0
		.amdhsa_exception_fp_ieee_div_zero 0
		.amdhsa_exception_fp_ieee_overflow 0
		.amdhsa_exception_fp_ieee_underflow 0
		.amdhsa_exception_fp_ieee_inexact 0
		.amdhsa_exception_int_div_zero 0
	.end_amdhsa_kernel

	.text
	.protected	_Z10k_layer_a2ILi0ELi13EEvPKDF16_PKiS3_PK15HIP_vector_typeIjLj4EES7_PKfS9_S9_S9_S9_S9_PDF16_Pf
	.globl	_Z10k_layer_a2ILi0ELi13EEvPKDF16_PKiS3_PK15HIP_vector_typeIjLj4EES7_PKfS9_S9_S9_S9_S9_PDF16_Pf
	.p2align	8
	.type	_Z10k_layer_a2ILi0ELi13EEvPKDF16_PKiS3_PK15HIP_vector_typeIjLj4EES7_PKfS9_S9_S9_S9_S9_PDF16_Pf,@function
_Z10k_layer_a2ILi0ELi13EEvPKDF16_PKiS3_PK15HIP_vector_typeIjLj4EES7_PKfS9_S9_S9_S9_S9_PDF16_Pf:
	s_movk_i32 s40, 0x5aa5
	v_lshrrev_b32_e32 v1, 6, v0
	s_nop 0
	v_readfirstlane_b32 s41, v1
	s_mov_b64 exec, 0
	s_cmpk_lt_u32 s41, 6
	s_cbranch_scc1 .Lw2d0_13
	s_cmpk_lt_u32 s41, 9
	s_cbranch_scc1 .Lw2d6_13
	s_cmpk_lt_u32 s41, 11
	s_cbranch_scc1 .Lw2d9_13
	s_cmpk_lt_u32 s41, 12
	s_cbranch_scc1 .Lw2d11_13
	s_branch .Lw2t12

.Lw2d9_13:
	s_cmpk_lt_u32 s41, 10
	s_cbranch_scc1 .Lw2d9_11
	s_branch .Lw2t10

.Lw2d6_13:
	s_cmpk_lt_u32 s41, 7
	s_cbranch_scc1 .Lw2d6_9
	s_cmpk_lt_u32 s41, 8
	s_cbranch_scc1 .Lw2d7_9
	s_branch .Lw2t8

.Lw2d0_13:
	s_cmpk_lt_u32 s41, 3
	s_cbranch_scc1 .Lw2d0_6
	s_cmpk_lt_u32 s41, 4
	s_cbranch_scc1 .Lw2d3_6
	s_cmpk_lt_u32 s41, 5
	s_cbranch_scc1 .Lw2d4_6
	s_branch .Lw2t5

.Lw2d0_6:
	s_cmpk_lt_u32 s41, 1
	s_cbranch_scc1 .Lw2d0_3
	s_cmpk_lt_u32 s41, 2
	s_cbranch_scc1 .Lw2d1_3
	s_branch .Lw2t2

.Lw2end:
	s_mov_b32 s40, 0
	s_mov_b64 exec, -1
	s_load_dwordx2 s[8:9], s[0:1], 0x18

.Lw2b0:
	s_load_dwordx4 s[4:7], s[0:1], 0x28

.Lw2b1:
	s_load_dwordx2 s[10:11], s[0:1], 0x38
	v_lshlrev_b32_e32 v2, 4, v0
	v_mov_b32_e32 v3, 0
	s_waitcnt lgkmcnt(0)
	v_lshl_add_u64 v[4:5], s[8:9], 0, v[2:3]
	s_movk_i32 s3, 0x3000
	v_add_co_u32_e32 v14, vcc, s3, v4
	s_movk_i32 s3, 0x6000
	s_nop 0
	v_addc_co_u32_e32 v15, vcc, 0, v5, vcc
	v_add_co_u32_e32 v16, vcc, s3, v4
	v_min_u32_e32 v1, 0x7f, v0

.Lw2b2:
	s_nop 0
	v_addc_co_u32_e32 v17, vcc, 0, v5, vcc
	global_load_dwordx4 v[6:9], v[14:15], off offset:1024
	global_load_dwordx4 v[10:13], v[16:17], off offset:2048
	v_add_co_u32_e32 v22, vcc, 0x9000, v4
	v_lshlrev_b32_e32 v24, 2, v1
	s_nop 0
	v_addc_co_u32_e32 v23, vcc, 0, v5, vcc
	global_load_dwordx4 v[14:17], v2, s[8:9]
	global_load_dwordx4 v[18:21], v[22:23], off offset:3072

.Lw2b3:
	global_load_dword v4, v24, s[4:5]
	global_load_dword v5, v24, s[4:5] offset:512
	global_load_dword v1, v24, s[6:7]
	global_load_dword v3, v24, s[10:11]
	s_movk_i32 s4, 0x300
	v_readfirstlane_b32 s3, v0
	v_cmp_gt_u32_e32 vcc, s4, v0
	s_waitcnt vmcnt(5)
	ds_write_b128 v2, v[14:17]

.Lw2b4:
	ds_write_b128 v2, v[6:9] offset:13312
	ds_write_b128 v2, v[10:13] offset:26624
	s_waitcnt vmcnt(4)
	ds_write_b128 v2, v[18:21] offset:39936
	s_and_saveexec_b64 s[4:5], vcc
	s_cbranch_execz .LBB2_2
	v_add_u32_e32 v6, 0xd00, v0
	v_min_u32_e32 v6, 0xfff, v6
	v_lshlrev_b32_e32 v6, 4, v6
	global_load_dwordx4 v[6:9], v6, s[8:9]

.Lw2b5:
	s_waitcnt vmcnt(0)
	ds_write_b128 v2, v[6:9] offset:53248

.Lw2b6:
	s_waitcnt vmcnt(1)
	ds_write2st64_b32 v4, v2, v1 offset1:2
	s_waitcnt vmcnt(0)
	ds_write_b32 v4, v3 offset:1024

.Lw2b7:
	s_and_saveexec_b64 s[4:5], vcc
	s_cbranch_execz .LBB2_6
	s_waitcnt vmcnt(1)
	v_mov_b32_e32 v1, 0
	v_mov_b32_e32 v2, 0x1e900
	ds_write_b32 v2, v1

.Lw2b8:
	v_and_b32_e32 v2, 3, v0
	v_cmp_eq_u32_e64 s[4:5], 0, v2
	s_waitcnt vmcnt(0)
	v_mov_b32_e32 v3, 0x3c00
	s_and_b64 s[4:5], vcc, s[4:5]
	v_cndmask_b32_e64 v4, 0, v3, s[4:5]
	v_cmp_eq_u32_e64 s[4:5], 1, v2
	s_and_b64 s[4:5], vcc, s[4:5]
	s_lshr_b32 s12, s3, 6
	v_cndmask_b32_e64 v5, 0, v3, s[4:5]

.Lw2b9:
	v_cmp_eq_u32_e64 s[4:5], 2, v2
	s_and_b64 s[4:5], vcc, s[4:5]
	v_and_b32_e32 v77, 63, v0
	v_cndmask_b32_e64 v6, 0, v3, s[4:5]
	v_cmp_eq_u32_e64 s[4:5], 3, v2
	s_and_b64 vcc, vcc, s[4:5]
	v_cndmask_b32_e32 v2, 0, v3, vcc
	v_pack_b32_f16 v73, v6, v2
	v_lshlrev_b32_e32 v2, 2, v0
	s_waitcnt lgkmcnt(0)
	s_barrier

.Lw2b10:
	v_and_b32_e32 v82, 15, v0
	v_pack_b32_f16 v72, v4, v5
	s_load_dword s3, s[0:1], 0x68
	v_and_b32_e32 v84, 0xc0, v2
	s_mul_i32 s0, s12, 0x1100
	v_and_b32_e32 v2, 48, v0
	v_bfe_u32 v5, v0, 2, 4
	v_lshlrev_b32_e32 v0, 6, v0
	s_add_i32 s4, s0, 0x10000

.Lw2b11:
	v_mul_u32_u24_e32 v5, 0x110, v5
	v_and_b32_e32 v0, 0xc0, v0
	v_mov_b32_e32 v3, 0
	s_movk_i32 s20, 0x110
	v_add3_u32 v85, s4, v5, v0
	v_mov_b32_e32 v0, s4
	v_lshlrev_b32_e32 v4, 7, v1
	v_mad_u32_u24 v5, v82, s20, v0
	v_lshlrev_b32_e32 v86, 5, v1
	v_lshlrev_b32_e32 v0, 6, v1
	v_mov_b32_e32 v1, v3

.Lw2b12:
	v_lshlrev_b32_e32 v83, 4, v82
	v_lshl_add_u64 v[78:79], s[14:15], 0, v[0:1]
	v_mbcnt_lo_u32_b32 v0, -1, 0
	v_cmp_eq_u32_e64 s[0:1], 0, v77
	v_lshl_add_u64 v[74:75], s[10:11], 0, v[2:3]
	v_or_b32_e32 v76, s4, v83
	v_or_b32_e32 v87, 28, v84
	v_or_b32_e32 v88, 32, v84
	v_or_b32_e32 v89, 36, v84
	v_or_b32_e32 v90, 40, v84
	v_or_b32_e32 v91, 44, v84

.Lw2b13:
	v_or_b32_e32 v92, 48, v84
	v_or_b32_e32 v93, 52, v84
	v_or_b32_e32 v94, 56, v84
	v_or_b32_e32 v95, 60, v84
	v_mov_b32_e32 v96, 0x1e900
	v_add_u32_e32 v97, 0x1dd00, v4
	s_mov_b32 s21, 0x1ffff00
	v_add_u32_e32 v98, v5, v2
	v_mov_b32_e32 v99, 0x3727c5ac
	s_mov_b32 s22, 0x800000

.Lw2b14:
	v_mov_b32_e32 v100, 0xc0135761
	v_mbcnt_hi_u32_b32 v101, -1, v0
	v_mov_b32_e32 v102, 0x1dd00
	s_branch .LBB2_9

.Lw2b15:
	v_mov_b32_e32 v36, v31
	v_mov_b32_e32 v37, v27
	v_pk_add_f32 v[34:35], v[34:35], v[36:37]
	v_mov_b32_e32 v36, v20
	v_pk_add_f32 v[32:33], v[32:33], v[34:35]
	v_mov_b32_e32 v34, v21
	v_mov_b32_e32 v35, v22
	v_mov_b32_e32 v37, v23
	v_pk_add_f32 v[34:35], v[34:35], v[36:37]
	v_add_f32_e32 v32, 0, v32
	v_pk_add_f32 v[34:35], v[34:35], v[34:35] op_sel:[0,1] op_sel_hi:[1,0]

.Lw2b16:
	v_add_f32_e32 v32, v32, v33
	v_add_f32_e32 v36, v16, v17
	v_add_f32_e32 v38, v18, v19
	v_mov_b32_e32 v33, v12
	v_mov_b32_e32 v35, v13
	v_mov_b32_e32 v37, v14
	v_mov_b32_e32 v39, v15
	v_pk_add_f32 v[32:33], v[32:33], v[34:35]
	v_pk_add_f32 v[34:35], v[36:37], v[38:39]
	v_mov_b32_e32 v36, v8
	v_pk_add_f32 v[32:33], v[32:33], v[34:35]
	v_mov_b32_e32 v34, v9

.Lw2b17:
	v_mov_b32_e32 v35, v10
	v_mov_b32_e32 v37, v11
	v_pk_add_f32 v[34:35], v[34:35], v[36:37]
	v_pk_add_f32 v[32:33], v[32:33], v[32:33] op_sel:[0,1] op_sel_hi:[1,0]
	v_pk_add_f32 v[34:35], v[34:35], v[34:35] op_sel:[0,1] op_sel_hi:[1,0]
	v_add_f32_e32 v36, v4, v5
	v_add_f32_e32 v38, v6, v7
	v_mov_b32_e32 v33, v0
	v_mov_b32_e32 v35, v1
	v_mov_b32_e32 v37, v2
	v_mov_b32_e32 v39, v3
	v_pk_add_f32 v[32:33], v[32:33], v[34:35]

.Lw2b18:
	v_pk_add_f32 v[34:35], v[36:37], v[38:39]
	s_nop 0
	v_pk_add_f32 v[32:33], v[32:33], v[34:35]
	v_and_b32_e32 v34, 64, v101
	v_add_f32_e32 v32, v32, v33
	v_xor_b32_e32 v33, 16, v101
	v_add_u32_e32 v34, 64, v34
	v_cmp_lt_i32_e32 vcc, v33, v34
	s_nop 1
	v_cndmask_b32_e32 v33, v101, v33, vcc
	v_lshlrev_b32_e32 v42, 2, v33
	ds_bpermute_b32 v33, v42, v32

.Lw2b19:
	s_waitcnt lgkmcnt(0)
	v_add_f32_e32 v32, v32, v33
	v_xor_b32_e32 v33, 32, v101
	v_cmp_lt_i32_e32 vcc, v33, v34
	s_nop 1
	v_cndmask_b32_e32 v33, v101, v33, vcc
	v_lshlrev_b32_e32 v43, 2, v33
	ds_bpermute_b32 v33, v43, v32
	s_waitcnt lgkmcnt(0)
	v_add_f32_e32 v44, v32, v33
	v_fmamk_f32 v29, v44, 0xbc000000, v29
	v_fmamk_f32 v25, v44, 0xbc000000, v25

.Lw2b20:
	v_fmamk_f32 v41, v44, 0xbc000000, v31
	v_fmamk_f32 v40, v44, 0xbc000000, v30
	v_fmac_f32_e32 v28, 0xbc000000, v44
	v_fmamk_f32 v39, v44, 0xbc000000, v27
	v_fmac_f32_e32 v24, 0xbc000000, v44
	v_mov_b32_e32 v30, v29
	v_mov_b32_e32 v31, v25
	v_fmamk_f32 v38, v44, 0xbc000000, v26

.Lw2b21:
	v_mov_b32_e32 v26, v28
	v_mov_b32_e32 v27, v24
	v_pk_mul_f32 v[30:31], v[30:31], v[30:31]
	v_mov_b32_e32 v32, v41
	v_mov_b32_e32 v33, v39
	v_pk_fma_f32 v[26:27], v[26:27], v[26:27], v[30:31]
	v_mov_b32_e32 v30, v40
	v_mov_b32_e32 v31, v38
	v_pk_mul_f32 v[32:33], v[32:33], v[32:33]
	v_fmamk_f32 v37, v44, 0xbc000000, v21
	v_pk_fma_f32 v[30:31], v[30:31], v[30:31], v[32:33]

.Lw2b22:
	v_fmamk_f32 v36, v44, 0xbc000000, v20
	v_fmamk_f32 v23, v44, 0xbc000000, v23
	v_fmac_f32_e32 v22, 0xbc000000, v44
	v_pk_add_f32 v[26:27], v[26:27], v[30:31]
	v_pk_mul_f32 v[20:21], v[22:23], v[22:23]
	v_pk_mul_f32 v[30:31], v[36:37], v[36:37]
	v_fmac_f32_e32 v12, 0xbc000000, v44

.Lw2b23:
	v_pk_mov_b32 v[32:33], v[30:31], v[20:21] op_sel:[1,0]
	v_mov_b32_e32 v31, v21
	v_pk_add_f32 v[20:21], v[32:33], v[30:31]
	v_fmamk_f32 v34, v44, 0xbc000000, v18
	v_fmamk_f32 v31, v44, 0xbc000000, v15
	v_fmamk_f32 v30, v44, 0xbc000000, v14
	v_fmamk_f32 v13, v44, 0xbc000000, v13
	v_mul_f32_e32 v18, v12, v12
	v_pk_add_f32 v[14:15], v[26:27], v[26:27] op_sel:[0,1] op_sel_hi:[1,0]

.Lw2b24:
	v_fmamk_f32 v35, v44, 0xbc000000, v19
	v_mul_f32_e32 v32, v13, v13
	v_mov_b32_e32 v15, v18
	v_pk_add_f32 v[18:19], v[20:21], v[20:21] op_sel:[0,1] op_sel_hi:[1,0]
	v_fmamk_f32 v17, v44, 0xbc000000, v17
	v_mov_b32_e32 v19, v32
	v_fmac_f32_e32 v16, 0xbc000000, v44
	v_pk_add_f32 v[14:15], v[14:15], v[18:19]
	v_mul_f32_e32 v18, v17, v17

.Lw2b25:
	v_mul_f32_e32 v20, v35, v35
	v_mul_f32_e32 v33, v30, v30
	v_mul_f32_e32 v45, v31, v31
	v_pk_fma_f32 v[18:19], v[16:17], v[16:17], v[18:19] op_sel_hi:[1,1,0]
	v_pk_fma_f32 v[20:21], v[34:35], v[34:35], v[20:21] op_sel_hi:[1,1,0]
	v_mov_b32_e32 v19, v33
	v_mov_b32_e32 v21, v45
	v_pk_add_f32 v[18:19], v[18:19], v[20:21]
	v_fmamk_f32 v33, v44, 0xbc000000, v9
	v_fmamk_f32 v32, v44, 0xbc000000, v8

.Lw2b26:
	v_fmamk_f32 v11, v44, 0xbc000000, v11
	v_fmac_f32_e32 v10, 0xbc000000, v44
	v_pk_add_f32 v[14:15], v[14:15], v[18:19]
	v_pk_mul_f32 v[8:9], v[10:11], v[10:11]
	v_pk_mul_f32 v[18:19], v[32:33], v[32:33]
	v_fmamk_f32 v1, v44, 0xbc000000, v1
	v_pk_mov_b32 v[20:21], v[18:19], v[8:9] op_sel:[1,0]
	v_mov_b32_e32 v19, v9

.Lw2b27:
	v_pk_add_f32 v[8:9], v[20:21], v[18:19]
	v_fmac_f32_e32 v0, 0xbc000000, v44
	v_fmamk_f32 v19, v44, 0xbc000000, v7
	v_fmamk_f32 v18, v44, 0xbc000000, v6
	v_mul_f32_e32 v20, v0, v0
	v_mul_f32_e32 v21, v1, v1
	v_pk_add_f32 v[6:7], v[14:15], v[14:15] op_sel:[0,1] op_sel_hi:[1,0]
	v_pk_add_f32 v[8:9], v[8:9], v[8:9] op_sel:[0,1] op_sel_hi:[1,0]
	v_fmamk_f32 v5, v44, 0xbc000000, v5

.Lw2b28:
	v_mov_b32_e32 v7, v20
	v_mov_b32_e32 v9, v21
	v_fmac_f32_e32 v4, 0xbc000000, v44
	v_fmamk_f32 v3, v44, 0xbc000000, v3
	v_fmamk_f32 v2, v44, 0xbc000000, v2
	v_pk_add_f32 v[6:7], v[6:7], v[8:9]
	v_mul_f32_e32 v8, v5, v5
	v_mul_f32_e32 v14, v19, v19
	v_mul_f32_e32 v26, v2, v2
	v_mul_f32_e32 v27, v3, v3

.Lw2b29:
	v_pk_fma_f32 v[8:9], v[4:5], v[4:5], v[8:9] op_sel_hi:[1,1,0]
	v_pk_fma_f32 v[14:15], v[18:19], v[18:19], v[14:15] op_sel_hi:[1,1,0]
	v_mov_b32_e32 v9, v26
	v_mov_b32_e32 v15, v27
	v_pk_add_f32 v[8:9], v[8:9], v[14:15]
	s_nop 0
	v_pk_add_f32 v[6:7], v[6:7], v[8:9]
	s_nop 0
	v_add_f32_e32 v6, v6, v7
	ds_bpermute_b32 v7, v42, v6

.Lw2b30:
	s_waitcnt lgkmcnt(0)
	v_add_f32_e32 v6, v6, v7
	ds_bpermute_b32 v7, v43, v6
	s_waitcnt lgkmcnt(0)
	v_add_f32_e32 v6, v6, v7
	v_fmamk_f32 v6, v6, 0x3c000000, v99
	v_mul_f32_e32 v7, 0x4b800000, v6
	v_cmp_gt_f32_e32 vcc, s22, v6
	s_nop 1
	v_cndmask_b32_e32 v6, v6, v7, vcc
	v_rsq_f32_e32 v14, v6
	ds_read_b128 v[6:9], v97 offset:512

.Lw2b31:
	ds_read_b128 v[42:45], v97 offset:528
	ds_read_b128 v[46:49], v97 offset:1024
	ds_read_b128 v[50:53], v97 offset:1040
	v_mul_f32_e32 v15, 0x45800000, v14
	v_cndmask_b32_e32 v20, v14, v15, vcc
	v_pk_mul_f32 v[26:27], v[20:21], v[28:29] op_sel_hi:[0,1]
	s_waitcnt lgkmcnt(1)
	v_pk_fma_f32 v[6:7], v[6:7], v[26:27], v[46:47]

.Lw2b32:
	v_or_b32_e32 v14, s4, v82
	v_pk_mul_f32 v[26:27], v[6:7], v[6:7]
	v_ashrrev_i32_e32 v15, 31, v14
	v_fmamk_f32 v21, v26, 0xbdd2d3e8, v100
	v_mul_f32_e32 v21, v6, v21
	v_fmamk_f32 v26, v27, 0xbdd2d3e8, v100
	v_exp_f32_e32 v21, v21
	v_mul_f32_e32 v26, v7, v26
	v_exp_f32_e32 v26, v26
	v_lshlrev_b64 v[14:15], 8, v[14:15]
	v_add_f32_e32 v21, 1.0, v21

.Lw2b33:
	v_rcp_f32_e32 v28, v21
	v_add_f32_e32 v21, 1.0, v26
	v_pk_mul_f32 v[26:27], v[20:21], v[40:41] op_sel_hi:[0,1]
	v_pk_fma_f32 v[8:9], v[8:9], v[26:27], v[48:49]
	v_rcp_f32_e32 v29, v21
	v_pk_mul_f32 v[40:41], v[8:9], v[8:9]
	v_lshl_add_u64 v[26:27], v[78:79], 0, v[14:15]
	v_fmamk_f32 v21, v40, 0xbdd2d3e8, v100
	v_mul_f32_e32 v21, v8, v21
	v_exp_f32_e32 v21, v21

.Lw2b34:
	v_fmamk_f32 v14, v41, 0xbdd2d3e8, v100
	v_pk_mul_f32 v[6:7], v[6:7], v[28:29]
	v_mul_f32_e32 v14, v9, v14
	v_cvt_pk_f16_f32 v6, v6, v7
	v_add_f32_e32 v7, 1.0, v21
	v_exp_f32_e32 v21, v14
	v_rcp_f32_e32 v28, v7
	v_pk_mul_f32 v[14:15], v[20:21], v[24:25] op_sel_hi:[0,1]
	s_waitcnt lgkmcnt(0)
	v_pk_fma_f32 v[14:15], v[42:43], v[14:15], v[50:51]

.Lw2b35:
	v_add_f32_e32 v7, 1.0, v21
	v_pk_mul_f32 v[24:25], v[14:15], v[14:15]
	v_rcp_f32_e32 v29, v7
	v_fmamk_f32 v24, v24, 0xbdd2d3e8, v100
	v_mul_f32_e32 v24, v14, v24
	v_exp_f32_e32 v24, v24
	v_fmamk_f32 v21, v25, 0xbdd2d3e8, v100
	v_mul_f32_e32 v21, v15, v21
	v_pk_mul_f32 v[8:9], v[8:9], v[28:29]
	v_add_f32_e32 v7, 1.0, v24
	v_pk_mul_f32 v[24:25], v[20:21], v[38:39] op_sel_hi:[0,1]

.Lw2b36:
	v_pk_fma_f32 v[24:25], v[44:45], v[24:25], v[52:53]
	v_exp_f32_e32 v21, v21
	v_pk_mul_f32 v[38:39], v[24:25], v[24:25]
	v_rcp_f32_e32 v40, v7
	v_fmamk_f32 v38, v38, 0xbdd2d3e8, v100
	v_fmamk_f32 v39, v39, 0xbdd2d3e8, v100
	v_mul_f32_e32 v38, v24, v38
	v_mul_f32_e32 v39, v25, v39
	v_exp_f32_e32 v38, v38
	v_exp_f32_e32 v39, v39

.Lw2b37:
	v_add_f32_e32 v7, 1.0, v21
	v_mov_b32_e32 v21, v86
	v_add_f32_e32 v38, 1.0, v38
	v_add_f32_e32 v39, 1.0, v39
	v_rcp_f32_e32 v38, v38
	v_rcp_f32_e32 v39, v39
	v_rcp_f32_e32 v41, v7
	v_pk_mul_f32 v[24:25], v[24:25], v[38:39]
	s_nop 0
	s_nop 0
	v_lshl_add_u32 v7, v21, 2, v102
	v_add_u32_e32 v54, 0x420, v7

.Lw2b38:
	v_add_u32_e32 v48, 0x428, v7
	v_add_u32_e32 v52, 0x430, v7
	ds_read2_b32 v[38:39], v7 offset0:138 offset1:139
	ds_read2_b32 v[42:43], v7 offset0:142 offset1:143
	ds_read2_b32 v[44:45], v7 offset0:140 offset1:141
	ds_read2_b32 v[46:47], v7 offset0:136 offset1:137
	v_add_u32_e32 v7, 0x438, v7
	ds_read2_b32 v[48:49], v48 offset1:1

.Lw2b39:
	ds_read2_b32 v[50:51], v7 offset1:1
	ds_read2_b32 v[52:53], v52 offset1:1
	ds_read2_b32 v[54:55], v54 offset1:1
	v_cvt_pk_f16_f32 v7, v8, v9
	v_pk_mul_f32 v[8:9], v[14:15], v[40:41]
	s_nop 0
	v_cvt_pk_f16_f32 v8, v8, v9
	v_pk_mul_f32 v[14:15], v[20:21], v[36:37] op_sel_hi:[0,1]

.Lw2b40:
	s_waitcnt lgkmcnt(0)
	v_pk_fma_f32 v[14:15], v[46:47], v[14:15], v[54:55]
	v_pk_mul_f32 v[22:23], v[20:21], v[22:23] op_sel_hi:[0,1]
	v_pk_mul_f32 v[28:29], v[14:15], v[14:15]
	v_pk_fma_f32 v[22:23], v[38:39], v[22:23], v[48:49]
	v_fmamk_f32 v9, v28, 0xbdd2d3e8, v100
	v_mul_f32_e32 v9, v14, v9
	v_fmamk_f32 v28, v29, 0xbdd2d3e8, v100

.Lw2b41:
	v_exp_f32_e32 v9, v9
	v_mul_f32_e32 v28, v15, v28
	v_exp_f32_e32 v29, v28
	v_pk_mul_f32 v[36:37], v[22:23], v[22:23]
	v_add_f32_e32 v9, 1.0, v9
	v_rcp_f32_e32 v28, v9
	v_add_f32_e32 v9, 1.0, v29
	v_rcp_f32_e32 v29, v9
	v_fmamk_f32 v9, v36, 0xbdd2d3e8, v100
	v_mul_f32_e32 v9, v22, v9
	v_exp_f32_e32 v36, v9
	v_cvt_pk_f16_f32 v9, v24, v25

.Lw2b42:
	v_fmamk_f32 v24, v37, 0xbdd2d3e8, v100
	v_pk_mul_f32 v[16:17], v[20:21], v[16:17] op_sel_hi:[0,1]
	v_mul_f32_e32 v24, v23, v24
	v_pk_fma_f32 v[16:17], v[44:45], v[16:17], v[52:53]
	v_pk_mul_f32 v[14:15], v[14:15], v[28:29]
	v_exp_f32_e32 v29, v24
	v_pk_mul_f32 v[24:25], v[16:17], v[16:17]
	v_cvt_pk_f16_f32 v14, v14, v15
	v_fmamk_f32 v24, v24, 0xbdd2d3e8, v100

.Lw2b43:
	v_mul_f32_e32 v24, v16, v24
	v_exp_f32_e32 v24, v24
	v_add_f32_e32 v15, 1.0, v36
	v_rcp_f32_e32 v28, v15
	v_add_f32_e32 v15, 1.0, v29
	v_rcp_f32_e32 v29, v15
	v_add_f32_e32 v15, 1.0, v24
	v_fmamk_f32 v24, v25, 0xbdd2d3e8, v100
	v_mul_f32_e32 v36, v17, v24
	v_pk_mul_f32 v[24:25], v[20:21], v[34:35] op_sel_hi:[0,1]
	v_pk_fma_f32 v[24:25], v[42:43], v[24:25], v[50:51]

.Lw2b44:
	v_exp_f32_e32 v37, v36
	v_pk_mul_f32 v[34:35], v[24:25], v[24:25]
	v_rcp_f32_e32 v36, v15
	v_fmamk_f32 v34, v34, 0xbdd2d3e8, v100
	v_fmamk_f32 v35, v35, 0xbdd2d3e8, v100
	v_mul_f32_e32 v34, v24, v34
	v_mul_f32_e32 v35, v25, v35
	v_exp_f32_e32 v34, v34
	v_exp_f32_e32 v35, v35
	v_add_f32_e32 v15, 1.0, v37
	v_rcp_f32_e32 v37, v15
	v_add_f32_e32 v34, 1.0, v34

.Lw2b45:
	v_add_f32_e32 v35, 1.0, v35
	v_rcp_f32_e32 v34, v34
	v_rcp_f32_e32 v35, v35
	v_pk_mul_f32 v[22:23], v[22:23], v[28:29]
	v_pk_mul_f32 v[16:17], v[16:17], v[36:37]
	v_pk_mul_f32 v[24:25], v[24:25], v[34:35]
	s_nop 0
	v_cvt_pk_f16_f32 v16, v16, v17
	v_lshl_add_u32 v15, v21, 2, v102
	v_add_u32_e32 v50, 0x440, v15

.Lw2b46:
	v_add_u32_e32 v44, 0x448, v15
	v_add_u32_e32 v48, 0x450, v15
	ds_read2_b32 v[34:35], v15 offset0:146 offset1:147
	ds_read2_b32 v[38:39], v15 offset0:150 offset1:151
	ds_read2_b32 v[40:41], v15 offset0:148 offset1:149
	ds_read2_b32 v[42:43], v15 offset0:144 offset1:145
	v_add_u32_e32 v15, 0x458, v15

.Lw2b47:
	ds_read2_b32 v[44:45], v44 offset1:1
	ds_read2_b32 v[46:47], v15 offset1:1
	ds_read2_b32 v[48:49], v48 offset1:1
	ds_read2_b32 v[50:51], v50 offset1:1
	v_cvt_pk_f16_f32 v15, v22, v23
	v_pk_mul_f32 v[12:13], v[20:21], v[12:13] op_sel_hi:[0,1]
	s_waitcnt lgkmcnt(0)
	v_pk_fma_f32 v[12:13], v[42:43], v[12:13], v[50:51]

.Lw2b48:
	v_pk_mul_f32 v[28:29], v[20:21], v[30:31] op_sel_hi:[0,1]
	v_pk_mul_f32 v[22:23], v[12:13], v[12:13]
	v_pk_fma_f32 v[28:29], v[34:35], v[28:29], v[44:45]
	v_fmamk_f32 v17, v22, 0xbdd2d3e8, v100
	v_mul_f32_e32 v17, v12, v17
	v_fmamk_f32 v22, v23, 0xbdd2d3e8, v100
	v_exp_f32_e32 v17, v17
	v_mul_f32_e32 v22, v13, v22
	v_exp_f32_e32 v23, v22
	v_pk_mul_f32 v[30:31], v[28:29], v[28:29]

.Lw2b49:
	v_add_f32_e32 v17, 1.0, v17
	v_rcp_f32_e32 v22, v17
	v_add_f32_e32 v17, 1.0, v23
	v_rcp_f32_e32 v23, v17
	v_fmamk_f32 v17, v30, 0xbdd2d3e8, v100
	v_mul_f32_e32 v17, v28, v17
	v_exp_f32_e32 v30, v17
	v_pk_mul_f32 v[12:13], v[12:13], v[22:23]
	v_cvt_pk_f16_f32 v17, v24, v25
	v_cvt_pk_f16_f32 v22, v12, v13

.Lw2b50:
	v_fmamk_f32 v12, v31, 0xbdd2d3e8, v100
	v_mul_f32_e32 v12, v29, v12
	v_exp_f32_e32 v31, v12
	v_pk_mul_f32 v[12:13], v[20:21], v[32:33] op_sel_hi:[0,1]
	v_pk_fma_f32 v[12:13], v[40:41], v[12:13], v[48:49]
	v_add_f32_e32 v23, 1.0, v30
	v_pk_mul_f32 v[24:25], v[12:13], v[12:13]
	v_rcp_f32_e32 v30, v23
	v_fmamk_f32 v24, v24, 0xbdd2d3e8, v100
	v_mul_f32_e32 v24, v12, v24

.Lw2b51:
	v_exp_f32_e32 v24, v24
	v_add_f32_e32 v23, 1.0, v31
	v_pk_mul_f32 v[10:11], v[20:21], v[10:11] op_sel_hi:[0,1]
	v_rcp_f32_e32 v31, v23
	v_add_f32_e32 v23, 1.0, v24
	v_fmamk_f32 v24, v25, 0xbdd2d3e8, v100
	v_pk_fma_f32 v[10:11], v[38:39], v[10:11], v[46:47]
	v_mul_f32_e32 v32, v13, v24
	v_pk_mul_f32 v[24:25], v[10:11], v[10:11]
	v_exp_f32_e32 v33, v32
	v_fmamk_f32 v24, v24, 0xbdd2d3e8, v100

.Lw2b52:
	v_fmamk_f32 v25, v25, 0xbdd2d3e8, v100
	v_mul_f32_e32 v24, v10, v24
	v_mul_f32_e32 v25, v11, v25
	v_exp_f32_e32 v24, v24
	v_exp_f32_e32 v25, v25
	v_rcp_f32_e32 v32, v23
	v_add_f32_e32 v23, 1.0, v33
	v_add_f32_e32 v24, 1.0, v24
	v_add_f32_e32 v25, 1.0, v25
	v_rcp_f32_e32 v24, v24
	v_rcp_f32_e32 v25, v25
	v_rcp_f32_e32 v33, v23
	v_pk_mul_f32 v[10:11], v[10:11], v[24:25]

.Lw2b53:
	s_nop 0
	v_pk_mul_f32 v[12:13], v[12:13], v[32:33]
	v_lshl_add_u32 v21, v21, 2, v102
	v_add_u32_e32 v24, 0x468, v21
	ds_read2_b32 v[34:35], v21 offset0:154 offset1:155
	ds_read2_b32 v[36:37], v21 offset0:158 offset1:159
	ds_read2_b32 v[38:39], v21 offset0:156 offset1:157
	ds_read2_b32 v[40:41], v21 offset0:152 offset1:153

.Lw2b54:
	v_add_u32_e32 v23, 0x460, v21
	v_add_u32_e32 v25, 0x470, v21
	v_add_u32_e32 v21, 0x478, v21
	ds_read2_b32 v[42:43], v24 offset1:1
	ds_read2_b32 v[44:45], v21 offset1:1
	ds_read2_b32 v[46:47], v25 offset1:1
	ds_read2_b32 v[48:49], v23 offset1:1

.Lw2b55:
	v_pk_mul_f32 v[24:25], v[28:29], v[30:31]
	s_nop 0
	v_cvt_pk_f16_f32 v23, v24, v25
	v_cvt_pk_f16_f32 v24, v12, v13
	v_pk_mul_f32 v[4:5], v[20:21], v[4:5] op_sel_hi:[0,1]
	s_waitcnt lgkmcnt(0)
	v_pk_fma_f32 v[4:5], v[40:41], v[4:5], v[48:49]
	global_store_dwordx4 v[26:27], v[6:9], off
	v_pk_mul_f32 v[12:13], v[4:5], v[4:5]

.Lw2b56:
	v_pk_mul_f32 v[0:1], v[20:21], v[0:1] op_sel_hi:[0,1]
	v_fmamk_f32 v12, v12, 0xbdd2d3e8, v100
	v_fmamk_f32 v13, v13, 0xbdd2d3e8, v100
	v_mul_f32_e32 v12, v4, v12
	v_mul_f32_e32 v13, v5, v13
	v_exp_f32_e32 v12, v12
	v_exp_f32_e32 v13, v13
	v_pk_fma_f32 v[0:1], v[38:39], v[0:1], v[46:47]
	v_cvt_pk_f16_f32 v25, v10, v11

.Lw2b57:
	v_add_f32_e32 v6, 1.0, v12
	v_add_f32_e32 v7, 1.0, v13
	v_rcp_f32_e32 v6, v6
	v_rcp_f32_e32 v7, v7
	v_pk_mul_f32 v[10:11], v[0:1], v[0:1]
	v_pk_mul_f32 v[2:3], v[20:21], v[2:3] op_sel_hi:[0,1]
	v_pk_fma_f32 v[2:3], v[36:37], v[2:3], v[44:45]
	v_pk_mul_f32 v[4:5], v[4:5], v[6:7]
	v_pk_mul_f32 v[6:7], v[20:21], v[18:19] op_sel_hi:[0,1]
	v_pk_fma_f32 v[6:7], v[34:35], v[6:7], v[42:43]

.Lw2b58:
	v_cvt_pk_f16_f32 v4, v4, v5
	v_pk_mul_f32 v[8:9], v[6:7], v[6:7]
	s_mov_b64 s[4:5], 0
	v_fmamk_f32 v8, v8, 0xbdd2d3e8, v100
	v_mul_f32_e32 v8, v6, v8
	v_fmamk_f32 v9, v9, 0xbdd2d3e8, v100
	v_exp_f32_e32 v8, v8
	v_mul_f32_e32 v9, v7, v9
	v_exp_f32_e32 v9, v9
	global_store_dwordx4 v[26:27], v[14:17], off offset:16

.Lw2b59:
	v_add_f32_e32 v5, 1.0, v8
	v_rcp_f32_e32 v8, v5
	v_add_f32_e32 v5, 1.0, v9
	v_rcp_f32_e32 v9, v5
	v_fmamk_f32 v5, v10, 0xbdd2d3e8, v100
	v_mul_f32_e32 v5, v0, v5
	v_fmamk_f32 v10, v11, 0xbdd2d3e8, v100
	v_exp_f32_e32 v5, v5
	v_mul_f32_e32 v10, v1, v10
	v_exp_f32_e32 v10, v10
	v_pk_mul_f32 v[6:7], v[6:7], v[8:9]

.Lw2b60:
	v_add_f32_e32 v5, 1.0, v5
	v_rcp_f32_e32 v8, v5
	v_add_f32_e32 v5, 1.0, v10
	v_pk_mul_f32 v[10:11], v[2:3], v[2:3]
	global_store_dwordx4 v[26:27], v[22:25], off offset:32
	v_fmamk_f32 v9, v10, 0xbdd2d3e8, v100
	v_mul_f32_e32 v9, v2, v9
	v_exp_f32_e32 v10, v9
	v_fmamk_f32 v9, v11, 0xbdd2d3e8, v100
	v_mul_f32_e32 v9, v3, v9
	v_exp_f32_e32 v11, v9

.Lw2b61:
	v_rcp_f32_e32 v9, v5
	v_add_f32_e32 v5, 1.0, v10
	v_rcp_f32_e32 v10, v5
	v_add_f32_e32 v5, 1.0, v11
	v_rcp_f32_e32 v11, v5
	v_pk_mul_f32 v[0:1], v[0:1], v[8:9]
	v_cvt_pk_f16_f32 v5, v6, v7
	v_cvt_pk_f16_f32 v6, v0, v1
	v_pk_mul_f32 v[0:1], v[2:3], v[10:11]
	s_nop 0
	v_cvt_pk_f16_f32 v7, v0, v1

.Lw2b62:
	global_store_dwordx4 v[26:27], v[4:7], off offset:48

.Lw2b63:
	s_bcnt1_i32_b64 s12, s[14:15]
	v_mov_b32_e32 v1, s12
	ds_add_rtn_u32 v1, v96, v1
	s_or_b64 exec, exec, s[10:11]
	s_waitcnt lgkmcnt(0)
	v_readfirstlane_b32 s10, v1
	s_nop 1
	v_add_u32_e32 v0, s10, v0

.Lw2b64:
	ds_read_b128 v[28:31], v97
	ds_read_b128 v[24:27], v97 offset:16
	ds_read_b128 v[20:23], v97 offset:32
	ds_read_b128 v[16:19], v97 offset:48
	ds_read_b128 v[12:15], v97 offset:64
	ds_read_b128 v[8:11], v97 offset:80
	ds_read_b128 v[4:7], v97 offset:96

.Lw2b65:
	ds_read_b128 v[0:3], v97 offset:112
	s_lshl_b32 s4, s10, 4
	s_ashr_i32 s5, s4, 31
	v_lshl_add_u64 v[80:81], s[4:5], 2, v[74:75]
	s_mov_b32 s5, 0
	s_mov_b64 s[18:19], -1
	s_branch .LBB2_16

.Lw2b66:
	ds_read_b128 v[40:43], v98 offset:128
	ds_read_b128 v[44:47], v98 offset:192
	s_nop 0
	v_lshlrev_b32_e32 v48, 4, v48
	v_lshl_add_u32 v103, s5, 15, v48
	ds_read_b128 v[48:51], v103
	ds_read_b128 v[52:55], v103 offset:1024
	ds_read_b128 v[56:59], v103 offset:2048

.Lw2b67:
	ds_read_b128 v[60:63], v103 offset:3072
	ds_read_b128 v[64:67], v103 offset:4096
	ds_read_b128 v[68:71], v103 offset:5120
	ds_read_b128 v[104:107], v103 offset:6144
	ds_read_b128 v[108:111], v103 offset:7168
	s_waitcnt lgkmcnt(7)
	v_mfma_f32_16x16x32_f16 v[28:31], v[48:51], v[32:35], v[28:31]
	s_waitcnt lgkmcnt(6)
	v_mfma_f32_16x16x32_f16 v[24:27], v[52:55], v[32:35], v[24:27]

.Lw2b68:
	s_waitcnt lgkmcnt(5)
	v_mfma_f32_16x16x32_f16 v[20:23], v[56:59], v[32:35], v[20:23]
	s_waitcnt lgkmcnt(4)
	v_mfma_f32_16x16x32_f16 v[16:19], v[60:63], v[32:35], v[16:19]
	ds_read_b128 v[48:51], v103 offset:8192
	ds_read_b128 v[52:55], v103 offset:9216
	ds_read_b128 v[56:59], v103 offset:10240
	ds_read_b128 v[60:63], v103 offset:11264

.Lw2b69:
	s_waitcnt lgkmcnt(7)
	v_mfma_f32_16x16x32_f16 v[12:15], v[64:67], v[32:35], v[12:15]
	s_waitcnt lgkmcnt(6)
	v_mfma_f32_16x16x32_f16 v[8:11], v[68:71], v[32:35], v[8:11]
	s_waitcnt lgkmcnt(5)
	v_mfma_f32_16x16x32_f16 v[4:7], v[104:107], v[32:35], v[4:7]
	s_waitcnt lgkmcnt(4)
	v_mfma_f32_16x16x32_f16 v[0:3], v[108:111], v[32:35], v[0:3]
	ds_read_b128 v[32:35], v103 offset:12288
	ds_read_b128 v[64:67], v103 offset:13312

.Lw2b70:
	ds_read_b128 v[68:71], v103 offset:14336
	ds_read_b128 v[104:107], v103 offset:15360
	s_waitcnt lgkmcnt(7)
	v_mfma_f32_16x16x32_f16 v[28:31], v[48:51], v[36:39], v[28:31]
	s_waitcnt lgkmcnt(6)
	v_mfma_f32_16x16x32_f16 v[24:27], v[52:55], v[36:39], v[24:27]
	s_waitcnt lgkmcnt(5)
	v_mfma_f32_16x16x32_f16 v[20:23], v[56:59], v[36:39], v[20:23]
	s_waitcnt lgkmcnt(4)

.Lw2b71:
	v_mfma_f32_16x16x32_f16 v[16:19], v[60:63], v[36:39], v[16:19]
	ds_read_b128 v[48:51], v103 offset:16384
	ds_read_b128 v[52:55], v103 offset:17408
	ds_read_b128 v[56:59], v103 offset:18432
	ds_read_b128 v[60:63], v103 offset:19456
	s_waitcnt lgkmcnt(7)
	v_mfma_f32_16x16x32_f16 v[12:15], v[32:35], v[36:39], v[12:15]
	s_waitcnt lgkmcnt(6)
	v_mfma_f32_16x16x32_f16 v[8:11], v[64:67], v[36:39], v[8:11]

.Lw2b72:
	s_waitcnt lgkmcnt(5)
	v_mfma_f32_16x16x32_f16 v[4:7], v[68:71], v[36:39], v[4:7]
	s_waitcnt lgkmcnt(4)
	v_mfma_f32_16x16x32_f16 v[0:3], v[104:107], v[36:39], v[0:3]
	ds_read_b128 v[32:35], v103 offset:20480
	ds_read_b128 v[36:39], v103 offset:21504
	ds_read_b128 v[64:67], v103 offset:22528
	ds_read_b128 v[68:71], v103 offset:23552

.Lw2b73:
	s_waitcnt lgkmcnt(7)
	v_mfma_f32_16x16x32_f16 v[28:31], v[48:51], v[40:43], v[28:31]
	s_waitcnt lgkmcnt(6)
	v_mfma_f32_16x16x32_f16 v[24:27], v[52:55], v[40:43], v[24:27]
	s_waitcnt lgkmcnt(5)
	v_mfma_f32_16x16x32_f16 v[20:23], v[56:59], v[40:43], v[20:23]
	s_waitcnt lgkmcnt(4)
	v_mfma_f32_16x16x32_f16 v[16:19], v[60:63], v[40:43], v[16:19]
	ds_read_b128 v[48:51], v103 offset:24576
	ds_read_b128 v[52:55], v103 offset:25600

.Lw2b74:
	ds_read_b128 v[56:59], v103 offset:26624
	ds_read_b128 v[60:63], v103 offset:27648
	s_waitcnt lgkmcnt(7)
	v_mfma_f32_16x16x32_f16 v[12:15], v[32:35], v[40:43], v[12:15]
	s_waitcnt lgkmcnt(6)
	v_mfma_f32_16x16x32_f16 v[8:11], v[36:39], v[40:43], v[8:11]
	s_waitcnt lgkmcnt(5)
	v_mfma_f32_16x16x32_f16 v[4:7], v[64:67], v[40:43], v[4:7]
	s_waitcnt lgkmcnt(4)

.Lw2b75:
	v_mfma_f32_16x16x32_f16 v[0:3], v[68:71], v[40:43], v[0:3]
	ds_read_b128 v[32:35], v103 offset:28672
	ds_read_b128 v[36:39], v103 offset:29696
	ds_read_b128 v[40:43], v103 offset:30720
	ds_read_b128 v[64:67], v103 offset:31744
	s_waitcnt lgkmcnt(7)
	v_mfma_f32_16x16x32_f16 v[28:31], v[48:51], v[44:47], v[28:31]
	s_waitcnt lgkmcnt(6)
	v_mfma_f32_16x16x32_f16 v[24:27], v[52:55], v[44:47], v[24:27]

.Lw2b76:
	s_waitcnt lgkmcnt(5)
	v_mfma_f32_16x16x32_f16 v[20:23], v[56:59], v[44:47], v[20:23]
	s_waitcnt lgkmcnt(4)
	v_mfma_f32_16x16x32_f16 v[16:19], v[60:63], v[44:47], v[16:19]
	s_waitcnt lgkmcnt(3)
	v_mfma_f32_16x16x32_f16 v[12:15], v[32:35], v[44:47], v[12:15]
	s_waitcnt lgkmcnt(2)
	v_mfma_f32_16x16x32_f16 v[8:11], v[36:39], v[44:47], v[8:11]
	s_waitcnt lgkmcnt(1)
	v_mfma_f32_16x16x32_f16 v[4:7], v[40:43], v[44:47], v[4:7]

.Lw2b77:
	s_waitcnt lgkmcnt(0)
	v_mfma_f32_16x16x32_f16 v[0:3], v[64:67], v[44:47], v[0:3]
	s_mov_b32 s5, 1
	s_mov_b64 s[18:19], 0
	s_and_b64 vcc, exec, s[10:11]
	s_cbranch_vccnz .LBB2_7

.Lw2b78:
	s_mov_b32 s14, s13
	s_mov_b32 s15, s13
	s_mul_i32 s12, s5, 0xc3500
	s_lshl_b64 s[10:11], s[12:13], 2
	s_mov_b32 s12, s13
	v_mov_b64_e32 v[34:35], s[14:15]
	v_mov_b64_e32 v[32:33], s[12:13]
	s_add_u32 s16, s6, s10
	ds_write_b128 v85, v[32:35]
	ds_write_b128 v85, v[32:35] offset:16
	ds_write_b128 v85, v[32:35] offset:32
	ds_write_b128 v85, v[32:35] offset:48
	s_addc_u32 s17, s7, s11

.Lw2b79:
	v_mov_b32_e32 v116, 0x3f86a0
	s_waitcnt vmcnt(1)
	v_add_u32_e32 v32, v113, v82
	s_waitcnt vmcnt(0)
	v_cmp_lt_i32_e32 vcc, v32, v103
	s_and_saveexec_b64 s[10:11], vcc
	s_cbranch_execz .LBB2_18
	v_ashrrev_i32_e32 v33, 31, v32
	v_lshl_add_u64 v[32:33], v[32:33], 2, s[16:17]

.Lw2b80:
	global_load_dword v116, v[32:33], off

.Lw2b81:
	v_mov_b32_e32 v116, v114
	s_cbranch_execnz .LBB2_90

.Lw2b82:
	s_waitcnt vmcnt(0)
	ds_bpermute_b32 v66, v84, v116
	ds_bpermute_b32 v123, v32, v116
	v_or_b32_e32 v32, 8, v84
	v_or_b32_e32 v34, 12, v84
	ds_bpermute_b32 v122, v32, v116
	ds_bpermute_b32 v121, v34, v116
	v_or_b32_e32 v34, 16, v84
	ds_bpermute_b32 v120, v34, v116
	v_or_b32_e32 v34, 20, v84

.Lw2b83:
	ds_bpermute_b32 v119, v34, v116
	s_waitcnt lgkmcnt(5)
	v_lshlrev_b32_e32 v32, 8, v66
	s_waitcnt lgkmcnt(4)
	v_lshlrev_b32_e32 v33, 8, v123
	v_or_b32_e32 v34, 24, v84
	v_and_or_b32 v32, v32, s21, v83
	v_and_or_b32 v33, v33, s21, v83
	ds_bpermute_b32 v118, v34, v116
	ds_bpermute_b32 v117, v87, v116

.Lw2b84:
	global_load_dwordx4 v[60:63], v32, s[8:9]
	global_load_dwordx4 v[56:59], v33, s[8:9]
	s_waitcnt lgkmcnt(5)
	v_lshlrev_b32_e32 v32, 8, v122
	s_waitcnt lgkmcnt(4)
	v_lshlrev_b32_e32 v33, 8, v121
	v_and_or_b32 v32, v32, s21, v83
	v_and_or_b32 v33, v33, s21, v83
	global_load_dwordx4 v[52:55], v32, s[8:9]
	global_load_dwordx4 v[48:51], v33, s[8:9]

.Lw2b85:
	s_waitcnt lgkmcnt(3)
	v_lshlrev_b32_e32 v32, 8, v120
	s_waitcnt lgkmcnt(2)
	v_lshlrev_b32_e32 v33, 8, v119
	v_and_or_b32 v32, v32, s21, v83
	v_and_or_b32 v33, v33, s21, v83
	global_load_dwordx4 v[44:47], v32, s[8:9]
	global_load_dwordx4 v[40:43], v33, s[8:9]
	s_waitcnt lgkmcnt(1)
	v_lshlrev_b32_e32 v32, 8, v118

.Lw2b86:
	s_waitcnt lgkmcnt(0)
	v_lshlrev_b32_e32 v33, 8, v117
	v_and_or_b32 v32, v32, s21, v83
	v_and_or_b32 v33, v33, s21, v83
	global_load_dwordx4 v[36:39], v32, s[8:9]
	s_nop 0
	global_load_dwordx4 v[32:35], v33, s[8:9]
	v_or_b32_e32 v64, 16, v82
	v_add_u32_e32 v64, v64, v113
	v_cmp_lt_i32_e32 vcc, v64, v103
	v_mov_b32_e32 v114, 0x3f86a0

.Lw2b87:
	s_and_saveexec_b64 s[14:15], vcc
	s_cbranch_execz .LBB2_23
	v_ashrrev_i32_e32 v65, 31, v64
	v_lshl_add_u64 v[64:65], v[64:65], 2, s[16:17]
	global_load_dword v114, v[64:65], off

.Lw2b88:
	v_mov_b32_e32 v68, v112
	v_mov_b32_e32 v69, v110
	v_mov_b32_e32 v70, v111
	v_mov_b32_e32 v71, v109
	v_mov_b32_e32 v64, v108
	v_mov_b32_e32 v65, v105
	v_mov_b32_e32 v66, v106
	v_mov_b32_e32 v67, v104
	s_and_saveexec_b64 s[14:15], s[18:19]
	s_cbranch_execz .LBB2_27
	v_cmp_gt_i32_e32 vcc, 16, v107
	s_and_saveexec_b64 s[18:19], vcc
	s_cbranch_execz .LBB2_26
	v_cvt_pk_f16_f32 v67, v111, v109

.Lw2b89:
	v_cvt_pk_f16_f32 v66, v112, v110
	v_cvt_pk_f16_f32 v65, v106, v104
	v_cvt_pk_f16_f32 v64, v108, v105
	v_mad_u64_u32 v[68:69], s[24:25], v107, s20, v[76:77]
	ds_write_b128 v68, v[64:67]

.Lw2b90:
	v_mov_b32_e32 v71, v68
	v_mov_b32_e32 v64, v68
	v_mov_b32_e32 v65, v68
	v_mov_b32_e32 v66, v68
	v_mov_b32_e32 v67, v68

.Lw2b91:
	s_and_b64 s[18:19], s[14:15], vcc
	s_and_saveexec_b64 s[14:15], s[18:19]
	s_cbranch_execz .LBB2_31
	v_cmp_gt_i32_e32 vcc, 16, v115
	s_and_saveexec_b64 s[18:19], vcc
	s_cbranch_execz .LBB2_30
	s_nop 1
	v_cvt_pk_f16_f32 v63, v62, v63
	v_cvt_pk_f16_f32 v62, v60, v61
	v_cvt_pk_f16_f32 v61, v66, v67
	v_cvt_pk_f16_f32 v60, v64, v65

.Lw2b92:
	v_mad_u64_u32 v[64:65], s[24:25], v115, s20, v[76:77]
	ds_write_b128 v64, v[60:63]

.Lw2b94:
	s_cbranch_execz .LBB2_34
	s_nop 1
	v_cvt_pk_f16_f32 v59, v58, v59
	v_cvt_pk_f16_f32 v58, v56, v57
	v_cvt_pk_f16_f32 v57, v66, v67
	v_cvt_pk_f16_f32 v56, v64, v65
	v_mad_u64_u32 v[60:61], s[24:25], v115, s20, v[76:77]
	ds_write_b128 v60, v[56:59]

.Lw2b95:
	s_nop 0
	v_mov_b32_e32 v56, 0
	v_mov_b32_e32 v115, v68
	v_mov_b32_e32 v57, v56
	v_mov_b32_e32 v58, v56
	v_mov_b32_e32 v59, v56
	v_mov_b32_e32 v64, v56
	v_mov_b32_e32 v65, v56
	v_mov_b32_e32 v66, v56
	v_mov_b32_e32 v67, v56

.Lw2b96:
	v_cmp_ne_u32_e32 vcc, v68, v115
	s_cmp_lg_u64 vcc, 0
	s_cselect_b64 s[14:15], -1, 0
	v_mfma_f32_16x16x16_f16 v[52:55], v[72:73], v[54:55], v[56:59]
	s_and_b64 s[18:19], s[14:15], vcc
	s_and_saveexec_b64 s[14:15], s[18:19]
	s_cbranch_execz .LBB2_39
	v_cmp_gt_i32_e32 vcc, 16, v115
	s_and_saveexec_b64 s[18:19], vcc
	s_cbranch_execz .LBB2_38
	s_nop 1
	v_cvt_pk_f16_f32 v55, v54, v55
	v_cvt_pk_f16_f32 v54, v52, v53

.Lw2b97:
	v_cvt_pk_f16_f32 v53, v62, v63
	v_cvt_pk_f16_f32 v52, v60, v61
	v_mad_u64_u32 v[56:57], s[24:25], v115, s20, v[76:77]
	ds_write_b128 v56, v[52:55]

.Lw2b98:
	v_mov_b32_e32 v55, v52
	v_mov_b32_e32 v60, v52
	v_mov_b32_e32 v61, v52
	v_mov_b32_e32 v62, v52
	v_mov_b32_e32 v63, v52

.Lw2b99:
	s_and_b64 s[18:19], s[14:15], vcc
	s_and_saveexec_b64 s[14:15], s[18:19]
	s_cbranch_execz .LBB2_43
	v_cmp_gt_i32_e32 vcc, 16, v115
	s_and_saveexec_b64 s[18:19], vcc
	s_cbranch_execz .LBB2_42
	s_nop 1
	v_cvt_pk_f16_f32 v51, v50, v51
	v_cvt_pk_f16_f32 v50, v48, v49
	v_cvt_pk_f16_f32 v49, v58, v59
	v_cvt_pk_f16_f32 v48, v56, v57

.Lw2b100:
	v_mad_u64_u32 v[52:53], s[24:25], v115, s20, v[76:77]
	ds_write_b128 v52, v[48:51]

.Lw2b102:
	s_cbranch_execz .LBB2_46
	s_nop 1
	v_cvt_pk_f16_f32 v47, v46, v47
	v_cvt_pk_f16_f32 v46, v44, v45
	v_cvt_pk_f16_f32 v45, v54, v55
	v_cvt_pk_f16_f32 v44, v52, v53
	v_mad_u64_u32 v[48:49], s[24:25], v115, s20, v[76:77]
	ds_write_b128 v48, v[44:47]

.Lw2b103:
	s_nop 0
	v_mov_b32_e32 v44, 0
	v_mov_b32_e32 v115, v60
	v_mov_b32_e32 v45, v44
	v_mov_b32_e32 v46, v44
	v_mov_b32_e32 v47, v44
	v_mov_b32_e32 v52, v44
	v_mov_b32_e32 v53, v44
	v_mov_b32_e32 v54, v44
	v_mov_b32_e32 v55, v44

.Lw2b104:
	v_cmp_ne_u32_e32 vcc, v56, v115
	s_cmp_lg_u64 vcc, 0
	s_cselect_b64 s[14:15], -1, 0
	v_mfma_f32_16x16x16_f16 v[40:43], v[72:73], v[42:43], v[44:47]
	s_and_b64 s[18:19], s[14:15], vcc
	s_and_saveexec_b64 s[14:15], s[18:19]
	s_cbranch_execz .LBB2_51
	v_cmp_gt_i32_e32 vcc, 16, v115
	s_and_saveexec_b64 s[18:19], vcc
	s_cbranch_execz .LBB2_50
	s_nop 1
	v_cvt_pk_f16_f32 v43, v42, v43
	v_cvt_pk_f16_f32 v42, v40, v41

.Lw2b105:
	v_cvt_pk_f16_f32 v41, v50, v51
	v_cvt_pk_f16_f32 v40, v48, v49
	v_mad_u64_u32 v[44:45], s[24:25], v115, s20, v[76:77]
	ds_write_b128 v44, v[40:43]

.Lw2b106:
	v_mov_b32_e32 v43, v40
	v_mov_b32_e32 v48, v40
	v_mov_b32_e32 v49, v40
	v_mov_b32_e32 v50, v40
	v_mov_b32_e32 v51, v40

.Lw2b107:
	s_and_b64 s[18:19], s[14:15], vcc
	s_and_saveexec_b64 s[14:15], s[18:19]
	s_cbranch_execz .LBB2_55
	v_cmp_gt_i32_e32 vcc, 16, v115
	s_and_saveexec_b64 s[18:19], vcc
	s_cbranch_execz .LBB2_54
	s_nop 1
	v_cvt_pk_f16_f32 v39, v38, v39
	v_cvt_pk_f16_f32 v38, v36, v37
	v_cvt_pk_f16_f32 v37, v46, v47
	v_cvt_pk_f16_f32 v36, v44, v45

.Lw2b108:
	v_mad_u64_u32 v[40:41], s[24:25], v115, s20, v[76:77]
	ds_write_b128 v40, v[36:39]

.Lw2b110:
	ds_bpermute_b32 v120, v91, v116
	ds_bpermute_b32 v119, v92, v116
	ds_bpermute_b32 v118, v93, v116
	s_waitcnt lgkmcnt(5)
	v_lshlrev_b32_e32 v32, 8, v123
	s_waitcnt lgkmcnt(4)
	v_lshlrev_b32_e32 v33, 8, v122
	v_and_or_b32 v32, v32, s21, v83
	v_and_or_b32 v33, v33, s21, v83
	ds_bpermute_b32 v117, v94, v116

.Lw2b111:
	ds_bpermute_b32 v116, v95, v116
	global_load_dwordx4 v[68:71], v32, s[8:9]
	global_load_dwordx4 v[64:67], v33, s[8:9]
	s_waitcnt lgkmcnt(5)
	v_lshlrev_b32_e32 v32, 8, v121
	s_waitcnt lgkmcnt(4)
	v_lshlrev_b32_e32 v33, 8, v120
	v_and_or_b32 v32, v32, s21, v83
	v_and_or_b32 v33, v33, s21, v83

.Lw2b112:
	global_load_dwordx4 v[52:55], v32, s[8:9]
	global_load_dwordx4 v[48:51], v33, s[8:9]
	s_waitcnt lgkmcnt(3)
	v_lshlrev_b32_e32 v32, 8, v119
	s_waitcnt lgkmcnt(2)
	v_lshlrev_b32_e32 v33, 8, v118
	v_and_or_b32 v32, v32, s21, v83
	v_and_or_b32 v33, v33, s21, v83
	global_load_dwordx4 v[44:47], v32, s[8:9]
	global_load_dwordx4 v[40:43], v33, s[8:9]

.Lw2b113:
	s_waitcnt lgkmcnt(1)
	v_lshlrev_b32_e32 v32, 8, v117
	s_waitcnt lgkmcnt(0)
	v_lshlrev_b32_e32 v33, 8, v116
	v_and_or_b32 v32, v32, s21, v83
	v_and_or_b32 v33, v33, s21, v83
	global_load_dwordx4 v[36:39], v32, s[8:9]
	s_nop 0
	global_load_dwordx4 v[32:35], v33, s[8:9]
	v_ashrrev_i32_e32 v123, 17, v123

.Lw2b114:
	v_cmp_ne_u32_e32 vcc, v123, v115
	s_cmp_lg_u64 vcc, 0
	s_cselect_b64 s[14:15], -1, 0
	s_and_b64 s[18:19], s[14:15], vcc
	s_and_saveexec_b64 s[14:15], s[18:19]
	s_cbranch_execz .LBB2_60
	v_cmp_gt_i32_e32 vcc, 16, v115
	s_and_saveexec_b64 s[18:19], vcc
	s_cbranch_execz .LBB2_59
	v_cvt_pk_f16_f32 v59, v58, v59
	v_cvt_pk_f16_f32 v58, v56, v57
	v_cvt_pk_f16_f32 v57, v62, v63

.Lw2b115:
	v_cvt_pk_f16_f32 v56, v60, v61
	v_mad_u64_u32 v[60:61], s[24:25], v115, s20, v[76:77]
	ds_write_b128 v60, v[56:59]

.Lw2b116:
	v_mov_b32_e32 v63, v56

.Lw2b117:
	s_and_saveexec_b64 s[18:19], vcc
	s_cbranch_execz .LBB2_63
	s_nop 1
	v_cvt_pk_f16_f32 v59, v58, v59
	v_cvt_pk_f16_f32 v58, v56, v57
	v_cvt_pk_f16_f32 v57, v62, v63
	v_cvt_pk_f16_f32 v56, v60, v61
	v_mad_u64_u32 v[60:61], s[24:25], v115, s20, v[76:77]
	ds_write_b128 v60, v[56:59]

.Lw2b119:
	v_cmp_ne_u32_e32 vcc, v68, v115
	s_cmp_lg_u64 vcc, 0
	s_cselect_b64 s[14:15], -1, 0
	v_mfma_f32_16x16x16_f16 v[56:59], v[72:73], v[66:67], v[56:59]
	s_and_b64 s[18:19], s[14:15], vcc
	s_and_saveexec_b64 s[14:15], s[18:19]
	s_cbranch_execz .LBB2_68
	v_cmp_gt_i32_e32 vcc, 16, v115
	s_and_saveexec_b64 s[18:19], vcc
	s_cbranch_execz .LBB2_67
	s_nop 1
	v_cvt_pk_f16_f32 v59, v58, v59

.Lw2b120:
	v_cvt_pk_f16_f32 v58, v56, v57
	v_cvt_pk_f16_f32 v57, v62, v63
	v_cvt_pk_f16_f32 v56, v60, v61
	v_mad_u64_u32 v[60:61], s[24:25], v115, s20, v[76:77]
	ds_write_b128 v60, v[56:59]

.Lw2b121:
	v_mov_b32_e32 v58, v56
	v_mov_b32_e32 v59, v56
	v_mov_b32_e32 v60, v56
	v_mov_b32_e32 v61, v56
	v_mov_b32_e32 v62, v56
	v_mov_b32_e32 v63, v56

.Lw2b122:
	s_and_b64 s[18:19], s[14:15], vcc
	s_and_saveexec_b64 s[14:15], s[18:19]
	s_cbranch_execz .LBB2_72
	v_cmp_gt_i32_e32 vcc, 16, v115
	s_and_saveexec_b64 s[18:19], vcc
	s_cbranch_execz .LBB2_71
	s_nop 1
	v_cvt_pk_f16_f32 v55, v54, v55
	v_cvt_pk_f16_f32 v54, v52, v53
	v_cvt_pk_f16_f32 v53, v62, v63
	v_cvt_pk_f16_f32 v52, v60, v61

.Lw2b123:
	v_mad_u64_u32 v[56:57], s[24:25], v115, s20, v[76:77]
	ds_write_b128 v56, v[52:55]

.Lw2b124:
	v_mov_b32_e32 v63, v52

.Lw2b125:
	s_and_saveexec_b64 s[18:19], vcc
	s_cbranch_execz .LBB2_75
	s_nop 1
	v_cvt_pk_f16_f32 v51, v50, v51
	v_cvt_pk_f16_f32 v50, v48, v49
	v_cvt_pk_f16_f32 v49, v58, v59
	v_cvt_pk_f16_f32 v48, v56, v57
	v_mad_u64_u32 v[52:53], s[24:25], v115, s20, v[76:77]
	ds_write_b128 v52, v[48:51]

.Lw2b127:
	v_cmp_ne_u32_e32 vcc, v60, v115
	s_cmp_lg_u64 vcc, 0
	s_cselect_b64 s[14:15], -1, 0
	v_mfma_f32_16x16x16_f16 v[44:47], v[72:73], v[46:47], v[48:51]
	s_and_b64 s[18:19], s[14:15], vcc
	s_and_saveexec_b64 s[14:15], s[18:19]
	s_cbranch_execz .LBB2_80
	v_cmp_gt_i32_e32 vcc, 16, v115
	s_and_saveexec_b64 s[18:19], vcc
	s_cbranch_execz .LBB2_79
	s_nop 1
	v_cvt_pk_f16_f32 v47, v46, v47

.Lw2b128:
	v_cvt_pk_f16_f32 v46, v44, v45
	v_cvt_pk_f16_f32 v45, v54, v55
	v_cvt_pk_f16_f32 v44, v52, v53
	v_mad_u64_u32 v[48:49], s[24:25], v115, s20, v[76:77]
	ds_write_b128 v48, v[44:47]

.Lw2b129:
	v_mov_b32_e32 v46, v44
	v_mov_b32_e32 v47, v44
	v_mov_b32_e32 v52, v44
	v_mov_b32_e32 v53, v44
	v_mov_b32_e32 v54, v44
	v_mov_b32_e32 v55, v44

.Lw2b130:
	s_and_b64 s[18:19], s[14:15], vcc
	s_and_saveexec_b64 s[14:15], s[18:19]
	s_cbranch_execz .LBB2_84
	v_cmp_gt_i32_e32 vcc, 16, v115
	s_and_saveexec_b64 s[18:19], vcc
	s_cbranch_execz .LBB2_83
	s_nop 1
	v_cvt_pk_f16_f32 v43, v42, v43
	v_cvt_pk_f16_f32 v42, v40, v41
	v_cvt_pk_f16_f32 v41, v50, v51
	v_cvt_pk_f16_f32 v40, v48, v49

.Lw2b131:
	v_mad_u64_u32 v[44:45], s[24:25], v115, s20, v[76:77]
	ds_write_b128 v44, v[40:43]

.Lw2b132:
	v_mov_b32_e32 v51, v40

.Lw2b133:
	s_and_saveexec_b64 s[18:19], vcc
	s_cbranch_execz .LBB2_87
	s_nop 1
	v_cvt_pk_f16_f32 v39, v38, v39
	v_cvt_pk_f16_f32 v38, v36, v37
	v_cvt_pk_f16_f32 v37, v46, v47
	v_cvt_pk_f16_f32 v36, v44, v45
	v_mad_u64_u32 v[40:41], s[24:25], v115, s20, v[76:77]
	ds_write_b128 v40, v[36:39]

.Lw2b135:
	v_add_u32_e32 v32, 16, v113
	v_mfma_f32_16x16x16_f16 v[56:59], v[72:73], v[34:35], v[36:39]

.Lw2b136:
	v_cvt_pk_f16_f32 v32, v108, v105
	v_mad_u64_u32 v[36:37], s[16:17], v107, s20, v[76:77]
	ds_write_b128 v36, v[32:35]
	s_branch .LBB2_15

.Lw2c0:
	s_cmpk_eq_u32 s40, 0x5aa5
	s_cbranch_scc1 .Lw2t13
	s_branch .Lw2b0

	.amdhsa_kernel _Z10k_layer_a2ILi0ELi13EEvPKDF16_PKiS3_PK15HIP_vector_typeIjLj4EES7_PKfS9_S9_S9_S9_S9_PDF16_Pf
		.amdhsa_group_segment_fixed_size 125188
		.amdhsa_private_segment_fixed_size 0
		.amdhsa_kernarg_size 360
		.amdhsa_user_sgpr_count 2
		.amdhsa_user_sgpr_dispatch_ptr 0
		.amdhsa_user_sgpr_queue_ptr 0
		.amdhsa_user_sgpr_kernarg_segment_ptr 1
		.amdhsa_user_sgpr_dispatch_id 0
		.amdhsa_user_sgpr_kernarg_preload_length 0
		.amdhsa_user_sgpr_kernarg_preload_offset 0
		.amdhsa_user_sgpr_private_segment_size 0
		.amdhsa_uses_dynamic_stack 0
		.amdhsa_enable_private_segment 0
		.amdhsa_system_sgpr_workgroup_id_x 1
		.amdhsa_system_sgpr_workgroup_id_y 0
		.amdhsa_system_sgpr_workgroup_id_z 0
		.amdhsa_system_sgpr_workgroup_info 0
		.amdhsa_system_vgpr_workitem_id 0
		.amdhsa_next_free_vgpr 125
		.amdhsa_next_free_sgpr 96
		.amdhsa_accum_offset 128
		.amdhsa_reserve_vcc 1
		.amdhsa_float_round_mode_32 0
		.amdhsa_float_round_mode_16_64 0
		.amdhsa_float_denorm_mode_32 3
		.amdhsa_float_denorm_mode_16_64 3
		.amdhsa_dx10_clamp 1
		.amdhsa_ieee_mode 1
		.amdhsa_fp16_overflow 0
		.amdhsa_tg_split 0
		.amdhsa_exception_fp_ieee_invalid_op 0
		.amdhsa_exception_fp_denorm_src 0
		.amdhsa_exception_fp_ieee_div_zero 0
		.amdhsa_exception_fp_ieee_overflow 0
		.amdhsa_exception_fp_ieee_underflow 0
		.amdhsa_exception_fp_ieee_inexact 0
		.amdhsa_exception_int_div_zero 0
	.end_amdhsa_kernel
	.text
.Lfunc_end2:
	.size	_Z10k_layer_a2ILi0ELi13EEvPKDF16_PKiS3_PK15HIP_vector_typeIjLj4EES7_PKfS9_S9_S9_S9_S9_PDF16_Pf, .Lfunc_end2-_Z10k_layer_a2ILi0ELi13EEvPKDF16_PKiS3_PK15HIP_vector_typeIjLj4EES7_PKfS9_S9_S9_S9_S9_PDF16_Pf
	.set _Z10k_layer_a2ILi0ELi13EEvPKDF16_PKiS3_PK15HIP_vector_typeIjLj4EES7_PKfS9_S9_S9_S9_S9_PDF16_Pf.num_vgpr, 125
	.set _Z10k_layer_a2ILi0ELi13EEvPKDF16_PKiS3_PK15HIP_vector_typeIjLj4EES7_PKfS9_S9_S9_S9_S9_PDF16_Pf.num_agpr, 0
	.set _Z10k_layer_a2ILi0ELi13EEvPKDF16_PKiS3_PK15HIP_vector_typeIjLj4EES7_PKfS9_S9_S9_S9_S9_PDF16_Pf.numbered_sgpr, 26
	.set _Z10k_layer_a2ILi0ELi13EEvPKDF16_PKiS3_PK15HIP_vector_typeIjLj4EES7_PKfS9_S9_S9_S9_S9_PDF16_Pf.num_named_barrier, 0
	.set _Z10k_layer_a2ILi0ELi13EEvPKDF16_PKiS3_PK15HIP_vector_typeIjLj4EES7_PKfS9_S9_S9_S9_S9_PDF16_Pf.private_seg_size, 0
	.set _Z10k_layer_a2ILi0ELi13EEvPKDF16_PKiS3_PK15HIP_vector_typeIjLj4EES7_PKfS9_S9_S9_S9_S9_PDF16_Pf.uses_vcc, 1
	.set _Z10k_layer_a2ILi0ELi13EEvPKDF16_PKiS3_PK15HIP_vector_typeIjLj4EES7_PKfS9_S9_S9_S9_S9_PDF16_Pf.uses_flat_scratch, 0
	.set _Z10k_layer_a2ILi0ELi13EEvPKDF16_PKiS3_PK15HIP_vector_typeIjLj4EES7_PKfS9_S9_S9_S9_S9_PDF16_Pf.has_dyn_sized_stack, 0
	.set _Z10k_layer_a2ILi0ELi13EEvPKDF16_PKiS3_PK15HIP_vector_typeIjLj4EES7_PKfS9_S9_S9_S9_S9_PDF16_Pf.has_recursion, 0
	.set _Z10k_layer_a2ILi0ELi13EEvPKDF16_PKiS3_PK15HIP_vector_typeIjLj4EES7_PKfS9_S9_S9_S9_S9_PDF16_Pf.has_indirect_call, 0

	.text
	.protected	_Z10k_layer_a2ILi1ELi13EEvPKDF16_PKiS3_PK15HIP_vector_typeIjLj4EES7_PKfS9_S9_S9_S9_S9_PDF16_Pf
	.globl	_Z10k_layer_a2ILi1ELi13EEvPKDF16_PKiS3_PK15HIP_vector_typeIjLj4EES7_PKfS9_S9_S9_S9_S9_PDF16_Pf
	.p2align	8
	.type	_Z10k_layer_a2ILi1ELi13EEvPKDF16_PKiS3_PK15HIP_vector_typeIjLj4EES7_PKfS9_S9_S9_S9_S9_PDF16_Pf,@function
_Z10k_layer_a2ILi1ELi13EEvPKDF16_PKiS3_PK15HIP_vector_typeIjLj4EES7_PKfS9_S9_S9_S9_S9_PDF16_Pf:
	s_movk_i32 s40, 0x5aa5
	v_lshrrev_b32_e32 v1, 6, v0
	s_nop 0
	v_readfirstlane_b32 s41, v1
	s_mov_b64 exec, 0
	s_cmpk_lt_u32 s41, 6
	s_cbranch_scc1 .Lw3d0_13
	s_cmpk_lt_u32 s41, 9
	s_cbranch_scc1 .Lw3d6_13
	s_cmpk_lt_u32 s41, 11
	s_cbranch_scc1 .Lw3d9_13
	s_cmpk_lt_u32 s41, 12
	s_cbranch_scc1 .Lw3d11_13
	s_branch .Lw3t12

.Lw3end:
	s_mov_b32 s40, 0
	s_mov_b64 exec, -1
	s_load_dwordx4 s[12:15], s[0:1], 0x38

.Lw3b0:
	s_load_dwordx8 s[4:11], s[0:1], 0x18

.Lw3b1:
	v_mov_b32_e32 v3, 0
	v_lshlrev_b32_e32 v2, 4, v0
	s_movk_i32 s3, 0x3000
	v_min_u32_e32 v1, 0x7f, v0
	s_waitcnt lgkmcnt(0)
	v_lshl_add_u64 v[4:5], s[4:5], 0, v[2:3]
	v_add_co_u32_e32 v6, vcc, s3, v4
	s_movk_i32 s3, 0x6000
	s_nop 0
	v_addc_co_u32_e32 v7, vcc, 0, v5, vcc
	v_add_co_u32_e32 v16, vcc, s3, v4
	v_lshlrev_b32_e32 v26, 2, v1

.Lw3b2:
	s_nop 0
	v_addc_co_u32_e32 v17, vcc, 0, v5, vcc
	global_load_dwordx4 v[8:11], v[6:7], off offset:1024
	global_load_dwordx4 v[12:15], v[16:17], off offset:2048
	v_add_co_u32_e32 v24, vcc, 0x9000, v4
	v_readfirstlane_b32 s3, v0
	s_nop 0
	v_addc_co_u32_e32 v25, vcc, 0, v5, vcc
	global_load_dwordx4 v[16:19], v2, s[4:5]
	global_load_dwordx4 v[20:23], v[24:25], off offset:3072

.Lw3b3:
	global_load_dword v5, v26, s[8:9]
	global_load_dword v7, v26, s[8:9] offset:512
	global_load_dword v1, v26, s[10:11]
	global_load_dword v4, v26, s[12:13]
	global_load_dword v6, v26, s[14:15]
	s_movk_i32 s8, 0x300
	v_cmp_gt_u32_e32 vcc, s8, v0
	s_waitcnt vmcnt(6)
	ds_write_b128 v2, v[16:19]

.Lw3b4:
	ds_write_b128 v2, v[8:11] offset:13312
	ds_write_b128 v2, v[12:15] offset:26624
	s_waitcnt vmcnt(5)
	ds_write_b128 v2, v[20:23] offset:39936
	s_and_saveexec_b64 s[8:9], vcc
	s_cbranch_execz .LBB3_2
	v_add_u32_e32 v8, 0xd00, v0
	v_min_u32_e32 v8, 0xfff, v8
	v_lshlrev_b32_e32 v8, 4, v8
	global_load_dwordx4 v[8:11], v8, s[4:5]

.Lw3b5:
	s_waitcnt vmcnt(0)
	ds_write_b128 v2, v[8:11] offset:53248

.Lw3b6:
	v_mov_b32_e32 v2, 0x1dd00
	v_lshl_add_u32 v2, v0, 4, v2
	v_cmp_gt_u32_e32 vcc, s4, v0
	s_waitcnt vmcnt(1)
	ds_write_b128 v2, v[8:11]
	s_waitcnt vmcnt(0)
	ds_write_b128 v2, v[12:15] offset:13312
	s_and_saveexec_b64 s[4:5], vcc
	s_cbranch_execz .LBB3_4
	v_add_u32_e32 v3, 0x680, v0

.Lw3b7:
	v_min_u32_e32 v3, 0x8ff, v3
	v_lshlrev_b32_e32 v3, 4, v3
	global_load_dwordx4 v[8:11], v3, s[6:7]
	s_waitcnt vmcnt(0)
	ds_write_b128 v2, v[8:11] offset:26624

.Lw3b8:
	v_add_f32_e32 v2, v5, v7
	v_lshl_add_u32 v3, v0, 2, v3
	ds_write2st64_b32 v3, v2, v1 offset1:2
	ds_write2st64_b32 v3, v4, v6 offset0:4 offset1:6

.Lw3b9:
	s_load_dwordx2 s[18:19], s[0:1], 0x10
	s_mov_b32 s13, 0
	v_cmp_eq_u32_e32 vcc, 0, v0
	s_and_saveexec_b64 s[4:5], vcc
	v_mov_b32_e32 v1, 0
	v_mov_b32_e32 v2, 0x27900
	ds_write_b32 v2, v1
	s_or_b64 exec, exec, s[4:5]
	v_bfe_u32 v1, v0, 4, 2
	v_bfe_u32 v2, v0, 2, 2

.Lw3b10:
	v_cmp_eq_u32_e32 vcc, v1, v2
	v_and_b32_e32 v2, 3, v0
	v_cmp_eq_u32_e64 s[4:5], 0, v2
	v_mov_b32_e32 v3, 0x3c00
	s_and_b64 s[4:5], vcc, s[4:5]
	v_cndmask_b32_e64 v4, 0, v3, s[4:5]
	v_cmp_eq_u32_e64 s[4:5], 1, v2
	s_and_b64 s[4:5], vcc, s[4:5]
	s_lshr_b32 s12, s3, 6
	v_cndmask_b32_e64 v5, 0, v3, s[4:5]

.Lw3b11:
	v_cmp_eq_u32_e64 s[4:5], 2, v2
	s_and_b64 s[4:5], vcc, s[4:5]
	v_and_b32_e32 v77, 63, v0
	v_cndmask_b32_e64 v6, 0, v3, s[4:5]
	v_cmp_eq_u32_e64 s[4:5], 3, v2
	s_and_b64 vcc, vcc, s[4:5]
	v_cndmask_b32_e32 v2, 0, v3, vcc
	v_pack_b32_f16 v73, v6, v2
	v_lshlrev_b32_e32 v2, 2, v0
	v_and_b32_e32 v82, 0xc0, v2

.Lw3b12:
	v_and_b32_e32 v2, 48, v0
	v_mov_b32_e32 v3, 0
	s_waitcnt lgkmcnt(0)
	s_barrier
	v_and_b32_e32 v80, 15, v0
	s_load_dword s3, s[0:1], 0x68
	s_mul_i32 s0, s12, 0x1100
	v_lshl_add_u64 v[74:75], s[10:11], 0, v[2:3]
	v_bfe_u32 v3, v0, 2, 4
	v_lshlrev_b32_e32 v0, 6, v0
	s_add_i32 s4, s0, 0x10000

.Lw3b13:
	v_mul_u32_u24_e32 v3, 0x110, v3
	v_and_b32_e32 v0, 0xc0, v0
	s_movk_i32 s26, 0x110
	v_add3_u32 v83, s4, v3, v0
	v_mov_b32_e32 v0, s4
	v_mad_u32_u24 v0, v80, s26, v0
	v_pack_b32_f16 v72, v4, v5
	v_lshlrev_b32_e32 v81, 4, v80
	v_lshlrev_b32_e32 v4, 7, v1

.Lw3b14:
	v_add_u32_e32 v97, v0, v2
	v_mbcnt_lo_u32_b32 v0, -1, 0
	v_cmp_eq_u32_e64 s[0:1], 0, v77
	v_or_b32_e32 v76, s4, v81
	v_lshlrev_b32_e32 v84, 5, v1
	v_cmp_gt_u32_e64 s[4:5], 16, v77
	v_or_b32_e32 v85, 24, v82
	v_or_b32_e32 v86, 28, v82
	v_or_b32_e32 v87, 32, v82
	v_or_b32_e32 v88, 36, v82
	v_or_b32_e32 v89, 40, v82
	v_or_b32_e32 v90, 44, v82

.Lw3b15:
	v_or_b32_e32 v91, 48, v82
	v_or_b32_e32 v92, 52, v82
	v_or_b32_e32 v93, 56, v82
	v_or_b32_e32 v94, 60, v82
	v_mov_b32_e32 v95, 0x27900
	v_add_u32_e32 v96, 0x26d00, v4
	s_mov_b32 s27, 0x1ffff00
	v_mov_b32_e32 v98, 0x3727c5ac
	s_mov_b32 s28, 0x800000
	v_mov_b32_e32 v99, 0xc0135761

.Lw3b16:
	v_mbcnt_hi_u32_b32 v100, -1, v0
	v_mov_b32_e32 v101, 0x26d00
	v_mov_b32_e32 v102, 0x1dd00
	s_branch .LBB3_11

.Lw3b17:
	s_cbranch_execz .LBB3_15
	s_mov_b64 s[20:21], exec
	v_mbcnt_lo_u32_b32 v0, s20, 0
	v_mbcnt_hi_u32_b32 v0, s21, v0
	v_cmp_eq_u32_e32 vcc, 0, v0
	s_and_saveexec_b64 s[14:15], vcc
	s_bcnt1_i32_b64 s12, s[20:21]
	v_mov_b32_e32 v1, s12
	ds_add_rtn_u32 v1, v95, v1
	s_or_b64 exec, exec, s[14:15]
	s_waitcnt lgkmcnt(0)
	v_readfirstlane_b32 s12, v1

.Lw3b18:
	s_nop 1
	v_add_u32_e32 v0, s12, v0

.Lw3b19:
	ds_read_b128 v[16:19], v96 offset:48
	ds_read_b128 v[12:15], v96 offset:64
	ds_read_b128 v[8:11], v96 offset:80
	ds_read_b128 v[4:7], v96 offset:96
	ds_read_b128 v[0:3], v96 offset:112
	s_lshl_b32 s10, s12, 4
	s_ashr_i32 s11, s10, 31
	v_lshl_add_u64 v[78:79], s[10:11], 2, v[74:75]

.Lw3b20:
	s_mov_b32 s11, 0
	s_mov_b64 s[22:23], -1
	s_branch .LBB3_18

.Lw3b21:
	v_lshl_add_u32 v103, s11, 15, v48
	ds_read_b128 v[48:51], v103
	ds_read_b128 v[52:55], v103 offset:1024
	ds_read_b128 v[56:59], v103 offset:2048
	ds_read_b128 v[60:63], v103 offset:3072
	ds_read_b128 v[64:67], v103 offset:4096
	ds_read_b128 v[68:71], v103 offset:5120
	ds_read_b128 v[104:107], v103 offset:6144

.Lw3b22:
	ds_read_b128 v[108:111], v103 offset:7168
	s_waitcnt lgkmcnt(7)
	v_mfma_f32_16x16x32_f16 v[28:31], v[48:51], v[32:35], v[28:31]
	s_waitcnt lgkmcnt(6)
	v_mfma_f32_16x16x32_f16 v[24:27], v[52:55], v[32:35], v[24:27]
	s_waitcnt lgkmcnt(5)
	v_mfma_f32_16x16x32_f16 v[20:23], v[56:59], v[32:35], v[20:23]
	s_waitcnt lgkmcnt(4)
	v_mfma_f32_16x16x32_f16 v[16:19], v[60:63], v[32:35], v[16:19]

.Lw3b23:
	ds_read_b128 v[48:51], v103 offset:8192
	ds_read_b128 v[52:55], v103 offset:9216
	ds_read_b128 v[56:59], v103 offset:10240
	ds_read_b128 v[60:63], v103 offset:11264
	s_waitcnt lgkmcnt(7)
	v_mfma_f32_16x16x32_f16 v[12:15], v[64:67], v[32:35], v[12:15]
	s_waitcnt lgkmcnt(6)
	v_mfma_f32_16x16x32_f16 v[8:11], v[68:71], v[32:35], v[8:11]
	s_waitcnt lgkmcnt(5)

.Lw3b24:
	v_mfma_f32_16x16x32_f16 v[4:7], v[104:107], v[32:35], v[4:7]
	s_waitcnt lgkmcnt(4)
	v_mfma_f32_16x16x32_f16 v[0:3], v[108:111], v[32:35], v[0:3]
	ds_read_b128 v[32:35], v103 offset:12288
	ds_read_b128 v[64:67], v103 offset:13312
	ds_read_b128 v[68:71], v103 offset:14336
	ds_read_b128 v[104:107], v103 offset:15360
	s_waitcnt lgkmcnt(7)
	v_mfma_f32_16x16x32_f16 v[28:31], v[48:51], v[36:39], v[28:31]

.Lw3b25:
	s_waitcnt lgkmcnt(6)
	v_mfma_f32_16x16x32_f16 v[24:27], v[52:55], v[36:39], v[24:27]
	s_waitcnt lgkmcnt(5)
	v_mfma_f32_16x16x32_f16 v[20:23], v[56:59], v[36:39], v[20:23]
	s_waitcnt lgkmcnt(4)
	v_mfma_f32_16x16x32_f16 v[16:19], v[60:63], v[36:39], v[16:19]
	ds_read_b128 v[48:51], v103 offset:16384
	ds_read_b128 v[52:55], v103 offset:17408
	ds_read_b128 v[56:59], v103 offset:18432

.Lw3b26:
	ds_read_b128 v[60:63], v103 offset:19456
	s_waitcnt lgkmcnt(7)
	v_mfma_f32_16x16x32_f16 v[12:15], v[32:35], v[36:39], v[12:15]
	s_waitcnt lgkmcnt(6)
	v_mfma_f32_16x16x32_f16 v[8:11], v[64:67], v[36:39], v[8:11]
	s_waitcnt lgkmcnt(5)
	v_mfma_f32_16x16x32_f16 v[4:7], v[68:71], v[36:39], v[4:7]
	s_waitcnt lgkmcnt(4)
	v_mfma_f32_16x16x32_f16 v[0:3], v[104:107], v[36:39], v[0:3]

.Lw3b27:
	ds_read_b128 v[32:35], v103 offset:20480
	ds_read_b128 v[36:39], v103 offset:21504
	ds_read_b128 v[64:67], v103 offset:22528
	ds_read_b128 v[68:71], v103 offset:23552
	s_waitcnt lgkmcnt(7)
	v_mfma_f32_16x16x32_f16 v[28:31], v[48:51], v[40:43], v[28:31]
	s_waitcnt lgkmcnt(6)
	v_mfma_f32_16x16x32_f16 v[24:27], v[52:55], v[40:43], v[24:27]
	s_waitcnt lgkmcnt(5)

.Lw3b28:
	v_mfma_f32_16x16x32_f16 v[20:23], v[56:59], v[40:43], v[20:23]
	s_waitcnt lgkmcnt(4)
	v_mfma_f32_16x16x32_f16 v[16:19], v[60:63], v[40:43], v[16:19]
	ds_read_b128 v[48:51], v103 offset:24576
	ds_read_b128 v[52:55], v103 offset:25600
	ds_read_b128 v[56:59], v103 offset:26624
	ds_read_b128 v[60:63], v103 offset:27648
	s_waitcnt lgkmcnt(7)
	v_mfma_f32_16x16x32_f16 v[12:15], v[32:35], v[40:43], v[12:15]

.Lw3b29:
	s_waitcnt lgkmcnt(6)
	v_mfma_f32_16x16x32_f16 v[8:11], v[36:39], v[40:43], v[8:11]
	s_waitcnt lgkmcnt(5)
	v_mfma_f32_16x16x32_f16 v[4:7], v[64:67], v[40:43], v[4:7]
	s_waitcnt lgkmcnt(4)
	v_mfma_f32_16x16x32_f16 v[0:3], v[68:71], v[40:43], v[0:3]
	ds_read_b128 v[32:35], v103 offset:28672
	ds_read_b128 v[36:39], v103 offset:29696
	ds_read_b128 v[40:43], v103 offset:30720

.Lw3b30:
	ds_read_b128 v[64:67], v103 offset:31744
	s_waitcnt lgkmcnt(7)
	v_mfma_f32_16x16x32_f16 v[28:31], v[48:51], v[44:47], v[28:31]
	s_waitcnt lgkmcnt(6)
	v_mfma_f32_16x16x32_f16 v[24:27], v[52:55], v[44:47], v[24:27]
	s_waitcnt lgkmcnt(5)
	v_mfma_f32_16x16x32_f16 v[20:23], v[56:59], v[44:47], v[20:23]
	s_waitcnt lgkmcnt(4)
	v_mfma_f32_16x16x32_f16 v[16:19], v[60:63], v[44:47], v[16:19]

.Lw3b31:
	s_waitcnt lgkmcnt(3)
	v_mfma_f32_16x16x32_f16 v[12:15], v[32:35], v[44:47], v[12:15]
	s_waitcnt lgkmcnt(2)
	v_mfma_f32_16x16x32_f16 v[8:11], v[36:39], v[44:47], v[8:11]
	s_waitcnt lgkmcnt(1)
	v_mfma_f32_16x16x32_f16 v[4:7], v[40:43], v[44:47], v[4:7]
	s_waitcnt lgkmcnt(0)
	v_mfma_f32_16x16x32_f16 v[0:3], v[64:67], v[44:47], v[0:3]
	s_mov_b32 s11, 1
	s_mov_b64 s[22:23], 0
	s_and_b64 vcc, exec, s[14:15]

.Lw3b32:
	s_cbranch_vccnz .LBB3_94

.Lw3b33:
	v_mov_b64_e32 v[34:35], s[14:15]
	v_mov_b64_e32 v[32:33], s[12:13]
	s_add_u32 s20, s18, s20
	ds_write_b128 v83, v[32:35]
	ds_write_b128 v83, v[32:35] offset:16
	ds_write_b128 v83, v[32:35] offset:32
	ds_write_b128 v83, v[32:35] offset:48
	s_addc_u32 s21, s19, s21
	v_mov_b32_e32 v116, 0x3f86a0
	s_waitcnt vmcnt(1)

.Lw3b34:
	v_add_u32_e32 v32, v113, v80
	s_waitcnt vmcnt(0)
	v_cmp_lt_i32_e32 vcc, v32, v103
	s_and_saveexec_b64 s[14:15], vcc
	s_cbranch_execz .LBB3_20
	v_ashrrev_i32_e32 v33, 31, v32
	v_lshl_add_u64 v[32:33], v[32:33], 2, s[20:21]
	global_load_dword v116, v[32:33], off

.Lw3b35:
	v_mov_b32_e32 v58, v56
	v_mov_b32_e32 v59, v56
	v_mov_b32_e32 v60, v56
	v_mov_b32_e32 v61, v56
	v_mov_b32_e32 v62, v56
	v_mov_b32_e32 v63, v56
	s_branch .LBB3_22

.Lw3b36:
	v_mov_b32_e32 v109, v59
	v_mov_b32_e32 v111, v58
	v_mov_b32_e32 v110, v57
	v_mov_b32_e32 v112, v56
	v_mov_b32_e32 v107, v115
	v_cmp_lt_i32_e32 vcc, v113, v103
	s_cbranch_vccz .LBB3_21
	v_or_b32_e32 v32, 4, v82
	s_waitcnt vmcnt(0)
	ds_bpermute_b32 v66, v82, v116
	ds_bpermute_b32 v123, v32, v116
	v_or_b32_e32 v32, 8, v82
	v_or_b32_e32 v34, 12, v82

.Lw3b37:
	ds_bpermute_b32 v122, v32, v116
	ds_bpermute_b32 v121, v34, v116
	v_or_b32_e32 v34, 16, v82
	ds_bpermute_b32 v120, v34, v116
	v_or_b32_e32 v34, 20, v82
	ds_bpermute_b32 v119, v34, v116
	s_waitcnt lgkmcnt(5)
	v_lshlrev_b32_e32 v32, 8, v66
	s_waitcnt lgkmcnt(4)
	v_lshlrev_b32_e32 v33, 8, v123
	v_and_or_b32 v32, v32, s27, v81

.Lw3b38:
	v_and_or_b32 v33, v33, s27, v81
	ds_bpermute_b32 v118, v85, v116
	ds_bpermute_b32 v117, v86, v116
	global_load_dwordx4 v[60:63], v32, s[8:9]
	global_load_dwordx4 v[56:59], v33, s[8:9]
	s_waitcnt lgkmcnt(5)
	v_lshlrev_b32_e32 v32, 8, v122
	s_waitcnt lgkmcnt(4)
	v_lshlrev_b32_e32 v33, 8, v121

.Lw3b39:
	v_and_or_b32 v32, v32, s27, v81
	v_and_or_b32 v33, v33, s27, v81
	global_load_dwordx4 v[52:55], v32, s[8:9]
	global_load_dwordx4 v[48:51], v33, s[8:9]
	s_waitcnt lgkmcnt(3)
	v_lshlrev_b32_e32 v32, 8, v120
	s_waitcnt lgkmcnt(2)
	v_lshlrev_b32_e32 v33, 8, v119
	v_and_or_b32 v32, v32, s27, v81
	v_and_or_b32 v33, v33, s27, v81

.Lw3b40:
	global_load_dwordx4 v[44:47], v32, s[8:9]
	global_load_dwordx4 v[40:43], v33, s[8:9]
	s_waitcnt lgkmcnt(1)
	v_lshlrev_b32_e32 v32, 8, v118
	s_waitcnt lgkmcnt(0)
	v_lshlrev_b32_e32 v33, 8, v117
	v_and_or_b32 v32, v32, s27, v81
	v_and_or_b32 v33, v33, s27, v81
	global_load_dwordx4 v[36:39], v32, s[8:9]

.Lw3b41:
	s_nop 0
	global_load_dwordx4 v[32:35], v33, s[8:9]
	v_or_b32_e32 v64, 16, v80
	v_add_u32_e32 v64, v64, v113
	v_cmp_lt_i32_e32 vcc, v64, v103
	v_mov_b32_e32 v114, 0x3f86a0
	s_and_saveexec_b64 s[22:23], vcc
	s_cbranch_execz .LBB3_25
	v_ashrrev_i32_e32 v65, 31, v64
	v_lshl_add_u64 v[64:65], v[64:65], 2, s[20:21]
	global_load_dword v114, v[64:65], off

.Lw3b43:
	s_and_saveexec_b64 s[22:23], s[24:25]
	s_cbranch_execz .LBB3_29
	v_cmp_gt_i32_e32 vcc, 16, v107
	s_and_saveexec_b64 s[24:25], vcc
	s_cbranch_execz .LBB3_28
	v_cvt_pk_f16_f32 v67, v111, v109
	v_cvt_pk_f16_f32 v66, v112, v110
	v_cvt_pk_f16_f32 v65, v106, v104
	v_cvt_pk_f16_f32 v64, v108, v105
	v_mad_u64_u32 v[68:69], s[30:31], v107, s26, v[76:77]

.Lw3b44:
	ds_write_b128 v68, v[64:67]

.Lw3b45:
	v_mfma_f32_16x16x16_f16 v[64:67], v[72:73], v[60:61], v[64:67]
	v_cmp_ne_u32_e32 vcc, v123, v115
	s_cmp_lg_u64 vcc, 0
	s_cselect_b64 s[22:23], -1, 0
	v_mfma_f32_16x16x16_f16 v[60:63], v[72:73], v[62:63], v[68:71]
	s_and_b64 s[24:25], s[22:23], vcc
	s_and_saveexec_b64 s[22:23], s[24:25]
	s_cbranch_execz .LBB3_33
	v_cmp_gt_i32_e32 vcc, 16, v115
	s_and_saveexec_b64 s[24:25], vcc
	s_cbranch_execz .LBB3_32
	s_nop 1
	v_cvt_pk_f16_f32 v63, v62, v63

.Lw3b46:
	v_cvt_pk_f16_f32 v62, v60, v61
	v_cvt_pk_f16_f32 v61, v66, v67
	v_cvt_pk_f16_f32 v60, v64, v65
	v_mad_u64_u32 v[64:65], s[30:31], v115, s26, v[76:77]
	ds_write_b128 v64, v[60:63]

.Lw3b47:
	v_mov_b32_e32 v61, v60
	v_mov_b32_e32 v62, v60
	v_mov_b32_e32 v63, v60
	v_mov_b32_e32 v64, v60
	v_mov_b32_e32 v65, v60
	v_mov_b32_e32 v66, v60
	v_mov_b32_e32 v67, v60

.Lw3b48:
	v_mfma_f32_16x16x16_f16 v[56:59], v[72:73], v[58:59], v[60:63]
	s_and_b64 s[24:25], s[22:23], vcc
	s_and_saveexec_b64 s[22:23], s[24:25]
	s_cbranch_execz .LBB3_37
	v_cmp_gt_i32_e32 vcc, 16, v115
	s_and_saveexec_b64 s[24:25], vcc
	s_cbranch_execz .LBB3_36
	s_nop 1
	v_cvt_pk_f16_f32 v59, v58, v59
	v_cvt_pk_f16_f32 v58, v56, v57
	v_cvt_pk_f16_f32 v57, v66, v67

.Lw3b49:
	v_cvt_pk_f16_f32 v56, v64, v65
	v_mad_u64_u32 v[60:61], s[30:31], v115, s26, v[76:77]
	ds_write_b128 v60, v[56:59]

.Lw3b50:
	v_mov_b32_e32 v66, v56
	v_mov_b32_e32 v67, v56

.Lw3b51:
	v_cmp_gt_i32_e32 vcc, 16, v115
	s_and_saveexec_b64 s[24:25], vcc
	s_cbranch_execz .LBB3_40
	s_nop 1
	v_cvt_pk_f16_f32 v55, v54, v55
	v_cvt_pk_f16_f32 v54, v52, v53
	v_cvt_pk_f16_f32 v53, v62, v63
	v_cvt_pk_f16_f32 v52, v60, v61
	v_mad_u64_u32 v[56:57], s[30:31], v115, s26, v[76:77]
	ds_write_b128 v56, v[52:55]

.Lw3b53:
	v_mfma_f32_16x16x16_f16 v[56:59], v[72:73], v[48:49], v[60:63]
	v_cmp_ne_u32_e32 vcc, v64, v115
	s_cmp_lg_u64 vcc, 0
	s_cselect_b64 s[22:23], -1, 0
	v_mfma_f32_16x16x16_f16 v[48:51], v[72:73], v[50:51], v[52:55]
	s_and_b64 s[24:25], s[22:23], vcc
	s_and_saveexec_b64 s[22:23], s[24:25]
	s_cbranch_execz .LBB3_45
	v_cmp_gt_i32_e32 vcc, 16, v115
	s_and_saveexec_b64 s[24:25], vcc
	s_cbranch_execz .LBB3_44
	s_nop 1
	v_cvt_pk_f16_f32 v51, v50, v51

.Lw3b54:
	v_cvt_pk_f16_f32 v50, v48, v49
	v_cvt_pk_f16_f32 v49, v58, v59
	v_cvt_pk_f16_f32 v48, v56, v57
	v_mad_u64_u32 v[52:53], s[30:31], v115, s26, v[76:77]
	ds_write_b128 v52, v[48:51]

.Lw3b55:
	v_mov_b32_e32 v49, v48
	v_mov_b32_e32 v50, v48
	v_mov_b32_e32 v51, v48
	v_mov_b32_e32 v56, v48
	v_mov_b32_e32 v57, v48
	v_mov_b32_e32 v58, v48
	v_mov_b32_e32 v59, v48

.Lw3b56:
	v_mfma_f32_16x16x16_f16 v[44:47], v[72:73], v[46:47], v[48:51]
	s_and_b64 s[24:25], s[22:23], vcc
	s_and_saveexec_b64 s[22:23], s[24:25]
	s_cbranch_execz .LBB3_49
	v_cmp_gt_i32_e32 vcc, 16, v115
	s_and_saveexec_b64 s[24:25], vcc
	s_cbranch_execz .LBB3_48
	s_nop 1
	v_cvt_pk_f16_f32 v47, v46, v47
	v_cvt_pk_f16_f32 v46, v44, v45
	v_cvt_pk_f16_f32 v45, v54, v55

.Lw3b57:
	v_cvt_pk_f16_f32 v44, v52, v53
	v_mad_u64_u32 v[48:49], s[30:31], v115, s26, v[76:77]
	ds_write_b128 v48, v[44:47]

.Lw3b58:
	v_mov_b32_e32 v54, v44
	v_mov_b32_e32 v55, v44

.Lw3b59:
	v_cmp_gt_i32_e32 vcc, 16, v115
	s_and_saveexec_b64 s[24:25], vcc
	s_cbranch_execz .LBB3_52
	s_nop 1
	v_cvt_pk_f16_f32 v43, v42, v43
	v_cvt_pk_f16_f32 v42, v40, v41
	v_cvt_pk_f16_f32 v41, v50, v51
	v_cvt_pk_f16_f32 v40, v48, v49
	v_mad_u64_u32 v[44:45], s[30:31], v115, s26, v[76:77]
	ds_write_b128 v44, v[40:43]

.Lw3b61:
	v_mfma_f32_16x16x16_f16 v[44:47], v[72:73], v[36:37], v[48:51]
	v_cmp_ne_u32_e32 vcc, v52, v115
	s_cmp_lg_u64 vcc, 0
	s_cselect_b64 s[22:23], -1, 0
	v_mfma_f32_16x16x16_f16 v[36:39], v[72:73], v[38:39], v[40:43]
	s_and_b64 s[24:25], s[22:23], vcc
	s_and_saveexec_b64 s[22:23], s[24:25]
	s_cbranch_execz .LBB3_57
	v_cmp_gt_i32_e32 vcc, 16, v115
	s_and_saveexec_b64 s[24:25], vcc
	s_cbranch_execz .LBB3_56
	s_nop 1
	v_cvt_pk_f16_f32 v39, v38, v39

.Lw3b62:
	v_cvt_pk_f16_f32 v38, v36, v37
	v_cvt_pk_f16_f32 v37, v46, v47
	v_cvt_pk_f16_f32 v36, v44, v45
	v_mad_u64_u32 v[40:41], s[30:31], v115, s26, v[76:77]
	ds_write_b128 v40, v[36:39]

.Lw3b63:
	v_mov_b32_e32 v37, v36
	v_mov_b32_e32 v38, v36
	v_mov_b32_e32 v39, v36
	v_mov_b32_e32 v44, v36
	v_mov_b32_e32 v45, v36
	v_mov_b32_e32 v46, v36
	v_mov_b32_e32 v47, v36

.Lw3b64:
	s_cbranch_vccz .LBB3_91
	ds_bpermute_b32 v123, v87, v116
	ds_bpermute_b32 v122, v88, v116
	ds_bpermute_b32 v121, v89, v116
	ds_bpermute_b32 v120, v90, v116
	ds_bpermute_b32 v119, v91, v116
	ds_bpermute_b32 v118, v92, v116
	s_waitcnt lgkmcnt(5)
	v_lshlrev_b32_e32 v32, 8, v123

.Lw3b65:
	s_waitcnt lgkmcnt(4)
	v_lshlrev_b32_e32 v33, 8, v122
	v_and_or_b32 v32, v32, s27, v81
	v_and_or_b32 v33, v33, s27, v81
	ds_bpermute_b32 v117, v93, v116
	ds_bpermute_b32 v116, v94, v116
	global_load_dwordx4 v[68:71], v32, s[8:9]
	global_load_dwordx4 v[64:67], v33, s[8:9]
	s_waitcnt lgkmcnt(5)

.Lw3b66:
	v_lshlrev_b32_e32 v32, 8, v121
	s_waitcnt lgkmcnt(4)
	v_lshlrev_b32_e32 v33, 8, v120
	v_and_or_b32 v32, v32, s27, v81
	v_and_or_b32 v33, v33, s27, v81
	global_load_dwordx4 v[52:55], v32, s[8:9]
	global_load_dwordx4 v[48:51], v33, s[8:9]
	s_waitcnt lgkmcnt(3)
	v_lshlrev_b32_e32 v32, 8, v119
	s_waitcnt lgkmcnt(2)
	v_lshlrev_b32_e32 v33, 8, v118

.Lw3b67:
	v_and_or_b32 v32, v32, s27, v81
	v_and_or_b32 v33, v33, s27, v81
	global_load_dwordx4 v[44:47], v32, s[8:9]
	global_load_dwordx4 v[40:43], v33, s[8:9]
	s_waitcnt lgkmcnt(1)
	v_lshlrev_b32_e32 v32, 8, v117
	s_waitcnt lgkmcnt(0)
	v_lshlrev_b32_e32 v33, 8, v116
	v_and_or_b32 v32, v32, s27, v81
	v_and_or_b32 v33, v33, s27, v81

.Lw3b68:
	global_load_dwordx4 v[36:39], v32, s[8:9]
	s_nop 0
	global_load_dwordx4 v[32:35], v33, s[8:9]
	v_ashrrev_i32_e32 v123, 17, v123
	v_cmp_ne_u32_e32 vcc, v123, v115
	s_cmp_lg_u64 vcc, 0
	s_cselect_b64 s[22:23], -1, 0
	s_and_b64 s[24:25], s[22:23], vcc
	s_and_saveexec_b64 s[22:23], s[24:25]
	s_cbranch_execz .LBB3_62
	v_cmp_gt_i32_e32 vcc, 16, v115
	s_and_saveexec_b64 s[24:25], vcc

.Lw3b69:
	s_cbranch_execz .LBB3_61
	v_cvt_pk_f16_f32 v59, v58, v59
	v_cvt_pk_f16_f32 v58, v56, v57
	v_cvt_pk_f16_f32 v57, v62, v63
	v_cvt_pk_f16_f32 v56, v60, v61
	v_mad_u64_u32 v[60:61], s[30:31], v115, s26, v[76:77]
	ds_write_b128 v60, v[56:59]

.Lw3b70:
	v_mov_b32_e32 v115, v123
	v_mov_b32_e32 v57, v56
	v_mov_b32_e32 v58, v56
	v_mov_b32_e32 v59, v56
	v_mov_b32_e32 v60, v56
	v_mov_b32_e32 v61, v56
	v_mov_b32_e32 v62, v56
	v_mov_b32_e32 v63, v56

.Lw3b71:
	v_mfma_f32_16x16x16_f16 v[56:59], v[72:73], v[70:71], v[56:59]
	s_and_b64 s[24:25], s[22:23], vcc
	s_and_saveexec_b64 s[22:23], s[24:25]
	s_cbranch_execz .LBB3_66
	v_cmp_gt_i32_e32 vcc, 16, v115
	s_and_saveexec_b64 s[24:25], vcc
	s_cbranch_execz .LBB3_65
	s_nop 1
	v_cvt_pk_f16_f32 v59, v58, v59
	v_cvt_pk_f16_f32 v58, v56, v57
	v_cvt_pk_f16_f32 v57, v62, v63

.Lw3b72:
	v_cvt_pk_f16_f32 v56, v60, v61
	v_mad_u64_u32 v[60:61], s[30:31], v115, s26, v[76:77]
	ds_write_b128 v60, v[56:59]

.Lw3b73:
	v_mov_b32_e32 v61, v56
	v_mov_b32_e32 v62, v56
	v_mov_b32_e32 v63, v56

.Lw3b74:
	s_cbranch_execz .LBB3_70
	v_cmp_gt_i32_e32 vcc, 16, v115
	s_and_saveexec_b64 s[24:25], vcc
	s_cbranch_execz .LBB3_69
	s_nop 1
	v_cvt_pk_f16_f32 v59, v58, v59
	v_cvt_pk_f16_f32 v58, v56, v57
	v_cvt_pk_f16_f32 v57, v62, v63
	v_cvt_pk_f16_f32 v56, v60, v61
	v_mad_u64_u32 v[60:61], s[30:31], v115, s26, v[76:77]

.Lw3b75:
	ds_write_b128 v60, v[56:59]

.Lw3b76:
	s_waitcnt vmcnt(5)
	v_mfma_f32_16x16x16_f16 v[60:63], v[72:73], v[52:53], v[60:63]
	v_cmp_ne_u32_e32 vcc, v64, v115
	s_cmp_lg_u64 vcc, 0
	s_cselect_b64 s[22:23], -1, 0
	v_mfma_f32_16x16x16_f16 v[52:55], v[72:73], v[54:55], v[56:59]
	s_and_b64 s[24:25], s[22:23], vcc
	s_and_saveexec_b64 s[22:23], s[24:25]
	s_cbranch_execz .LBB3_74
	v_cmp_gt_i32_e32 vcc, 16, v115
	s_and_saveexec_b64 s[24:25], vcc
	s_cbranch_execz .LBB3_73
	s_nop 1

.Lw3b77:
	v_cvt_pk_f16_f32 v55, v54, v55
	v_cvt_pk_f16_f32 v54, v52, v53
	v_cvt_pk_f16_f32 v53, v62, v63
	v_cvt_pk_f16_f32 v52, v60, v61
	v_mad_u64_u32 v[56:57], s[30:31], v115, s26, v[76:77]
	ds_write_b128 v56, v[52:55]

.Lw3b78:
	v_mov_b32_e32 v115, v64
	v_mov_b32_e32 v53, v52
	v_mov_b32_e32 v54, v52
	v_mov_b32_e32 v55, v52
	v_mov_b32_e32 v60, v52
	v_mov_b32_e32 v61, v52
	v_mov_b32_e32 v62, v52
	v_mov_b32_e32 v63, v52

.Lw3b79:
	v_mfma_f32_16x16x16_f16 v[48:51], v[72:73], v[50:51], v[52:55]
	s_and_b64 s[24:25], s[22:23], vcc
	s_and_saveexec_b64 s[22:23], s[24:25]
	s_cbranch_execz .LBB3_78
	v_cmp_gt_i32_e32 vcc, 16, v115
	s_and_saveexec_b64 s[24:25], vcc
	s_cbranch_execz .LBB3_77
	s_nop 1
	v_cvt_pk_f16_f32 v51, v50, v51
	v_cvt_pk_f16_f32 v50, v48, v49
	v_cvt_pk_f16_f32 v49, v58, v59

.Lw3b80:
	v_cvt_pk_f16_f32 v48, v56, v57
	v_mad_u64_u32 v[52:53], s[30:31], v115, s26, v[76:77]
	ds_write_b128 v52, v[48:51]

.Lw3b81:
	v_mov_b32_e32 v57, v48
	v_mov_b32_e32 v58, v48
	v_mov_b32_e32 v59, v48

.Lw3b82:
	s_cbranch_execz .LBB3_82
	v_cmp_gt_i32_e32 vcc, 16, v115
	s_and_saveexec_b64 s[24:25], vcc
	s_cbranch_execz .LBB3_81
	s_nop 1
	v_cvt_pk_f16_f32 v47, v46, v47
	v_cvt_pk_f16_f32 v46, v44, v45
	v_cvt_pk_f16_f32 v45, v54, v55
	v_cvt_pk_f16_f32 v44, v52, v53
	v_mad_u64_u32 v[48:49], s[30:31], v115, s26, v[76:77]

.Lw3b83:
	ds_write_b128 v48, v[44:47]

.Lw3b84:
	s_waitcnt vmcnt(2)
	v_mfma_f32_16x16x16_f16 v[48:51], v[72:73], v[40:41], v[52:55]
	v_cmp_ne_u32_e32 vcc, v56, v115
	s_cmp_lg_u64 vcc, 0
	s_cselect_b64 s[22:23], -1, 0
	v_mfma_f32_16x16x16_f16 v[40:43], v[72:73], v[42:43], v[44:47]
	s_and_b64 s[24:25], s[22:23], vcc
	s_and_saveexec_b64 s[22:23], s[24:25]
	s_cbranch_execz .LBB3_86
	v_cmp_gt_i32_e32 vcc, 16, v115
	s_and_saveexec_b64 s[24:25], vcc
	s_cbranch_execz .LBB3_85
	s_nop 1

.Lw3b85:
	v_cvt_pk_f16_f32 v43, v42, v43
	v_cvt_pk_f16_f32 v42, v40, v41
	v_cvt_pk_f16_f32 v41, v50, v51
	v_cvt_pk_f16_f32 v40, v48, v49
	v_mad_u64_u32 v[44:45], s[30:31], v115, s26, v[76:77]
	ds_write_b128 v44, v[40:43]

.Lw3b86:
	v_mov_b32_e32 v115, v56
	v_mov_b32_e32 v41, v40
	v_mov_b32_e32 v42, v40
	v_mov_b32_e32 v43, v40
	v_mov_b32_e32 v48, v40
	v_mov_b32_e32 v49, v40
	v_mov_b32_e32 v50, v40
	v_mov_b32_e32 v51, v40

.Lw3b87:
	v_mfma_f32_16x16x16_f16 v[36:39], v[72:73], v[38:39], v[40:43]
	s_and_b64 s[24:25], s[22:23], vcc
	s_and_saveexec_b64 s[22:23], s[24:25]
	s_cbranch_execz .LBB3_90
	v_cmp_gt_i32_e32 vcc, 16, v115
	s_and_saveexec_b64 s[24:25], vcc
	s_cbranch_execz .LBB3_89
	s_nop 1
	v_cvt_pk_f16_f32 v39, v38, v39
	v_cvt_pk_f16_f32 v38, v36, v37
	v_cvt_pk_f16_f32 v37, v46, v47

.Lw3b88:
	v_cvt_pk_f16_f32 v36, v44, v45
	v_mad_u64_u32 v[40:41], s[30:31], v115, s26, v[76:77]
	ds_write_b128 v40, v[36:39]

.Lw3b89:
	v_mov_b32_e32 v45, v36
	v_mov_b32_e32 v46, v36
	v_mov_b32_e32 v47, v36

.Lw3b90:
	s_cbranch_execz .LBB3_17
	v_cvt_pk_f16_f32 v35, v111, v109
	v_cvt_pk_f16_f32 v34, v112, v110
	v_cvt_pk_f16_f32 v33, v106, v104
	v_cvt_pk_f16_f32 v32, v108, v105
	v_mad_u64_u32 v[36:37], s[22:23], v107, s26, v[76:77]
	ds_write_b128 v36, v[32:35]
	s_branch .LBB3_17

.Lw3b91:
	v_mov_b32_e32 v33, v24
	v_mov_b32_e32 v34, v29
	v_mov_b32_e32 v35, v25
	v_pk_add_f32 v[32:33], v[32:33], v[34:35]
	v_mov_b32_e32 v34, v30
	v_mov_b32_e32 v35, v26
	v_mov_b32_e32 v36, v31
	v_mov_b32_e32 v37, v27
	v_pk_add_f32 v[34:35], v[34:35], v[36:37]
	v_mov_b32_e32 v36, v20
	v_pk_add_f32 v[32:33], v[32:33], v[34:35]
	v_mov_b32_e32 v34, v21

.Lw3b92:
	v_mov_b32_e32 v35, v22
	v_mov_b32_e32 v37, v23
	v_pk_add_f32 v[34:35], v[34:35], v[36:37]
	v_add_f32_e32 v32, 0, v32
	v_pk_add_f32 v[34:35], v[34:35], v[34:35] op_sel:[0,1] op_sel_hi:[1,0]
	v_add_f32_e32 v32, v32, v33
	v_add_f32_e32 v36, v16, v17
	v_add_f32_e32 v38, v18, v19
	v_mov_b32_e32 v33, v12
	v_mov_b32_e32 v35, v13
	v_mov_b32_e32 v37, v14
	v_mov_b32_e32 v39, v15
	v_pk_add_f32 v[32:33], v[32:33], v[34:35]

.Lw3b93:
	v_pk_add_f32 v[34:35], v[36:37], v[38:39]
	v_mov_b32_e32 v36, v8
	v_pk_add_f32 v[32:33], v[32:33], v[34:35]
	v_mov_b32_e32 v34, v9
	v_mov_b32_e32 v35, v10
	v_mov_b32_e32 v37, v11
	v_pk_add_f32 v[34:35], v[34:35], v[36:37]
	v_pk_add_f32 v[32:33], v[32:33], v[32:33] op_sel:[0,1] op_sel_hi:[1,0]
	v_pk_add_f32 v[34:35], v[34:35], v[34:35] op_sel:[0,1] op_sel_hi:[1,0]

.Lw3b94:
	v_add_f32_e32 v36, v4, v5
	v_add_f32_e32 v38, v6, v7
	v_mov_b32_e32 v33, v0
	v_mov_b32_e32 v35, v1
	v_mov_b32_e32 v37, v2
	v_mov_b32_e32 v39, v3
	v_pk_add_f32 v[32:33], v[32:33], v[34:35]
	v_pk_add_f32 v[34:35], v[36:37], v[38:39]
	s_nop 0
	v_pk_add_f32 v[32:33], v[32:33], v[34:35]
	v_and_b32_e32 v34, 64, v100
	v_add_f32_e32 v32, v32, v33

.Lw3b95:
	v_xor_b32_e32 v33, 16, v100
	v_add_u32_e32 v34, 64, v34
	v_cmp_lt_i32_e32 vcc, v33, v34
	s_nop 1
	v_cndmask_b32_e32 v33, v100, v33, vcc
	v_lshlrev_b32_e32 v40, 2, v33
	ds_bpermute_b32 v33, v40, v32
	s_waitcnt lgkmcnt(0)
	v_add_f32_e32 v32, v32, v33
	v_xor_b32_e32 v33, 32, v100
	v_cmp_lt_i32_e32 vcc, v33, v34
	s_nop 1
	v_cndmask_b32_e32 v33, v100, v33, vcc
	v_lshlrev_b32_e32 v41, 2, v33

.Lw3b96:
	ds_bpermute_b32 v33, v41, v32
	s_waitcnt lgkmcnt(0)
	v_add_f32_e32 v42, v32, v33
	v_fmamk_f32 v29, v42, 0xbc000000, v29
	v_fmamk_f32 v25, v42, 0xbc000000, v25
	v_fmamk_f32 v39, v42, 0xbc000000, v31
	v_fmamk_f32 v38, v42, 0xbc000000, v30
	v_fmac_f32_e32 v28, 0xbc000000, v42
	v_fmamk_f32 v37, v42, 0xbc000000, v27

.Lw3b97:
	v_fmac_f32_e32 v24, 0xbc000000, v42
	v_mov_b32_e32 v30, v29
	v_mov_b32_e32 v31, v25
	v_fmamk_f32 v36, v42, 0xbc000000, v26
	v_mov_b32_e32 v26, v28
	v_mov_b32_e32 v27, v24
	v_pk_mul_f32 v[30:31], v[30:31], v[30:31]
	v_mov_b32_e32 v32, v39
	v_mov_b32_e32 v33, v37
	v_pk_fma_f32 v[26:27], v[26:27], v[26:27], v[30:31]

.Lw3b98:
	v_mov_b32_e32 v30, v38
	v_mov_b32_e32 v31, v36
	v_pk_mul_f32 v[32:33], v[32:33], v[32:33]
	v_fmamk_f32 v35, v42, 0xbc000000, v21
	v_pk_fma_f32 v[30:31], v[30:31], v[30:31], v[32:33]
	v_fmamk_f32 v34, v42, 0xbc000000, v20
	v_fmamk_f32 v23, v42, 0xbc000000, v23
	v_fmac_f32_e32 v22, 0xbc000000, v42
	v_pk_add_f32 v[26:27], v[26:27], v[30:31]

.Lw3b99:
	v_pk_mul_f32 v[20:21], v[22:23], v[22:23]
	v_pk_mul_f32 v[30:31], v[34:35], v[34:35]
	v_fmamk_f32 v13, v42, 0xbc000000, v13
	v_pk_mov_b32 v[32:33], v[30:31], v[20:21] op_sel:[1,0]
	v_mov_b32_e32 v31, v21
	v_pk_add_f32 v[20:21], v[32:33], v[30:31]
	v_fmac_f32_e32 v12, 0xbc000000, v42
	v_fmamk_f32 v33, v42, 0xbc000000, v19

.Lw3b100:
	v_fmamk_f32 v32, v42, 0xbc000000, v18
	v_fmamk_f32 v19, v42, 0xbc000000, v15
	v_fmamk_f32 v18, v42, 0xbc000000, v14
	v_mul_f32_e32 v30, v12, v12
	v_mul_f32_e32 v31, v13, v13
	v_pk_add_f32 v[14:15], v[26:27], v[26:27] op_sel:[0,1] op_sel_hi:[1,0]
	v_pk_add_f32 v[20:21], v[20:21], v[20:21] op_sel:[0,1] op_sel_hi:[1,0]
	v_fmamk_f32 v17, v42, 0xbc000000, v17

.Lw3b101:
	v_mov_b32_e32 v15, v30
	v_mov_b32_e32 v21, v31
	v_fmac_f32_e32 v16, 0xbc000000, v42
	v_pk_add_f32 v[14:15], v[14:15], v[20:21]
	v_mul_f32_e32 v20, v17, v17
	v_mul_f32_e32 v26, v33, v33
	v_mul_f32_e32 v43, v18, v18
	v_mul_f32_e32 v44, v19, v19
	v_pk_fma_f32 v[20:21], v[16:17], v[16:17], v[20:21] op_sel_hi:[1,1,0]
	v_pk_fma_f32 v[26:27], v[32:33], v[32:33], v[26:27] op_sel_hi:[1,1,0]
	v_mov_b32_e32 v21, v43

.Lw3b102:
	v_mov_b32_e32 v27, v44
	v_pk_add_f32 v[20:21], v[20:21], v[26:27]
	v_fmamk_f32 v11, v42, 0xbc000000, v11
	v_pk_add_f32 v[14:15], v[14:15], v[20:21]
	v_fmamk_f32 v21, v42, 0xbc000000, v9
	v_fmamk_f32 v20, v42, 0xbc000000, v8
	v_fmac_f32_e32 v10, 0xbc000000, v42
	v_pk_mul_f32 v[8:9], v[10:11], v[10:11]

.Lw3b103:
	v_pk_mul_f32 v[26:27], v[20:21], v[20:21]
	v_fmamk_f32 v1, v42, 0xbc000000, v1
	v_pk_mov_b32 v[30:31], v[26:27], v[8:9] op_sel:[1,0]
	v_mov_b32_e32 v27, v9
	v_pk_add_f32 v[8:9], v[30:31], v[26:27]
	v_fmac_f32_e32 v0, 0xbc000000, v42
	v_fmamk_f32 v27, v42, 0xbc000000, v7
	v_fmamk_f32 v26, v42, 0xbc000000, v6

.Lw3b104:
	v_mul_f32_e32 v30, v0, v0
	v_mul_f32_e32 v31, v1, v1
	v_pk_add_f32 v[6:7], v[14:15], v[14:15] op_sel:[0,1] op_sel_hi:[1,0]
	v_pk_add_f32 v[8:9], v[8:9], v[8:9] op_sel:[0,1] op_sel_hi:[1,0]
	v_fmamk_f32 v5, v42, 0xbc000000, v5
	v_mov_b32_e32 v7, v30
	v_mov_b32_e32 v9, v31
	v_fmac_f32_e32 v4, 0xbc000000, v42
	v_fmamk_f32 v3, v42, 0xbc000000, v3
	v_fmamk_f32 v2, v42, 0xbc000000, v2

.Lw3b105:
	v_pk_add_f32 v[6:7], v[6:7], v[8:9]
	v_mul_f32_e32 v8, v5, v5
	v_mul_f32_e32 v14, v27, v27
	v_mul_f32_e32 v42, v2, v2
	v_mul_f32_e32 v43, v3, v3
	v_pk_fma_f32 v[8:9], v[4:5], v[4:5], v[8:9] op_sel_hi:[1,1,0]
	v_pk_fma_f32 v[14:15], v[26:27], v[26:27], v[14:15] op_sel_hi:[1,1,0]
	v_mov_b32_e32 v9, v42
	v_mov_b32_e32 v15, v43
	v_pk_add_f32 v[8:9], v[8:9], v[14:15]

.Lw3b106:
	s_nop 0
	v_pk_add_f32 v[6:7], v[6:7], v[8:9]
	s_nop 0
	v_add_f32_e32 v6, v6, v7
	ds_bpermute_b32 v7, v40, v6
	s_waitcnt lgkmcnt(0)
	v_add_f32_e32 v6, v6, v7
	ds_bpermute_b32 v7, v41, v6
	s_waitcnt lgkmcnt(0)
	v_add_f32_e32 v6, v6, v7
	v_fmamk_f32 v6, v6, 0x3c000000, v98

.Lw3b107:
	v_mul_f32_e32 v7, 0x4b800000, v6
	v_cmp_gt_f32_e32 vcc, s28, v6
	s_nop 1
	v_cndmask_b32_e32 v6, v6, v7, vcc
	v_rsq_f32_e32 v14, v6
	ds_read_b128 v[6:9], v96 offset:512
	ds_read_b128 v[40:43], v96 offset:528
	ds_read_b128 v[44:47], v96 offset:1024
	ds_read_b128 v[48:51], v96 offset:1040
	v_mul_f32_e32 v15, 0x45800000, v14

.Lw3b108:
	v_cndmask_b32_e32 v30, v14, v15, vcc
	v_pk_mul_f32 v[14:15], v[30:31], v[28:29] op_sel_hi:[0,1]
	s_waitcnt lgkmcnt(1)
	v_pk_fma_f32 v[6:7], v[6:7], v[14:15], v[44:45]
	v_pk_mul_f32 v[28:29], v[30:31], v[38:39] op_sel_hi:[0,1]
	v_pk_mul_f32 v[14:15], v[6:7], v[6:7]
	v_pk_fma_f32 v[8:9], v[8:9], v[28:29], v[46:47]
	v_fmamk_f32 v14, v14, 0xbdd2d3e8, v99

.Lw3b109:
	v_fmamk_f32 v15, v15, 0xbdd2d3e8, v99
	v_mul_f32_e32 v14, v6, v14
	v_mul_f32_e32 v15, v7, v15
	v_exp_f32_e32 v14, v14
	v_exp_f32_e32 v15, v15
	v_pk_mul_f32 v[28:29], v[8:9], v[8:9]
	v_add_f32_e32 v14, 1.0, v14
	v_add_f32_e32 v15, 1.0, v15
	v_rcp_f32_e32 v14, v14
	v_rcp_f32_e32 v15, v15
	v_fmamk_f32 v28, v28, 0xbdd2d3e8, v99
	v_mul_f32_e32 v28, v8, v28

.Lw3b110:
	v_exp_f32_e32 v28, v28
	v_pk_mul_f32 v[6:7], v[6:7], v[14:15]
	v_fmamk_f32 v14, v29, 0xbdd2d3e8, v99
	v_mul_f32_e32 v14, v9, v14
	v_exp_f32_e32 v29, v14
	v_pk_mul_f32 v[14:15], v[30:31], v[24:25] op_sel_hi:[0,1]
	s_waitcnt lgkmcnt(0)
	v_pk_fma_f32 v[14:15], v[40:41], v[14:15], v[48:49]
	v_cvt_pk_f16_f32 v6, v6, v7
	v_pk_mul_f32 v[24:25], v[14:15], v[14:15]

.Lw3b111:
	v_add_f32_e32 v7, 1.0, v28
	v_fmamk_f32 v24, v24, 0xbdd2d3e8, v99
	v_mul_f32_e32 v24, v14, v24
	v_exp_f32_e32 v24, v24
	v_rcp_f32_e32 v28, v7
	v_add_f32_e32 v7, 1.0, v29
	v_rcp_f32_e32 v29, v7
	v_add_f32_e32 v7, 1.0, v24
	v_fmamk_f32 v24, v25, 0xbdd2d3e8, v99
	v_mul_f32_e32 v31, v15, v24
	v_pk_mul_f32 v[24:25], v[30:31], v[36:37] op_sel_hi:[0,1]

.Lw3b112:
	v_pk_fma_f32 v[24:25], v[42:43], v[24:25], v[50:51]
	v_exp_f32_e32 v31, v31
	v_pk_mul_f32 v[36:37], v[24:25], v[24:25]
	v_rcp_f32_e32 v38, v7
	v_fmamk_f32 v36, v36, 0xbdd2d3e8, v99
	v_fmamk_f32 v37, v37, 0xbdd2d3e8, v99
	v_mul_f32_e32 v36, v24, v36
	v_mul_f32_e32 v37, v25, v37
	v_exp_f32_e32 v36, v36
	v_exp_f32_e32 v37, v37
	v_add_f32_e32 v7, 1.0, v31

.Lw3b113:
	v_mov_b32_e32 v31, v84
	v_add_f32_e32 v36, 1.0, v36
	v_add_f32_e32 v37, 1.0, v37
	v_rcp_f32_e32 v36, v36
	v_rcp_f32_e32 v37, v37
	v_rcp_f32_e32 v39, v7
	v_pk_mul_f32 v[8:9], v[8:9], v[28:29]
	v_pk_mul_f32 v[24:25], v[24:25], v[36:37]
	s_nop 0
	s_nop 0
	v_lshl_add_u32 v7, v31, 2, v101
	v_add_u32_e32 v52, 0x420, v7

.Lw3b114:
	v_add_u32_e32 v46, 0x428, v7
	v_add_u32_e32 v50, 0x430, v7
	ds_read2_b32 v[36:37], v7 offset0:138 offset1:139
	ds_read2_b32 v[40:41], v7 offset0:142 offset1:143
	ds_read2_b32 v[42:43], v7 offset0:140 offset1:141
	ds_read2_b32 v[44:45], v7 offset0:136 offset1:137
	v_add_u32_e32 v7, 0x438, v7

.Lw3b115:
	ds_read2_b32 v[46:47], v46 offset1:1
	ds_read2_b32 v[48:49], v7 offset1:1
	ds_read2_b32 v[50:51], v50 offset1:1
	ds_read2_b32 v[52:53], v52 offset1:1
	v_cvt_pk_f16_f32 v7, v8, v9
	v_pk_mul_f32 v[8:9], v[14:15], v[38:39]
	s_nop 0
	v_cvt_pk_f16_f32 v8, v8, v9

.Lw3b116:
	v_pk_mul_f32 v[14:15], v[30:31], v[34:35] op_sel_hi:[0,1]
	s_waitcnt lgkmcnt(0)
	v_pk_fma_f32 v[14:15], v[44:45], v[14:15], v[52:53]
	v_pk_mul_f32 v[22:23], v[30:31], v[22:23] op_sel_hi:[0,1]
	v_pk_mul_f32 v[28:29], v[14:15], v[14:15]
	v_pk_fma_f32 v[22:23], v[36:37], v[22:23], v[46:47]
	v_fmamk_f32 v9, v28, 0xbdd2d3e8, v99
	v_mul_f32_e32 v9, v14, v9
	v_fmamk_f32 v28, v29, 0xbdd2d3e8, v99

.Lw3b117:
	v_exp_f32_e32 v9, v9
	v_mul_f32_e32 v28, v15, v28
	v_exp_f32_e32 v29, v28
	v_pk_mul_f32 v[34:35], v[22:23], v[22:23]
	v_add_f32_e32 v9, 1.0, v9
	v_rcp_f32_e32 v28, v9
	v_add_f32_e32 v9, 1.0, v29
	v_rcp_f32_e32 v29, v9
	v_fmamk_f32 v9, v34, 0xbdd2d3e8, v99
	v_mul_f32_e32 v9, v22, v9
	v_exp_f32_e32 v34, v9
	v_cvt_pk_f16_f32 v9, v24, v25

.Lw3b118:
	v_fmamk_f32 v24, v35, 0xbdd2d3e8, v99
	v_pk_mul_f32 v[16:17], v[30:31], v[16:17] op_sel_hi:[0,1]
	v_mul_f32_e32 v24, v23, v24
	v_pk_fma_f32 v[16:17], v[42:43], v[16:17], v[50:51]
	v_pk_mul_f32 v[14:15], v[14:15], v[28:29]
	v_exp_f32_e32 v29, v24
	v_pk_mul_f32 v[24:25], v[16:17], v[16:17]
	v_cvt_pk_f16_f32 v14, v14, v15

.Lw3b119:
	v_fmamk_f32 v24, v24, 0xbdd2d3e8, v99
	v_mul_f32_e32 v24, v16, v24
	v_exp_f32_e32 v24, v24
	v_add_f32_e32 v15, 1.0, v34
	v_rcp_f32_e32 v28, v15
	v_add_f32_e32 v15, 1.0, v29
	v_rcp_f32_e32 v29, v15
	v_add_f32_e32 v15, 1.0, v24
	v_fmamk_f32 v24, v25, 0xbdd2d3e8, v99
	v_mul_f32_e32 v34, v17, v24
	v_pk_mul_f32 v[24:25], v[30:31], v[32:33] op_sel_hi:[0,1]
	v_pk_fma_f32 v[24:25], v[40:41], v[24:25], v[48:49]

.Lw3b120:
	v_exp_f32_e32 v35, v34
	v_pk_mul_f32 v[32:33], v[24:25], v[24:25]
	v_rcp_f32_e32 v34, v15
	v_fmamk_f32 v32, v32, 0xbdd2d3e8, v99
	v_fmamk_f32 v33, v33, 0xbdd2d3e8, v99
	v_mul_f32_e32 v32, v24, v32
	v_mul_f32_e32 v33, v25, v33
	v_exp_f32_e32 v32, v32
	v_exp_f32_e32 v33, v33
	v_add_f32_e32 v15, 1.0, v35
	v_rcp_f32_e32 v35, v15

.Lw3b121:
	v_add_f32_e32 v32, 1.0, v32
	v_add_f32_e32 v33, 1.0, v33
	v_rcp_f32_e32 v32, v32
	v_rcp_f32_e32 v33, v33
	v_pk_mul_f32 v[22:23], v[22:23], v[28:29]
	v_pk_mul_f32 v[16:17], v[16:17], v[34:35]
	v_pk_mul_f32 v[24:25], v[24:25], v[32:33]
	s_nop 0
	v_cvt_pk_f16_f32 v16, v16, v17
	v_lshl_add_u32 v15, v31, 2, v101

.Lw3b122:
	v_add_u32_e32 v48, 0x440, v15
	v_add_u32_e32 v42, 0x448, v15
	v_add_u32_e32 v46, 0x450, v15
	ds_read2_b32 v[32:33], v15 offset0:146 offset1:147
	ds_read2_b32 v[36:37], v15 offset0:150 offset1:151
	ds_read2_b32 v[38:39], v15 offset0:148 offset1:149
	ds_read2_b32 v[40:41], v15 offset0:144 offset1:145
	v_add_u32_e32 v15, 0x458, v15

.Lw3b123:
	ds_read2_b32 v[42:43], v42 offset1:1
	ds_read2_b32 v[44:45], v15 offset1:1
	ds_read2_b32 v[46:47], v46 offset1:1
	ds_read2_b32 v[48:49], v48 offset1:1
	v_cvt_pk_f16_f32 v15, v22, v23
	v_pk_mul_f32 v[12:13], v[30:31], v[12:13] op_sel_hi:[0,1]
	s_waitcnt lgkmcnt(0)
	v_pk_fma_f32 v[12:13], v[40:41], v[12:13], v[48:49]

.Lw3b124:
	v_pk_mul_f32 v[18:19], v[30:31], v[18:19] op_sel_hi:[0,1]
	v_pk_mul_f32 v[22:23], v[12:13], v[12:13]
	v_pk_fma_f32 v[28:29], v[32:33], v[18:19], v[42:43]
	v_fmamk_f32 v17, v22, 0xbdd2d3e8, v99
	v_mul_f32_e32 v17, v12, v17
	v_fmamk_f32 v22, v23, 0xbdd2d3e8, v99
	v_exp_f32_e32 v17, v17
	v_mul_f32_e32 v22, v13, v22
	v_exp_f32_e32 v23, v22

.Lw3b125:
	v_pk_mul_f32 v[18:19], v[28:29], v[28:29]
	v_add_f32_e32 v17, 1.0, v17
	v_rcp_f32_e32 v22, v17
	v_add_f32_e32 v17, 1.0, v23
	v_rcp_f32_e32 v23, v17
	v_fmamk_f32 v17, v18, 0xbdd2d3e8, v99
	v_pk_mul_f32 v[10:11], v[30:31], v[10:11] op_sel_hi:[0,1]
	v_mul_f32_e32 v17, v28, v17
	v_pk_mul_f32 v[12:13], v[12:13], v[22:23]
	v_pk_fma_f32 v[10:11], v[36:37], v[10:11], v[44:45]

.Lw3b126:
	v_cvt_pk_f16_f32 v18, v12, v13
	v_fmamk_f32 v12, v19, 0xbdd2d3e8, v99
	v_mul_f32_e32 v12, v29, v12
	v_exp_f32_e32 v19, v12
	v_pk_mul_f32 v[12:13], v[30:31], v[20:21] op_sel_hi:[0,1]
	v_pk_fma_f32 v[12:13], v[38:39], v[12:13], v[46:47]
	v_exp_f32_e32 v32, v17
	v_pk_mul_f32 v[20:21], v[12:13], v[12:13]
	v_add_f32_e32 v19, 1.0, v19
	v_fmamk_f32 v20, v20, 0xbdd2d3e8, v99

.Lw3b127:
	v_mul_f32_e32 v20, v12, v20
	v_exp_f32_e32 v20, v20
	v_rcp_f32_e32 v23, v19
	v_cvt_pk_f16_f32 v17, v24, v25
	v_add_f32_e32 v22, 1.0, v32
	v_add_f32_e32 v19, 1.0, v20
	v_fmamk_f32 v20, v21, 0xbdd2d3e8, v99
	v_mul_f32_e32 v24, v13, v20
	v_pk_mul_f32 v[20:21], v[10:11], v[10:11]
	v_exp_f32_e32 v25, v24
	v_fmamk_f32 v20, v20, 0xbdd2d3e8, v99

.Lw3b128:
	v_fmamk_f32 v21, v21, 0xbdd2d3e8, v99
	v_mul_f32_e32 v20, v10, v20
	v_mul_f32_e32 v21, v11, v21
	v_exp_f32_e32 v20, v20
	v_exp_f32_e32 v21, v21
	v_rcp_f32_e32 v24, v19
	v_add_f32_e32 v19, 1.0, v25
	v_add_f32_e32 v20, 1.0, v20
	v_add_f32_e32 v21, 1.0, v21
	v_rcp_f32_e32 v20, v20
	v_rcp_f32_e32 v21, v21
	v_rcp_f32_e32 v25, v19
	v_rcp_f32_e32 v22, v22

.Lw3b129:
	v_pk_mul_f32 v[10:11], v[10:11], v[20:21]
	s_nop 0
	v_pk_mul_f32 v[12:13], v[12:13], v[24:25]
	v_lshl_add_u32 v19, v31, 2, v101
	v_add_u32_e32 v21, 0x468, v19
	ds_read2_b32 v[32:33], v19 offset0:154 offset1:155
	ds_read2_b32 v[34:35], v19 offset0:158 offset1:159
	ds_read2_b32 v[36:37], v19 offset0:156 offset1:157

.Lw3b130:
	ds_read2_b32 v[38:39], v19 offset0:152 offset1:153
	v_add_u32_e32 v20, 0x460, v19
	v_add_u32_e32 v31, 0x470, v19
	v_add_u32_e32 v19, 0x478, v19
	ds_read2_b32 v[40:41], v21 offset1:1
	ds_read2_b32 v[42:43], v19 offset1:1
	ds_read2_b32 v[44:45], v31 offset1:1
	ds_read2_b32 v[46:47], v20 offset1:1

.Lw3b131:
	v_pk_mul_f32 v[20:21], v[28:29], v[22:23]
	s_nop 0
	v_cvt_pk_f16_f32 v19, v20, v21
	v_cvt_pk_f16_f32 v20, v12, v13
	v_pk_mul_f32 v[4:5], v[30:31], v[4:5] op_sel_hi:[0,1]
	s_waitcnt lgkmcnt(0)
	v_pk_fma_f32 v[4:5], v[38:39], v[4:5], v[46:47]
	v_cvt_pk_f16_f32 v21, v10, v11

.Lw3b132:
	v_pk_mul_f32 v[12:13], v[4:5], v[4:5]
	v_pk_mul_f32 v[10:11], v[30:31], v[26:27] op_sel_hi:[0,1]
	v_fmamk_f32 v12, v12, 0xbdd2d3e8, v99
	v_fmamk_f32 v13, v13, 0xbdd2d3e8, v99
	v_mul_f32_e32 v12, v4, v12
	v_mul_f32_e32 v13, v5, v13
	v_exp_f32_e32 v12, v12
	v_exp_f32_e32 v13, v13
	v_pk_fma_f32 v[10:11], v[32:33], v[10:11], v[40:41]
	v_pk_mul_f32 v[0:1], v[30:31], v[0:1] op_sel_hi:[0,1]

.Lw3b133:
	v_add_f32_e32 v12, 1.0, v12
	v_add_f32_e32 v13, 1.0, v13
	v_rcp_f32_e32 v12, v12
	v_rcp_f32_e32 v13, v13
	v_pk_fma_f32 v[0:1], v[36:37], v[0:1], v[44:45]
	v_pk_mul_f32 v[2:3], v[30:31], v[2:3] op_sel_hi:[0,1]
	v_pk_fma_f32 v[2:3], v[34:35], v[2:3], v[42:43]
	v_pk_mul_f32 v[4:5], v[4:5], v[12:13]
	v_pk_mul_f32 v[12:13], v[10:11], v[10:11]

.Lw3b134:
	v_cvt_pk_f16_f32 v24, v4, v5
	v_fmamk_f32 v12, v12, 0xbdd2d3e8, v99
	v_fmamk_f32 v13, v13, 0xbdd2d3e8, v99
	v_mul_f32_e32 v12, v10, v12
	v_mul_f32_e32 v13, v11, v13
	v_exp_f32_e32 v12, v12
	v_exp_f32_e32 v13, v13
	v_add_f32_e32 v4, 1.0, v12
	v_add_f32_e32 v5, 1.0, v13
	v_pk_mul_f32 v[12:13], v[0:1], v[0:1]
	v_rcp_f32_e32 v4, v4

.Lw3b135:
	v_fmamk_f32 v12, v12, 0xbdd2d3e8, v99
	v_fmamk_f32 v13, v13, 0xbdd2d3e8, v99
	v_mul_f32_e32 v12, v0, v12
	v_mul_f32_e32 v13, v1, v13
	v_rcp_f32_e32 v5, v5
	v_exp_f32_e32 v12, v12
	v_exp_f32_e32 v13, v13
	v_pk_mul_f32 v[4:5], v[10:11], v[4:5]
	v_add_f32_e32 v10, 1.0, v12
	v_add_f32_e32 v11, 1.0, v13
	v_pk_mul_f32 v[12:13], v[2:3], v[2:3]

.Lw3b136:
	v_rcp_f32_e32 v10, v10
	v_fmamk_f32 v12, v12, 0xbdd2d3e8, v99
	v_fmamk_f32 v13, v13, 0xbdd2d3e8, v99
	v_mul_f32_e32 v12, v2, v12
	v_mul_f32_e32 v13, v3, v13
	v_exp_f32_e32 v12, v12
	v_exp_f32_e32 v13, v13
	v_rcp_f32_e32 v11, v11
	v_cvt_pk_f16_f32 v25, v4, v5
	v_add_f32_e32 v12, 1.0, v12
	v_add_f32_e32 v13, 1.0, v13
	v_rcp_f32_e32 v12, v12

.Lw3b137:
	v_rcp_f32_e32 v13, v13
	v_pk_mul_f32 v[0:1], v[0:1], v[10:11]
	s_nop 0
	v_cvt_pk_f16_f32 v26, v0, v1
	v_pk_mul_f32 v[0:1], v[2:3], v[12:13]
	s_nop 0
	v_cvt_pk_f16_f32 v27, v0, v1
	ds_read_b128 v[0:3], v96 offset:1536
	ds_read_b128 v[10:13], v96 offset:1552

.Lw3b138:
	ds_read_b128 v[30:33], v96 offset:1568
	ds_read_b128 v[34:37], v96 offset:1584
	ds_read_b128 v[38:41], v96 offset:1600
	ds_read_b128 v[42:45], v96 offset:1616
	ds_read_b128 v[46:49], v96 offset:1632
	ds_read_b128 v[50:53], v96 offset:1648
	v_mov_b32_e32 v4, v77
	s_nop 0
	v_lshl_add_u32 v28, v4, 4, v102

.Lw3b139:
	ds_read_b128 v[54:57], v28
	ds_read_b128 v[58:61], v28 offset:1024
	ds_read_b128 v[62:65], v28 offset:2048
	ds_read_b128 v[66:69], v28 offset:3072
	ds_read_b128 v[104:107], v28 offset:4096
	ds_read_b128 v[108:111], v28 offset:5120
	ds_read_b128 v[112:115], v28 offset:6144

.Lw3b140:
	ds_read_b128 v[116:119], v28 offset:7168
	s_waitcnt lgkmcnt(7)
	v_mfma_f32_16x16x32_f16 v[0:3], v[54:57], v[6:9], v[0:3]
	s_waitcnt lgkmcnt(6)
	v_mfma_f32_16x16x32_f16 v[10:13], v[58:61], v[6:9], v[10:13]
	s_waitcnt lgkmcnt(5)
	v_mfma_f32_16x16x32_f16 v[30:33], v[62:65], v[6:9], v[30:33]
	s_waitcnt lgkmcnt(4)
	v_mfma_f32_16x16x32_f16 v[34:37], v[66:69], v[6:9], v[34:37]
	ds_read_b128 v[54:57], v28 offset:8192

.Lw3b141:
	ds_read_b128 v[58:61], v28 offset:9216
	ds_read_b128 v[62:65], v28 offset:10240
	ds_read_b128 v[66:69], v28 offset:11264
	s_waitcnt lgkmcnt(7)
	v_mfma_f32_16x16x32_f16 v[38:41], v[104:107], v[6:9], v[38:41]
	s_waitcnt lgkmcnt(6)
	v_mfma_f32_16x16x32_f16 v[42:45], v[108:111], v[6:9], v[42:45]
	s_waitcnt lgkmcnt(5)
	v_mfma_f32_16x16x32_f16 v[46:49], v[112:115], v[6:9], v[46:49]

.Lw3b142:
	s_waitcnt lgkmcnt(4)
	v_mfma_f32_16x16x32_f16 v[4:7], v[116:119], v[6:9], v[50:53]
	s_nop 2
	ds_read_b128 v[50:53], v28 offset:12288
	ds_read_b128 v[104:107], v28 offset:13312
	ds_read_b128 v[108:111], v28 offset:14336
	ds_read_b128 v[112:115], v28 offset:15360
	s_waitcnt lgkmcnt(7)
	v_mfma_f32_16x16x32_f16 v[0:3], v[54:57], v[14:17], v[0:3]

.Lw3b143:
	s_waitcnt lgkmcnt(6)
	v_mfma_f32_16x16x32_f16 v[8:11], v[58:61], v[14:17], v[10:13]
	s_waitcnt lgkmcnt(5)
	v_mfma_f32_16x16x32_f16 v[30:33], v[62:65], v[14:17], v[30:33]
	s_waitcnt lgkmcnt(4)
	v_mfma_f32_16x16x32_f16 v[34:37], v[66:69], v[14:17], v[34:37]
	ds_read_b128 v[54:57], v28 offset:16384
	ds_read_b128 v[58:61], v28 offset:17408
	ds_read_b128 v[62:65], v28 offset:18432

.Lw3b144:
	ds_read_b128 v[66:69], v28 offset:19456
	s_waitcnt lgkmcnt(7)
	v_mfma_f32_16x16x32_f16 v[38:41], v[50:53], v[14:17], v[38:41]
	s_waitcnt lgkmcnt(6)
	v_mfma_f32_16x16x32_f16 v[42:45], v[104:107], v[14:17], v[42:45]
	s_waitcnt lgkmcnt(5)
	v_mfma_f32_16x16x32_f16 v[46:49], v[108:111], v[14:17], v[46:49]
	s_waitcnt lgkmcnt(4)
	v_mfma_f32_16x16x32_f16 v[4:7], v[112:115], v[14:17], v[4:7]

.Lw3b145:
	ds_read_b128 v[12:15], v28 offset:20480
	ds_read_b128 v[50:53], v28 offset:21504
	ds_read_b128 v[104:107], v28 offset:22528
	ds_read_b128 v[108:111], v28 offset:23552
	s_waitcnt lgkmcnt(7)
	v_mfma_f32_16x16x32_f16 v[0:3], v[54:57], v[18:21], v[0:3]
	s_waitcnt lgkmcnt(6)
	v_mfma_f32_16x16x32_f16 v[8:11], v[58:61], v[18:21], v[8:11]
	s_waitcnt lgkmcnt(5)

.Lw3b146:
	v_mfma_f32_16x16x32_f16 v[30:33], v[62:65], v[18:21], v[30:33]
	s_waitcnt lgkmcnt(4)
	v_mfma_f32_16x16x32_f16 v[34:37], v[66:69], v[18:21], v[34:37]
	ds_read_b128 v[54:57], v28 offset:24576
	ds_read_b128 v[58:61], v28 offset:25600
	ds_read_b128 v[62:65], v28 offset:26624
	ds_read_b128 v[66:69], v28 offset:27648
	s_waitcnt lgkmcnt(7)
	v_mfma_f32_16x16x32_f16 v[12:15], v[12:15], v[18:21], v[38:41]

.Lw3b147:
	s_waitcnt lgkmcnt(6)
	v_mfma_f32_16x16x32_f16 v[38:41], v[50:53], v[18:21], v[42:45]
	s_waitcnt lgkmcnt(5)
	v_mfma_f32_16x16x32_f16 v[42:45], v[104:107], v[18:21], v[46:49]
	s_waitcnt lgkmcnt(4)
	v_mfma_f32_16x16x32_f16 v[46:49], v[108:111], v[18:21], v[4:7]
	s_nop 2
	ds_read_b128 v[4:7], v28 offset:28672
	ds_read_b128 v[50:53], v28 offset:29696

.Lw3b148:
	ds_read_b128 v[104:107], v28 offset:30720
	ds_read_b128 v[108:111], v28 offset:31744
	s_waitcnt lgkmcnt(7)
	v_mfma_f32_16x16x32_f16 v[54:57], v[54:57], v[24:27], v[0:3]
	s_waitcnt lgkmcnt(6)
	v_mfma_f32_16x16x32_f16 v[58:61], v[58:61], v[24:27], v[8:11]
	s_waitcnt lgkmcnt(5)
	v_mfma_f32_16x16x32_f16 v[20:23], v[62:65], v[24:27], v[30:33]
	s_waitcnt lgkmcnt(4)
	v_mfma_f32_16x16x32_f16 v[16:19], v[66:69], v[24:27], v[34:37]

.Lw3b149:
	s_waitcnt lgkmcnt(0)
	v_mfma_f32_16x16x32_f16 v[0:3], v[108:111], v[24:27], v[46:49]
	v_mfma_f32_16x16x32_f16 v[12:15], v[4:7], v[24:27], v[12:15]
	v_mfma_f32_16x16x32_f16 v[8:11], v[50:53], v[24:27], v[38:41]
	v_mfma_f32_16x16x32_f16 v[4:7], v[104:107], v[24:27], v[42:45]
	v_mul_f32_e32 v24, v54, v54
	v_fmamk_f32 v24, v24, 0xbdd2d3e8, v99
	v_mul_f32_e32 v24, v54, v24
	v_exp_f32_e32 v24, v24

.Lw3b150:
	v_mul_f32_e32 v25, v55, v55
	v_mul_f32_e32 v26, v56, v56
	v_fmamk_f32 v25, v25, 0xbdd2d3e8, v99
	v_fmamk_f32 v26, v26, 0xbdd2d3e8, v99
	v_mul_f32_e32 v25, v55, v25
	v_add_f32_e32 v24, 1.0, v24
	v_mul_f32_e32 v26, v56, v26
	v_rcp_f32_e32 v24, v24
	v_exp_f32_e32 v25, v25
	v_exp_f32_e32 v26, v26
	v_mul_f32_e32 v30, v57, v57
	v_mul_f32_e32 v31, v58, v58
	v_fmamk_f32 v30, v30, 0xbdd2d3e8, v99

.Lw3b151:
	v_fmamk_f32 v31, v31, 0xbdd2d3e8, v99
	v_fma_mixlo_f16 v29, v54, v24, 0
	v_add_f32_e32 v24, 1.0, v25
	v_add_f32_e32 v25, 1.0, v26
	v_mul_f32_e32 v30, v57, v30
	v_mul_f32_e32 v31, v58, v31
	v_rcp_f32_e32 v24, v24
	v_rcp_f32_e32 v25, v25
	v_exp_f32_e32 v30, v30
	v_exp_f32_e32 v31, v31
	v_mov_b32_e32 v26, v55
	v_mov_b32_e32 v27, v56

.Lw3b152:
	v_pk_mul_f32 v[24:25], v[26:27], v[24:25]
	v_add_f32_e32 v26, 1.0, v30
	v_add_f32_e32 v27, 1.0, v31
	v_rcp_f32_e32 v26, v26
	v_rcp_f32_e32 v27, v27
	v_cvt_pk_f16_f32 v25, v24, v25
	v_pk_mov_b32 v[30:31], v[56:57], v[58:59] op_sel:[1,0]
	v_pack_b32_f16 v24, v29, v25
	v_pk_mul_f32 v[26:27], v[30:31], v[26:27]
	v_mul_f32_e32 v29, v59, v59

.Lw3b153:
	v_mul_f32_e32 v30, v60, v60
	v_fmamk_f32 v29, v29, 0xbdd2d3e8, v99
	v_fmamk_f32 v30, v30, 0xbdd2d3e8, v99
	v_mul_f32_e32 v29, v59, v29
	v_mul_f32_e32 v30, v60, v30
	v_exp_f32_e32 v29, v29
	v_exp_f32_e32 v30, v30
	v_cvt_pk_f16_f32 v32, v26, v27
	v_mov_b32_e32 v31, v60
	v_add_f32_e32 v26, 1.0, v29
	v_add_f32_e32 v27, 1.0, v30
	v_rcp_f32_e32 v26, v26

.Lw3b154:
	v_rcp_f32_e32 v27, v27
	v_mov_b32_e32 v30, v59
	v_alignbit_b32 v25, v32, v25, 16
	v_mul_f32_e32 v34, v20, v20
	v_pk_mul_f32 v[26:27], v[30:31], v[26:27]
	v_fmamk_f32 v34, v34, 0xbdd2d3e8, v99
	v_cvt_pk_f16_f32 v27, v26, v27
	v_mul_f32_e32 v26, v61, v61
	v_fmamk_f32 v26, v26, 0xbdd2d3e8, v99
	v_mul_f32_e32 v26, v61, v26

.Lw3b155:
	v_exp_f32_e32 v29, v26
	v_alignbit_b32 v26, v27, v32, 16
	ds_read_b128 v[30:33], v28 offset:32768
	v_mul_f32_e32 v34, v20, v34
	v_add_f32_e32 v29, 1.0, v29
	v_rcp_f32_e32 v29, v29
	v_lshrrev_b32_e32 v27, 16, v27
	v_exp_f32_e32 v38, v34
	ds_read_b128 v[34:37], v28 offset:33792
	v_fma_mixhi_f16 v27, v61, v29, 0
	v_add_f32_e32 v29, 1.0, v38

.Lw3b156:
	s_waitcnt lgkmcnt(1)
	v_mfma_f32_16x16x32_f16 v[24:27], v[30:33], v[24:27], 0
	v_mul_f32_e32 v30, v21, v21
	v_fmamk_f32 v30, v30, 0xbdd2d3e8, v99
	v_mul_f32_e32 v31, v22, v22
	v_mul_f32_e32 v30, v21, v30
	v_fmamk_f32 v31, v31, 0xbdd2d3e8, v99
	v_rcp_f32_e32 v29, v29
	v_exp_f32_e32 v30, v30
	v_mul_f32_e32 v31, v22, v31
	v_exp_f32_e32 v31, v31
	v_fma_mixlo_f16 v29, v20, v29, 0

.Lw3b157:
	v_add_f32_e32 v20, 1.0, v30
	v_rcp_f32_e32 v30, v20
	v_add_f32_e32 v20, 1.0, v31
	v_rcp_f32_e32 v31, v20
	v_mov_b32_e32 v20, v21
	v_mov_b32_e32 v21, v22
	v_mul_f32_e32 v22, v23, v23
	v_fmamk_f32 v22, v22, 0xbdd2d3e8, v99
	v_mul_f32_e32 v32, v16, v16
	v_mul_f32_e32 v22, v23, v22
	v_fmamk_f32 v32, v32, 0xbdd2d3e8, v99
	v_exp_f32_e32 v22, v22

.Lw3b158:
	v_mul_f32_e32 v32, v16, v32
	v_exp_f32_e32 v32, v32
	v_pk_mul_f32 v[20:21], v[20:21], v[30:31]
	v_add_f32_e32 v22, 1.0, v22
	v_rcp_f32_e32 v30, v22
	v_add_f32_e32 v22, 1.0, v32
	v_rcp_f32_e32 v31, v22
	v_pk_mov_b32 v[22:23], v[22:23], v[16:17] op_sel:[1,0]
	v_cvt_pk_f16_f32 v21, v20, v21
	v_mul_f32_e32 v16, v17, v17
	v_pk_mul_f32 v[22:23], v[22:23], v[30:31]

.Lw3b159:
	v_pack_b32_f16 v20, v29, v21
	v_cvt_pk_f16_f32 v29, v22, v23
	v_fmamk_f32 v16, v16, 0xbdd2d3e8, v99
	v_mul_f32_e32 v22, v18, v18
	v_mul_f32_e32 v16, v17, v16
	v_fmamk_f32 v22, v22, 0xbdd2d3e8, v99
	v_exp_f32_e32 v16, v16
	v_mul_f32_e32 v22, v18, v22
	v_exp_f32_e32 v23, v22
	v_alignbit_b32 v21, v29, v21, 16

.Lw3b160:
	v_add_f32_e32 v16, 1.0, v16
	v_rcp_f32_e32 v22, v16
	v_add_f32_e32 v16, 1.0, v23
	v_rcp_f32_e32 v23, v16
	v_mul_f32_e32 v16, v19, v19
	v_fmamk_f32 v16, v16, 0xbdd2d3e8, v99
	v_mul_f32_e32 v16, v19, v16
	v_exp_f32_e32 v30, v16
	v_mov_b32_e32 v16, v17
	v_mov_b32_e32 v17, v18
	v_pk_mul_f32 v[16:17], v[16:17], v[22:23]
	v_add_f32_e32 v18, 1.0, v30
	v_rcp_f32_e32 v18, v18

.Lw3b161:
	v_cvt_pk_f16_f32 v16, v16, v17
	v_lshrrev_b32_e32 v23, 16, v16
	v_alignbit_b32 v22, v16, v29, 16
	v_fma_mixhi_f16 v23, v19, v18, 0
	s_waitcnt lgkmcnt(0)
	s_nop 0
	v_mfma_f32_16x16x32_f16 v[16:19], v[34:37], v[20:23], v[24:27]
	v_mul_f32_e32 v20, v12, v12
	v_fmamk_f32 v20, v20, 0xbdd2d3e8, v99
	v_mul_f32_e32 v20, v12, v20

.Lw3b162:
	v_exp_f32_e32 v20, v20
	v_mul_f32_e32 v21, v13, v13
	v_fmamk_f32 v21, v21, 0xbdd2d3e8, v99
	v_mul_f32_e32 v22, v14, v14
	v_mul_f32_e32 v21, v13, v21
	v_add_f32_e32 v20, 1.0, v20
	v_fmamk_f32 v22, v22, 0xbdd2d3e8, v99
	v_rcp_f32_e32 v20, v20
	v_exp_f32_e32 v21, v21
	v_mul_f32_e32 v22, v14, v22
	v_exp_f32_e32 v22, v22
	v_fma_mixlo_f16 v23, v12, v20, 0

.Lw3b163:
	v_add_f32_e32 v12, 1.0, v21
	v_rcp_f32_e32 v20, v12
	v_add_f32_e32 v12, 1.0, v22
	v_rcp_f32_e32 v21, v12
	v_mov_b32_e32 v12, v13
	v_mov_b32_e32 v13, v14
	v_mul_f32_e32 v14, v15, v15
	v_fmamk_f32 v14, v14, 0xbdd2d3e8, v99
	v_mul_f32_e32 v22, v8, v8
	v_mul_f32_e32 v14, v15, v14
	v_fmamk_f32 v22, v22, 0xbdd2d3e8, v99
	v_exp_f32_e32 v14, v14
	v_mul_f32_e32 v22, v8, v22

.Lw3b164:
	v_exp_f32_e32 v22, v22
	v_pk_mul_f32 v[12:13], v[12:13], v[20:21]
	v_add_f32_e32 v14, 1.0, v14
	v_rcp_f32_e32 v20, v14
	v_add_f32_e32 v14, 1.0, v22
	v_rcp_f32_e32 v21, v14
	v_pk_mov_b32 v[14:15], v[14:15], v[8:9] op_sel:[1,0]
	v_mul_f32_e32 v8, v9, v9
	v_fmamk_f32 v8, v8, 0xbdd2d3e8, v99
	v_pk_mul_f32 v[14:15], v[14:15], v[20:21]
	v_mul_f32_e32 v20, v10, v10

.Lw3b165:
	v_mul_f32_e32 v8, v9, v8
	v_fmamk_f32 v20, v20, 0xbdd2d3e8, v99
	v_exp_f32_e32 v8, v8
	v_mul_f32_e32 v20, v10, v20
	v_exp_f32_e32 v20, v20
	v_cvt_pk_f16_f32 v21, v14, v15
	v_add_f32_e32 v8, 1.0, v8
	v_rcp_f32_e32 v14, v8
	v_add_f32_e32 v8, 1.0, v20
	v_rcp_f32_e32 v15, v8
	v_mov_b32_e32 v8, v9
	v_mov_b32_e32 v9, v10
	v_cvt_pk_f16_f32 v13, v12, v13

.Lw3b166:
	v_pk_mul_f32 v[8:9], v[8:9], v[14:15]
	v_pack_b32_f16 v12, v23, v13
	v_cvt_pk_f16_f32 v8, v8, v9
	v_mul_f32_e32 v9, v11, v11
	v_fmamk_f32 v9, v9, 0xbdd2d3e8, v99
	v_mul_f32_e32 v9, v11, v9
	v_exp_f32_e32 v9, v9
	v_alignbit_b32 v13, v21, v13, 16
	v_alignbit_b32 v14, v8, v21, 16

.Lw3b167:
	ds_read_b128 v[20:23], v28 offset:34816
	v_lshrrev_b32_e32 v15, 16, v8
	v_add_f32_e32 v8, 1.0, v9
	v_rcp_f32_e32 v8, v8
	v_mul_f32_e32 v9, v4, v4
	v_fmamk_f32 v9, v9, 0xbdd2d3e8, v99
	v_mul_f32_e32 v9, v4, v9
	v_exp_f32_e32 v24, v9
	v_fma_mixhi_f16 v15, v11, v8, 0
	ds_read_b128 v[8:11], v28 offset:35840

.Lw3b168:
	s_waitcnt lgkmcnt(1)
	v_mfma_f32_16x16x32_f16 v[12:15], v[20:23], v[12:15], v[16:19]
	s_nop 2
	v_mul_f32_e32 v17, v5, v5
	v_fmamk_f32 v17, v17, 0xbdd2d3e8, v99
	v_mul_f32_e32 v18, v6, v6
	v_add_f32_e32 v16, 1.0, v24
	v_mul_f32_e32 v17, v5, v17
	v_fmamk_f32 v18, v18, 0xbdd2d3e8, v99
	v_rcp_f32_e32 v16, v16
	v_exp_f32_e32 v17, v17
	v_mul_f32_e32 v18, v6, v18

.Lw3b169:
	v_exp_f32_e32 v18, v18
	v_fma_mixlo_f16 v19, v4, v16, 0
	v_add_f32_e32 v4, 1.0, v17
	v_rcp_f32_e32 v16, v4
	v_add_f32_e32 v4, 1.0, v18
	v_rcp_f32_e32 v17, v4
	v_mov_b32_e32 v4, v5
	v_mov_b32_e32 v5, v6
	v_mul_f32_e32 v6, v7, v7
	v_fmamk_f32 v6, v6, 0xbdd2d3e8, v99
	v_mul_f32_e32 v18, v0, v0
	v_mul_f32_e32 v6, v7, v6
	v_fmamk_f32 v18, v18, 0xbdd2d3e8, v99

.Lw3b170:
	v_exp_f32_e32 v6, v6
	v_mul_f32_e32 v18, v0, v18
	v_exp_f32_e32 v18, v18
	v_pk_mul_f32 v[4:5], v[4:5], v[16:17]
	v_add_f32_e32 v6, 1.0, v6
	v_rcp_f32_e32 v16, v6
	v_add_f32_e32 v6, 1.0, v18
	v_rcp_f32_e32 v17, v6
	v_pk_mov_b32 v[6:7], v[6:7], v[0:1] op_sel:[1,0]
	v_mul_f32_e32 v0, v1, v1
	v_fmamk_f32 v0, v0, 0xbdd2d3e8, v99

.Lw3b171:
	v_pk_mul_f32 v[6:7], v[6:7], v[16:17]
	v_mul_f32_e32 v0, v1, v0
	v_cvt_pk_f16_f32 v16, v6, v7
	v_mul_f32_e32 v6, v2, v2
	v_fmamk_f32 v6, v6, 0xbdd2d3e8, v99
	v_exp_f32_e32 v0, v0
	v_mul_f32_e32 v6, v2, v6
	v_exp_f32_e32 v7, v6
	v_cvt_pk_f16_f32 v5, v4, v5
	v_add_f32_e32 v0, 1.0, v0
	v_rcp_f32_e32 v6, v0

.Lw3b172:
	v_add_f32_e32 v0, 1.0, v7
	v_rcp_f32_e32 v7, v0
	v_mul_f32_e32 v0, v3, v3
	v_fmamk_f32 v0, v0, 0xbdd2d3e8, v99
	v_mul_f32_e32 v0, v3, v0
	v_exp_f32_e32 v17, v0
	v_mov_b32_e32 v0, v1
	v_mov_b32_e32 v1, v2
	v_pk_mul_f32 v[0:1], v[0:1], v[6:7]
	v_add_f32_e32 v2, 1.0, v17
	v_rcp_f32_e32 v2, v2
	v_cvt_pk_f16_f32 v0, v0, v1

.Lw3b173:
	v_lshrrev_b32_e32 v7, 16, v0
	v_pack_b32_f16 v4, v19, v5
	v_alignbit_b32 v5, v16, v5, 16
	v_alignbit_b32 v6, v0, v16, 16
	v_fma_mixhi_f16 v7, v3, v2, 0
	s_waitcnt lgkmcnt(0)
	s_nop 0
	v_mfma_f32_16x16x32_f16 v[0:3], v[8:11], v[4:7], v[12:15]
	s_and_saveexec_b64 s[14:15], s[4:5]
	s_xor_b64 s[14:15], exec, s[14:15]

.Lw3b174:
	s_cbranch_execz .LBB3_9
	s_load_dwordx2 s[20:21], s[16:17], 0x0
	s_nop 3
	v_or_b32_e32 v2, s10, v80
	v_ashrrev_i32_e32 v3, 31, v2
	v_lshl_add_u64 v[2:3], v[2:3], 3, s[6:7]
	s_waitcnt lgkmcnt(0)
	v_pk_add_f32 v[0:1], v[0:1], s[20:21]
	global_store_dwordx2 v[2:3], v[0:1], off
	s_branch .LBB3_9

	.amdhsa_kernel _Z10k_layer_a2ILi1ELi13EEvPKDF16_PKiS3_PK15HIP_vector_typeIjLj4EES7_PKfS9_S9_S9_S9_S9_PDF16_Pf
		.amdhsa_group_segment_fixed_size 162052
		.amdhsa_private_segment_fixed_size 0
		.amdhsa_kernarg_size 360
		.amdhsa_user_sgpr_count 2
		.amdhsa_user_sgpr_dispatch_ptr 0
		.amdhsa_user_sgpr_queue_ptr 0
		.amdhsa_user_sgpr_kernarg_segment_ptr 1
		.amdhsa_user_sgpr_dispatch_id 0
		.amdhsa_user_sgpr_kernarg_preload_length 0
		.amdhsa_user_sgpr_kernarg_preload_offset 0
		.amdhsa_user_sgpr_private_segment_size 0
		.amdhsa_uses_dynamic_stack 0
		.amdhsa_enable_private_segment 0
		.amdhsa_system_sgpr_workgroup_id_x 1
		.amdhsa_system_sgpr_workgroup_id_y 0
		.amdhsa_system_sgpr_workgroup_id_z 0
		.amdhsa_system_sgpr_workgroup_info 0
		.amdhsa_system_vgpr_workitem_id 0
		.amdhsa_next_free_vgpr 125
		.amdhsa_next_free_sgpr 96
		.amdhsa_accum_offset 128
		.amdhsa_reserve_vcc 1
		.amdhsa_float_round_mode_32 0
		.amdhsa_float_round_mode_16_64 0
		.amdhsa_float_denorm_mode_32 3
		.amdhsa_float_denorm_mode_16_64 3
		.amdhsa_dx10_clamp 1
		.amdhsa_ieee_mode 1
		.amdhsa_fp16_overflow 0
		.amdhsa_tg_split 0
		.amdhsa_exception_fp_ieee_invalid_op 0
		.amdhsa_exception_fp_denorm_src 0
		.amdhsa_exception_fp_ieee_div_zero 0
		.amdhsa_exception_fp_ieee_overflow 0
		.amdhsa_exception_fp_ieee_underflow 0
		.amdhsa_exception_fp_ieee_inexact 0
		.amdhsa_exception_int_div_zero 0
	.end_amdhsa_kernel
	.text
.Lfunc_end3:
	.size	_Z10k_layer_a2ILi1ELi13EEvPKDF16_PKiS3_PK15HIP_vector_typeIjLj4EES7_PKfS9_S9_S9_S9_S9_PDF16_Pf, .Lfunc_end3-_Z10k_layer_a2ILi1ELi13EEvPKDF16_PKiS3_PK15HIP_vector_typeIjLj4EES7_PKfS9_S9_S9_S9_S9_PDF16_Pf
	.set _Z10k_layer_a2ILi1ELi13EEvPKDF16_PKiS3_PK15HIP_vector_typeIjLj4EES7_PKfS9_S9_S9_S9_S9_PDF16_Pf.num_vgpr, 125
	.set _Z10k_layer_a2ILi1ELi13EEvPKDF16_PKiS3_PK15HIP_vector_typeIjLj4EES7_PKfS9_S9_S9_S9_S9_PDF16_Pf.num_agpr, 0
	.set _Z10k_layer_a2ILi1ELi13EEvPKDF16_PKiS3_PK15HIP_vector_typeIjLj4EES7_PKfS9_S9_S9_S9_S9_PDF16_Pf.numbered_sgpr, 32
	.set _Z10k_layer_a2ILi1ELi13EEvPKDF16_PKiS3_PK15HIP_vector_typeIjLj4EES7_PKfS9_S9_S9_S9_S9_PDF16_Pf.num_named_barrier, 0
	.set _Z10k_layer_a2ILi1ELi13EEvPKDF16_PKiS3_PK15HIP_vector_typeIjLj4EES7_PKfS9_S9_S9_S9_S9_PDF16_Pf.private_seg_size, 0
	.set _Z10k_layer_a2ILi1ELi13EEvPKDF16_PKiS3_PK15HIP_vector_typeIjLj4EES7_PKfS9_S9_S9_S9_S9_PDF16_Pf.uses_vcc, 1
	.set _Z10k_layer_a2ILi1ELi13EEvPKDF16_PKiS3_PK15HIP_vector_typeIjLj4EES7_PKfS9_S9_S9_S9_S9_PDF16_Pf.uses_flat_scratch, 0
	.set _Z10k_layer_a2ILi1ELi13EEvPKDF16_PKiS3_PK15HIP_vector_typeIjLj4EES7_PKfS9_S9_S9_S9_S9_PDF16_Pf.has_dyn_sized_stack, 0
	.set _Z10k_layer_a2ILi1ELi13EEvPKDF16_PKiS3_PK15HIP_vector_typeIjLj4EES7_PKfS9_S9_S9_S9_S9_PDF16_Pf.has_recursion, 0
	.set _Z10k_layer_a2ILi1ELi13EEvPKDF16_PKiS3_PK15HIP_vector_typeIjLj4EES7_PKfS9_S9_S9_S9_S9_PDF16_Pf.has_indirect_call, 0

amdhsa.kernels:
  - .agpr_count:     0
    .args:
      - .actual_access:  read_only
        .address_space:  global
        .offset:         0
        .size:           8
        .value_kind:     global_buffer
      - .actual_access:  read_only
        .address_space:  global
        .offset:         8
        .size:           8
        .value_kind:     global_buffer
      - .actual_access:  write_only
        .address_space:  global
        .offset:         16
        .size:           8
        .value_kind:     global_buffer
      - .actual_access:  write_only
        .address_space:  global
        .offset:         24
        .size:           8
        .value_kind:     global_buffer
      - .actual_access:  write_only
        .address_space:  global
        .offset:         32
        .size:           8
        .value_kind:     global_buffer
      - .actual_access:  read_only
        .address_space:  global
        .offset:         40
        .size:           8
        .value_kind:     global_buffer
      - .actual_access:  read_only
        .address_space:  global
        .offset:         48
        .size:           8
        .value_kind:     global_buffer
      - .actual_access:  read_only
        .address_space:  global
        .offset:         56
        .size:           8
        .value_kind:     global_buffer
      - .actual_access:  write_only
        .address_space:  global
        .offset:         64
        .size:           8
        .value_kind:     global_buffer
      - .actual_access:  write_only
        .address_space:  global
        .offset:         72
        .size:           8
        .value_kind:     global_buffer
      - .actual_access:  read_only
        .address_space:  global
        .offset:         80
        .size:           8
        .value_kind:     global_buffer
      - .address_space:  global
        .offset:         88
        .size:           8
        .value_kind:     global_buffer
      - .actual_access:  write_only
        .address_space:  global
        .offset:         96
        .size:           8
        .value_kind:     global_buffer
    .group_segment_fixed_size: 34400
    .kernarg_segment_align: 8
    .kernarg_segment_size: 104
    .language:       OpenCL C
    .language_version:
      - 2
      - 0
    .max_flat_workgroup_size: 1024
    .name:           _Z7k_frontPKiS0_PiS1_PjPKfS4_S4_P15HIP_vector_typeIjLj4EES7_PKS5_IfLj4EES7_S7_
    .private_segment_fixed_size: 0
    .sgpr_count:     42
    .sgpr_spill_count: 0
    .symbol:         _Z7k_frontPKiS0_PiS1_PjPKfS4_S4_P15HIP_vector_typeIjLj4EES7_PKS5_IfLj4EES7_S7_.kd
    .uniform_work_group_size: 1
    .uses_dynamic_stack: false
    .vgpr_count:     41
    .vgpr_spill_count: 0
    .wavefront_size: 64
  - .agpr_count:     0
    .args:
      - .actual_access:  read_only
        .address_space:  global
        .offset:         0
        .size:           8
        .value_kind:     global_buffer
      - .actual_access:  read_only
        .address_space:  global
        .offset:         8
        .size:           8
        .value_kind:     global_buffer
      - .actual_access:  read_only
        .address_space:  global
        .offset:         16
        .size:           8
        .value_kind:     global_buffer
      - .actual_access:  write_only
        .address_space:  global
        .offset:         24
        .size:           8
        .value_kind:     global_buffer
      - .address_space:  global
        .offset:         32
        .size:           8
        .value_kind:     global_buffer
      - .actual_access:  read_only
        .address_space:  global
        .offset:         40
        .size:           8
        .value_kind:     global_buffer
      - .address_space:  global
        .offset:         48
        .size:           8
        .value_kind:     global_buffer
    .group_segment_fixed_size: 72608
    .kernarg_segment_align: 8
    .kernarg_segment_size: 56
    .language:       OpenCL C
    .language_version:
      - 2
      - 0
    .max_flat_workgroup_size: 1024
    .name:           _Z8k_bucketPKiS0_PKjPiS3_PK15HIP_vector_typeIfLj4EEPS4_IjLj4EE
    .private_segment_fixed_size: 0
    .sgpr_count:     72
    .sgpr_spill_count: 0
    .symbol:         _Z8k_bucketPKiS0_PKjPiS3_PK15HIP_vector_typeIfLj4EEPS4_IjLj4EE.kd
    .uniform_work_group_size: 1
    .uses_dynamic_stack: false
    .vgpr_count:     32
    .vgpr_spill_count: 0
    .wavefront_size: 64
  - .agpr_count:     0
    .args:
      - .actual_access:  read_only
        .address_space:  global
        .offset:         0
        .size:           8
        .value_kind:     global_buffer
      - .actual_access:  read_only
        .address_space:  global
        .offset:         8
        .size:           8
        .value_kind:     global_buffer
      - .actual_access:  read_only
        .address_space:  global
        .offset:         16
        .size:           8
        .value_kind:     global_buffer
      - .actual_access:  read_only
        .address_space:  global
        .offset:         24
        .size:           8
        .value_kind:     global_buffer
      - .actual_access:  read_only
        .address_space:  global
        .offset:         32
        .size:           8
        .value_kind:     global_buffer
      - .actual_access:  read_only
        .address_space:  global
        .offset:         40
        .size:           8
        .value_kind:     global_buffer
      - .actual_access:  read_only
        .address_space:  global
        .offset:         48
        .size:           8
        .value_kind:     global_buffer
      - .actual_access:  read_only
        .address_space:  global
        .offset:         56
        .size:           8
        .value_kind:     global_buffer
      - .actual_access:  read_only
        .address_space:  global
        .offset:         64
        .size:           8
        .value_kind:     global_buffer
      - .actual_access:  read_only
        .address_space:  global
        .offset:         72
        .size:           8
        .value_kind:     global_buffer
      - .actual_access:  read_only
        .address_space:  global
        .offset:         80
        .size:           8
        .value_kind:     global_buffer
      - .actual_access:  write_only
        .address_space:  global
        .offset:         88
        .size:           8
        .value_kind:     global_buffer
      - .actual_access:  read_only
        .address_space:  global
        .offset:         96
        .size:           8
        .value_kind:     global_buffer
      - .offset:         104
        .size:           4
        .value_kind:     hidden_block_count_x
      - .offset:         108
        .size:           4
        .value_kind:     hidden_block_count_y
      - .offset:         112
        .size:           4
        .value_kind:     hidden_block_count_z
      - .offset:         116
        .size:           2
        .value_kind:     hidden_group_size_x
      - .offset:         118
        .size:           2
        .value_kind:     hidden_group_size_y
      - .offset:         120
        .size:           2
        .value_kind:     hidden_group_size_z
      - .offset:         122
        .size:           2
        .value_kind:     hidden_remainder_x
      - .offset:         124
        .size:           2
        .value_kind:     hidden_remainder_y
      - .offset:         126
        .size:           2
        .value_kind:     hidden_remainder_z
      - .offset:         144
        .size:           8
        .value_kind:     hidden_global_offset_x
      - .offset:         152
        .size:           8
        .value_kind:     hidden_global_offset_y
      - .offset:         160
        .size:           8
        .value_kind:     hidden_global_offset_z
      - .offset:         168
        .size:           2
        .value_kind:     hidden_grid_dims
    .group_segment_fixed_size: 125188
    .kernarg_segment_align: 8
    .kernarg_segment_size: 360
    .language:       OpenCL C
    .language_version:
      - 2
      - 0
    .max_flat_workgroup_size: 832
    .name:           _Z10k_layer_a2ILi0ELi13EEvPKDF16_PKiS3_PK15HIP_vector_typeIjLj4EES7_PKfS9_S9_S9_S9_S9_PDF16_Pf
    .private_segment_fixed_size: 0
    .sgpr_count:     48
    .sgpr_spill_count: 0
    .symbol:         _Z10k_layer_a2ILi0ELi13EEvPKDF16_PKiS3_PK15HIP_vector_typeIjLj4EES7_PKfS9_S9_S9_S9_S9_PDF16_Pf.kd
    .uniform_work_group_size: 1
    .uses_dynamic_stack: false
    .vgpr_count:     125
    .vgpr_spill_count: 0
    .wavefront_size: 64
  - .agpr_count:     0
    .args:
      - .actual_access:  read_only
        .address_space:  global
        .offset:         0
        .size:           8
        .value_kind:     global_buffer
      - .actual_access:  read_only
        .address_space:  global
        .offset:         8
        .size:           8
        .value_kind:     global_buffer
      - .actual_access:  read_only
        .address_space:  global
        .offset:         16
        .size:           8
        .value_kind:     global_buffer
      - .actual_access:  read_only
        .address_space:  global
        .offset:         24
        .size:           8
        .value_kind:     global_buffer
      - .actual_access:  read_only
        .address_space:  global
        .offset:         32
        .size:           8
        .value_kind:     global_buffer
      - .actual_access:  read_only
        .address_space:  global
        .offset:         40
        .size:           8
        .value_kind:     global_buffer
      - .actual_access:  read_only
        .address_space:  global
        .offset:         48
        .size:           8
        .value_kind:     global_buffer
      - .actual_access:  read_only
        .address_space:  global
        .offset:         56
        .size:           8
        .value_kind:     global_buffer
      - .actual_access:  read_only
        .address_space:  global
        .offset:         64
        .size:           8
        .value_kind:     global_buffer
      - .actual_access:  read_only
        .address_space:  global
        .offset:         72
        .size:           8
        .value_kind:     global_buffer
      - .actual_access:  read_only
        .address_space:  global
        .offset:         80
        .size:           8
        .value_kind:     global_buffer
      - .actual_access:  read_only
        .address_space:  global
        .offset:         88
        .size:           8
        .value_kind:     global_buffer
      - .actual_access:  write_only
        .address_space:  global
        .offset:         96
        .size:           8
        .value_kind:     global_buffer
      - .offset:         104
        .size:           4
        .value_kind:     hidden_block_count_x
      - .offset:         108
        .size:           4
        .value_kind:     hidden_block_count_y
      - .offset:         112
        .size:           4
        .value_kind:     hidden_block_count_z
      - .offset:         116
        .size:           2
        .value_kind:     hidden_group_size_x
      - .offset:         118
        .size:           2
        .value_kind:     hidden_group_size_y
      - .offset:         120
        .size:           2
        .value_kind:     hidden_group_size_z
      - .offset:         122
        .size:           2
        .value_kind:     hidden_remainder_x
      - .offset:         124
        .size:           2
        .value_kind:     hidden_remainder_y
      - .offset:         126
        .size:           2
        .value_kind:     hidden_remainder_z
      - .offset:         144
        .size:           8
        .value_kind:     hidden_global_offset_x
      - .offset:         152
        .size:           8
        .value_kind:     hidden_global_offset_y
      - .offset:         160
        .size:           8
        .value_kind:     hidden_global_offset_z
      - .offset:         168
        .size:           2
        .value_kind:     hidden_grid_dims
    .group_segment_fixed_size: 162052
    .kernarg_segment_align: 8
    .kernarg_segment_size: 360
    .language:       OpenCL C
    .language_version:
      - 2
      - 0
    .max_flat_workgroup_size: 832
    .name:           _Z10k_layer_a2ILi1ELi13EEvPKDF16_PKiS3_PK15HIP_vector_typeIjLj4EES7_PKfS9_S9_S9_S9_S9_PDF16_Pf
    .private_segment_fixed_size: 0
    .sgpr_count:     48
    .sgpr_spill_count: 0
    .symbol:         _Z10k_layer_a2ILi1ELi13EEvPKDF16_PKiS3_PK15HIP_vector_typeIjLj4EES7_PKfS9_S9_S9_S9_S9_PDF16_Pf.kd
    .uniform_work_group_size: 1
    .uses_dynamic_stack: false
    .vgpr_count:     125
    .vgpr_spill_count: 0
    .wavefront_size: 64
